# GEMM K-loops: loop-edge SALU block (pointer bumps, exit test) moved in front of the loop-back barrier (doc 7.11 back-edge rotation, partial)
# baseline (speedup 1.0000x reference)
; #define G8_STAGE(bufoff, gbase, voff) do { _Pragma("unroll") for (int _i = 0; _i < 2; ++_i) \
;         __builtin_amdgcn_global_load_lds((const unsigned*)((const char*)(gbase) + (voff)[_i]), (LAS unsigned*)(lds + (bufoff) + ldsw + _i * 8192), 16, 0, 0); } while (0)
; #define G8_STAGE_A(bufoff, gbase, h_, nx_) do { if constexpr (Sched::GATHER) { unsigned vo_[2]; _Pragma("unroll") for (int q_ = 0; q_ < 2; ++q_) vo_[q_] = (nx_) ? gnxt[h_][q_] : goff[h_][q_]; G8_STAGE(bufoff, gbase, vo_); } \
;         else { G8_STAGE(bufoff, (gbase) + ((h_) ? hstepA : (size_t)0), voffA); } } while (0)
; #define G8_XLDA(b, h) do { if constexpr (Epi::FP8) { G8_LD8(A8, G8_SA(b, h) + aoff, 4); } else { G8_LDA(At, b, h); } } while (0)
; #define G8_XLDB0(b, h) do { if constexpr (Epi::FP8) { G8_LD8(B08, G8_SB(b, h) + boff, 2); } else { G8_LDB(B0, b, h); } } while (0)
; #define G8_XLDB1(b, h) do { if constexpr (Epi::FP8) { G8_LD8(B18, G8_SB(b, h) + boff, 2); } else { G8_LDB(B1, b, h); } } while (0)
; #define G8_MM0(ai, bj) do { if constexpr (Epi::FP8) { G8_MMA8(ai, bj, A8, B08); } else { G8_MMA(ai, bj, At, B0); } } while (0)
; #define G8_MM1(ai, bj) do { if constexpr (Epi::FP8) { G8_MMA8(ai, bj, A8, B18); } else { G8_MMA(ai, bj, At, B1); } } while (0)
; template <int lda, int ldb, class Epi, class Sched>
; __device__ __forceinline__ void gemm_phase(LAS unsigned char* lds, int wid, int lane, const char* baseA, const char* baseB, const Sched& S, const Epi& E) {
;     ...
;         for (int t = 0; t < nt; t += 2) {
;             const bool last = (t == nt - 2);
;             const char* a1 = cA + (size_t)(t + 1) * kstep;
;             const char* a2 = last ? nA : cA + (size_t)(t + 2) * kstep; const char* b2 = last ? nB : cB + (size_t)(t + 2) * kstep;
;             const char* a3 = a2 + kstep; const char* b3 = b2 + kstep;
;     ...
;             G8_XLDB0(0, 0); if constexpr (!Epi::HALFN) { G8_XLDB1(0, 1); } G8_SCHED; G8_XLDA(0, 0); G8_STAGE_A(G8_SA(1, 1), a1, 1, false);
;             G8_WAIT_VK; G8_WAIT_L(0); G8_BAR; G8_MM0(0, 0); if constexpr (!Epi::HALFN) { G8_MM1(0, 1); } G8_BAR; G8_SCHED;
;             G8_XLDA(0, 1); G8_STAGE(G8_SB(0, 0), b2, voffB); if constexpr (!Epi::HALFN) { G8_STAGE(G8_SB(0, 1), b2 + hstepB, voffB); } G8_STAGE_A(G8_SA(0, 0), a2, 0, last);
;             G8_WAIT_VK; G8_WAIT_L(0); G8_BAR; G8_MM0(1, 0); if constexpr (!Epi::HALFN) { G8_MM1(1, 1); } G8_BAR; G8_SCHED;
.LBB0_367:
	v_add_u32_e32 v1, 0x10000, v148
	ds_read_b128 v[144:147], v1
	ds_read_b128 v[150:153], v1 offset:1024
	ds_read_b128 v[154:157], v1 offset:2048
	ds_read_b128 v[158:161], v1 offset:3072
	v_add_u32_e32 v1, 0x14000, v148
	ds_read_b128 v[162:165], v1
	ds_read_b128 v[166:169], v1 offset:1024
	ds_read_b128 v[170:173], v1 offset:2048
	ds_read_b128 v[174:177], v1 offset:3072
	s_add_i32 s78, s44, 2
	s_add_u32 s45, s42, 0xfffc0080
	s_addc_u32 s46, s43, -1
	s_cmp_eq_u32 s56, s44
	s_cselect_b32 s44, s55, s57
	s_cselect_b32 s47, s48, s46
	s_cselect_b32 s46, s49, s45
	s_cselect_b32 s45, s54, s77
	v_lshl_add_u64 v[218:219], s[42:43], 0, v[140:141]
	s_add_i32 m0, s27, 0xc000
	ds_read_b128 v[178:181], v30
	ds_read_b128 v[184:187], v30 offset:1024
	ds_read_b128 v[188:191], v30 offset:2048
	ds_read_b128 v[192:195], v30 offset:3072
	ds_read_b128 v[196:199], v30 offset:4096
	ds_read_b128 v[206:209], v30 offset:5120
	ds_read_b128 v[210:213], v30 offset:6144
	ds_read_b128 v[214:217], v30 offset:7168
	global_load_lds_dwordx4 v[218:219], off
	v_lshl_add_u64 v[218:219], s[42:43], 0, v[142:143]
	s_add_i32 m0, s27, 0xe000
	s_nop 0
	global_load_lds_dwordx4 v[218:219], off
	s_waitcnt vmcnt(8)
	s_waitcnt lgkmcnt(0)
	s_barrier
	s_setprio 1
	s_waitcnt lgkmcnt(0)
	v_mfma_f32_16x16x32_bf16 v[128:131], v[144:147], v[178:181], v[128:131]
	v_mfma_f32_16x16x32_bf16 v[124:127], v[154:157], v[178:181], v[124:127]
	v_mfma_f32_16x16x32_bf16 v[112:115], v[144:147], v[188:191], v[112:115]
	v_mfma_f32_16x16x32_bf16 v[108:111], v[154:157], v[188:191], v[108:111]
	v_mfma_f32_16x16x32_bf16 v[96:99], v[144:147], v[196:199], v[96:99]
	v_mfma_f32_16x16x32_bf16 v[92:95], v[154:157], v[196:199], v[92:95]
	v_mfma_f32_16x16x32_bf16 v[80:83], v[144:147], v[210:213], v[80:83]
	v_mfma_f32_16x16x32_bf16 v[76:79], v[154:157], v[210:213], v[76:79]
	v_mfma_f32_16x16x32_bf16 v[128:131], v[150:153], v[184:187], v[128:131]
	v_mfma_f32_16x16x32_bf16 v[124:127], v[158:161], v[184:187], v[124:127]
	v_mfma_f32_16x16x32_bf16 v[112:115], v[150:153], v[192:195], v[112:115]
	v_mfma_f32_16x16x32_bf16 v[108:111], v[158:161], v[192:195], v[108:111]
	v_mfma_f32_16x16x32_bf16 v[96:99], v[150:153], v[206:209], v[96:99]
	v_mfma_f32_16x16x32_bf16 v[92:95], v[158:161], v[206:209], v[92:95]
	v_mfma_f32_16x16x32_bf16 v[80:83], v[150:153], v[214:217], v[80:83]
	v_mfma_f32_16x16x32_bf16 v[76:79], v[158:161], v[214:217], v[76:79]
	s_setprio 0
	s_setprio 1
	v_mfma_f32_16x16x32_bf16 v[120:123], v[162:165], v[178:181], v[120:123]
	v_mfma_f32_16x16x32_bf16 v[116:119], v[170:173], v[178:181], v[116:119]
	v_mfma_f32_16x16x32_bf16 v[104:107], v[162:165], v[188:191], v[104:107]
	v_mfma_f32_16x16x32_bf16 v[100:103], v[170:173], v[188:191], v[100:103]
	v_mfma_f32_16x16x32_bf16 v[88:91], v[162:165], v[196:199], v[88:91]
	v_mfma_f32_16x16x32_bf16 v[84:87], v[170:173], v[196:199], v[84:87]
	v_mfma_f32_16x16x32_bf16 v[72:75], v[162:165], v[210:213], v[72:75]
	v_mfma_f32_16x16x32_bf16 v[68:71], v[170:173], v[210:213], v[68:71]
	v_mfma_f32_16x16x32_bf16 v[120:123], v[166:169], v[184:187], v[120:123]
	v_mfma_f32_16x16x32_bf16 v[116:119], v[174:177], v[184:187], v[116:119]
	v_mfma_f32_16x16x32_bf16 v[104:107], v[166:169], v[192:195], v[104:107]
	v_mfma_f32_16x16x32_bf16 v[100:103], v[174:177], v[192:195], v[100:103]
	v_mfma_f32_16x16x32_bf16 v[88:91], v[166:169], v[206:209], v[88:91]
	v_mfma_f32_16x16x32_bf16 v[84:87], v[174:177], v[206:209], v[84:87]
	v_mfma_f32_16x16x32_bf16 v[72:75], v[166:169], v[214:217], v[72:75]
	v_mfma_f32_16x16x32_bf16 v[68:71], v[174:177], v[214:217], v[68:71]
	s_setprio 0
	s_barrier
	s_mov_b32 m0, s21
	v_lshl_add_u64 v[218:219], s[44:45], 0, v[134:135]
	s_add_u32 s80, s44, 0x40000
	ds_read_b128 v[178:181], v30 offset:16384
	ds_read_b128 v[184:187], v30 offset:17408
	ds_read_b128 v[188:191], v30 offset:18432
	ds_read_b128 v[192:195], v30 offset:19456
	ds_read_b128 v[196:199], v30 offset:20480
	ds_read_b128 v[206:209], v30 offset:21504
	ds_read_b128 v[210:213], v30 offset:22528
	ds_read_b128 v[214:217], v30 offset:23552
	global_load_lds_dwordx4 v[218:219], off
	v_lshl_add_u64 v[220:221], s[44:45], 0, v[138:139]
	s_mov_b32 m0, s28
	s_addc_u32 s81, s45, 0
	global_load_lds_dwordx4 v[220:221], off
	v_lshl_add_u64 v[222:223], s[80:81], 0, v[134:135]
	s_mov_b32 m0, s29
	v_lshl_add_u64 v[224:225], s[46:47], 0, v[136:137]
	global_load_lds_dwordx4 v[222:223], off
	v_lshl_add_u64 v[222:223], s[80:81], 0, v[138:139]
	s_mov_b32 m0, s31
	s_nop 0
	global_load_lds_dwordx4 v[222:223], off
	v_lshl_add_u64 v[222:223], s[46:47], 0, v[132:133]
	s_mov_b32 m0, s27
	s_nop 0
	global_load_lds_dwordx4 v[222:223], off
	s_mov_b32 m0, s58
	s_nop 0
	global_load_lds_dwordx4 v[224:225], off
	s_waitcnt vmcnt(8)
	s_waitcnt lgkmcnt(0)
	s_barrier
; #define G8_STAGE_A(bufoff, gbase, h_, nx_) do { if constexpr (Sched::GATHER) { unsigned vo_[2]; _Pragma("unroll") for (int q_ = 0; q_ < 2; ++q_) vo_[q_] = (nx_) ? gnxt[h_][q_] : goff[h_][q_]; G8_STAGE(bufoff, gbase, vo_); } \
;         else { G8_STAGE(bufoff, (gbase) + ((h_) ? hstepA : (size_t)0), voffA); } } while (0)
; #define G8_XLDA(b, h) do { if constexpr (Epi::FP8) { G8_LD8(A8, G8_SA(b, h) + aoff, 4); } else { G8_LDA(At, b, h); } } while (0)
; #define G8_XLDB0(b, h) do { if constexpr (Epi::FP8) { G8_LD8(B08, G8_SB(b, h) + boff, 2); } else { G8_LDB(B0, b, h); } } while (0)
; #define G8_XLDB1(b, h) do { if constexpr (Epi::FP8) { G8_LD8(B18, G8_SB(b, h) + boff, 2); } else { G8_LDB(B1, b, h); } } while (0)
; #define G8_MM0(ai, bj) do { if constexpr (Epi::FP8) { G8_MMA8(ai, bj, A8, B08); } else { G8_MMA(ai, bj, At, B0); } } while (0)
; #define G8_MM1(ai, bj) do { if constexpr (Epi::FP8) { G8_MMA8(ai, bj, A8, B18); } else { G8_MMA(ai, bj, At, B1); } } while (0)
; #define G8_WAIT_L(n) asm volatile("s_waitcnt lgkmcnt(" #n ")" ::: "memory")
; #define G8_BAR __builtin_amdgcn_s_barrier()
; #define G8_SCHED __builtin_amdgcn_sched_barrier(0)
; #define G8_WAIT_VK do { if constexpr (Epi::HALFN) { G8_WAIT_V(6); } else { G8_WAIT_V(8); } } while (0)
; template <int lda, int ldb, class Epi, class Sched>
; __device__ __forceinline__ void gemm_phase(LAS unsigned char* lds, int wid, int lane, const char* baseA, const char* baseB, const Sched& S, const Epi& E) {
;     ...
;             G8_WAIT_VK; G8_WAIT_L(0); G8_BAR; G8_MM0(1, 0); if constexpr (!Epi::HALFN) { G8_MM1(1, 1); } G8_BAR; G8_SCHED;
;             G8_XLDB0(1, 0); if constexpr (!Epi::HALFN) { G8_XLDB1(1, 1); } G8_SCHED; G8_XLDA(1, 0); G8_STAGE_A(G8_SA(0, 1), a2, 1, last);
;             G8_WAIT_VK; G8_WAIT_L(0); G8_BAR; G8_MM0(0, 0); if constexpr (!Epi::HALFN) { G8_MM1(0, 1); } G8_BAR; G8_SCHED;
	s_setprio 1
	s_waitcnt lgkmcnt(0)
	v_mfma_f32_16x16x32_bf16 v[64:67], v[144:147], v[178:181], v[64:67]
	v_mfma_f32_16x16x32_bf16 v[60:63], v[154:157], v[178:181], v[60:63]
	v_mfma_f32_16x16x32_bf16 v[48:51], v[144:147], v[188:191], v[48:51]
	v_mfma_f32_16x16x32_bf16 v[44:47], v[154:157], v[188:191], v[44:47]
	v_mfma_f32_16x16x32_bf16 v[32:35], v[144:147], v[196:199], v[32:35]
	v_mfma_f32_16x16x32_bf16 v[26:29], v[154:157], v[196:199], v[26:29]
	v_mfma_f32_16x16x32_bf16 v[14:17], v[144:147], v[210:213], v[14:17]
	v_mfma_f32_16x16x32_bf16 v[10:13], v[154:157], v[210:213], v[10:13]
	v_mfma_f32_16x16x32_bf16 v[64:67], v[150:153], v[184:187], v[64:67]
	v_mfma_f32_16x16x32_bf16 v[60:63], v[158:161], v[184:187], v[60:63]
	v_mfma_f32_16x16x32_bf16 v[48:51], v[150:153], v[192:195], v[48:51]
	v_mfma_f32_16x16x32_bf16 v[44:47], v[158:161], v[192:195], v[44:47]
	v_mfma_f32_16x16x32_bf16 v[32:35], v[150:153], v[206:209], v[32:35]
	v_mfma_f32_16x16x32_bf16 v[26:29], v[158:161], v[206:209], v[26:29]
	v_mfma_f32_16x16x32_bf16 v[14:17], v[150:153], v[214:217], v[14:17]
	v_mfma_f32_16x16x32_bf16 v[10:13], v[158:161], v[214:217], v[10:13]
	s_setprio 0
	s_setprio 1
	v_mfma_f32_16x16x32_bf16 v[56:59], v[162:165], v[178:181], v[56:59]
	v_mfma_f32_16x16x32_bf16 v[52:55], v[170:173], v[178:181], v[52:55]
	v_mfma_f32_16x16x32_bf16 v[40:43], v[162:165], v[188:191], v[40:43]
	v_mfma_f32_16x16x32_bf16 v[36:39], v[170:173], v[188:191], v[36:39]
	v_mfma_f32_16x16x32_bf16 v[22:25], v[162:165], v[196:199], v[22:25]
	v_mfma_f32_16x16x32_bf16 v[18:21], v[170:173], v[196:199], v[18:21]
	v_mfma_f32_16x16x32_bf16 v[6:9], v[162:165], v[210:213], v[6:9]
	v_mfma_f32_16x16x32_bf16 v[2:5], v[170:173], v[210:213], v[2:5]
	v_mfma_f32_16x16x32_bf16 v[56:59], v[166:169], v[184:187], v[56:59]
	v_mfma_f32_16x16x32_bf16 v[52:55], v[174:177], v[184:187], v[52:55]
	v_mfma_f32_16x16x32_bf16 v[40:43], v[166:169], v[192:195], v[40:43]
	v_mfma_f32_16x16x32_bf16 v[36:39], v[174:177], v[192:195], v[36:39]
	v_mfma_f32_16x16x32_bf16 v[22:25], v[166:169], v[206:209], v[22:25]
	v_mfma_f32_16x16x32_bf16 v[18:21], v[174:177], v[206:209], v[18:21]
	v_mfma_f32_16x16x32_bf16 v[6:9], v[166:169], v[214:217], v[6:9]
	v_mfma_f32_16x16x32_bf16 v[2:5], v[174:177], v[214:217], v[2:5]
	s_setprio 0
	s_barrier
	v_add_u32_e32 v1, 0x18000, v148
	ds_read_b128 v[144:147], v1
	ds_read_b128 v[150:153], v1 offset:1024
	ds_read_b128 v[154:157], v1 offset:2048
	ds_read_b128 v[158:161], v1 offset:3072
	v_add_u32_e32 v1, 0x1c000, v148
	ds_read_b128 v[162:165], v1
	ds_read_b128 v[166:169], v1 offset:1024
	ds_read_b128 v[170:173], v1 offset:2048
	ds_read_b128 v[174:177], v1 offset:3072
	s_add_u32 s46, s46, 0x40000
	s_addc_u32 s47, s47, 0
	s_mov_b32 m0, s59
	v_lshl_add_u64 v[226:227], s[46:47], 0, v[132:133]
	ds_read_b128 v[178:181], v30 offset:32768
	ds_read_b128 v[184:187], v30 offset:33792
	ds_read_b128 v[188:191], v30 offset:34816
	ds_read_b128 v[192:195], v30 offset:35840
	ds_read_b128 v[196:199], v30 offset:36864
	ds_read_b128 v[206:209], v30 offset:37888
	ds_read_b128 v[210:213], v30 offset:38912
	ds_read_b128 v[214:217], v30 offset:39936
	global_load_lds_dwordx4 v[226:227], off
	v_lshl_add_u64 v[226:227], s[46:47], 0, v[136:137]
	s_mov_b32 m0, s60
	s_nop 0
	global_load_lds_dwordx4 v[226:227], off
	s_waitcnt vmcnt(8)
	s_waitcnt lgkmcnt(0)
	s_barrier
	s_setprio 1
	s_waitcnt lgkmcnt(0)
	v_mfma_f32_16x16x32_bf16 v[128:131], v[144:147], v[178:181], v[128:131]
	v_mfma_f32_16x16x32_bf16 v[124:127], v[154:157], v[178:181], v[124:127]
	v_mfma_f32_16x16x32_bf16 v[112:115], v[144:147], v[188:191], v[112:115]
	v_mfma_f32_16x16x32_bf16 v[108:111], v[154:157], v[188:191], v[108:111]
	v_mfma_f32_16x16x32_bf16 v[96:99], v[144:147], v[196:199], v[96:99]
	v_mfma_f32_16x16x32_bf16 v[92:95], v[154:157], v[196:199], v[92:95]
	v_mfma_f32_16x16x32_bf16 v[80:83], v[144:147], v[210:213], v[80:83]
	v_mfma_f32_16x16x32_bf16 v[76:79], v[154:157], v[210:213], v[76:79]
	v_mfma_f32_16x16x32_bf16 v[128:131], v[150:153], v[184:187], v[128:131]
	v_mfma_f32_16x16x32_bf16 v[124:127], v[158:161], v[184:187], v[124:127]
	v_mfma_f32_16x16x32_bf16 v[112:115], v[150:153], v[192:195], v[112:115]
	v_mfma_f32_16x16x32_bf16 v[108:111], v[158:161], v[192:195], v[108:111]
	v_mfma_f32_16x16x32_bf16 v[96:99], v[150:153], v[206:209], v[96:99]
	v_mfma_f32_16x16x32_bf16 v[92:95], v[158:161], v[206:209], v[92:95]
	v_mfma_f32_16x16x32_bf16 v[80:83], v[150:153], v[214:217], v[80:83]
	v_mfma_f32_16x16x32_bf16 v[76:79], v[158:161], v[214:217], v[76:79]
	s_setprio 0
	s_setprio 1
	v_mfma_f32_16x16x32_bf16 v[120:123], v[162:165], v[178:181], v[120:123]
	v_mfma_f32_16x16x32_bf16 v[116:119], v[170:173], v[178:181], v[116:119]
	v_mfma_f32_16x16x32_bf16 v[104:107], v[162:165], v[188:191], v[104:107]
	v_mfma_f32_16x16x32_bf16 v[100:103], v[170:173], v[188:191], v[100:103]
	v_mfma_f32_16x16x32_bf16 v[88:91], v[162:165], v[196:199], v[88:91]
	v_mfma_f32_16x16x32_bf16 v[84:87], v[170:173], v[196:199], v[84:87]
	v_mfma_f32_16x16x32_bf16 v[72:75], v[162:165], v[210:213], v[72:75]
	v_mfma_f32_16x16x32_bf16 v[68:71], v[170:173], v[210:213], v[68:71]
	v_mfma_f32_16x16x32_bf16 v[120:123], v[166:169], v[184:187], v[120:123]
	v_mfma_f32_16x16x32_bf16 v[116:119], v[174:177], v[184:187], v[116:119]
	v_mfma_f32_16x16x32_bf16 v[104:107], v[166:169], v[192:195], v[104:107]
	v_mfma_f32_16x16x32_bf16 v[100:103], v[174:177], v[192:195], v[100:103]
	v_mfma_f32_16x16x32_bf16 v[88:91], v[166:169], v[206:209], v[88:91]
	v_mfma_f32_16x16x32_bf16 v[84:87], v[174:177], v[206:209], v[84:87]
	v_mfma_f32_16x16x32_bf16 v[72:75], v[166:169], v[214:217], v[72:75]
	v_mfma_f32_16x16x32_bf16 v[68:71], v[174:177], v[214:217], v[68:71]
	s_setprio 0
	s_barrier
; #define G8_STAGE(bufoff, gbase, voff) do { _Pragma("unroll") for (int _i = 0; _i < 2; ++_i) \
;         __builtin_amdgcn_global_load_lds((const unsigned*)((const char*)(gbase) + (voff)[_i]), (LAS unsigned*)(lds + (bufoff) + ldsw + _i * 8192), 16, 0, 0); } while (0)
; #define G8_STAGE_A(bufoff, gbase, h_, nx_) do { if constexpr (Sched::GATHER) { unsigned vo_[2]; _Pragma("unroll") for (int q_ = 0; q_ < 2; ++q_) vo_[q_] = (nx_) ? gnxt[h_][q_] : goff[h_][q_]; G8_STAGE(bufoff, gbase, vo_); } \
;         else { G8_STAGE(bufoff, (gbase) + ((h_) ? hstepA : (size_t)0), voffA); } } while (0)
; #define G8_XLDA(b, h) do { if constexpr (Epi::FP8) { G8_LD8(A8, G8_SA(b, h) + aoff, 4); } else { G8_LDA(At, b, h); } } while (0)
; #define G8_MM0(ai, bj) do { if constexpr (Epi::FP8) { G8_MMA8(ai, bj, A8, B08); } else { G8_MMA(ai, bj, At, B0); } } while (0)
; #define G8_MM1(ai, bj) do { if constexpr (Epi::FP8) { G8_MMA8(ai, bj, A8, B18); } else { G8_MMA(ai, bj, At, B1); } } while (0)
; #define G8_WAIT_L(n) asm volatile("s_waitcnt lgkmcnt(" #n ")" ::: "memory")
; #define G8_BAR __builtin_amdgcn_s_barrier()
; #define G8_SCHED __builtin_amdgcn_sched_barrier(0)
; #define G8_WAIT_VK do { if constexpr (Epi::HALFN) { G8_WAIT_V(6); } else { G8_WAIT_V(8); } } while (0)
; template <int lda, int ldb, class Epi, class Sched>
; __device__ __forceinline__ void gemm_phase(LAS unsigned char* lds, int wid, int lane, const char* baseA, const char* baseB, const Sched& S, const Epi& E) {
;     ...
;         for (int t = 0; t < nt; t += 2) {
;     ...
;             G8_XLDA(1, 1); G8_STAGE(G8_SB(1, 0), b3, voffB); if constexpr (!Epi::HALFN) { G8_STAGE(G8_SB(1, 1), b3 + hstepB, voffB); } G8_STAGE_A(G8_SA(1, 0), a3, 0, last);
;             G8_WAIT_VK; G8_WAIT_L(0); G8_BAR; G8_MM0(1, 0); if constexpr (!Epi::HALFN) { G8_MM1(1, 1); } G8_BAR; G8_SCHED;
;         }
	s_mov_b32 m0, s65
	v_lshl_add_u64 v[218:219], v[218:219], 0, s[22:23]
	s_add_u32 s44, s44, 0x40080
	ds_read_b128 v[178:181], v30 offset:49152
	ds_read_b128 v[184:187], v30 offset:50176
	ds_read_b128 v[188:191], v30 offset:51200
	ds_read_b128 v[192:195], v30 offset:52224
	ds_read_b128 v[196:199], v30 offset:53248
	ds_read_b128 v[206:209], v30 offset:54272
	ds_read_b128 v[210:213], v30 offset:55296
	ds_read_b128 v[214:217], v30 offset:56320
	global_load_lds_dwordx4 v[218:219], off
	v_lshl_add_u64 v[218:219], v[220:221], 0, s[22:23]
	s_mov_b32 m0, s66
	s_addc_u32 s45, s45, 0
	global_load_lds_dwordx4 v[218:219], off
	v_lshl_add_u64 v[218:219], s[44:45], 0, v[134:135]
	s_mov_b32 m0, s69
	s_nop 0
	global_load_lds_dwordx4 v[218:219], off
	v_lshl_add_u64 v[218:219], s[44:45], 0, v[138:139]
	s_mov_b32 m0, s70
	s_nop 0
	global_load_lds_dwordx4 v[218:219], off
	v_lshl_add_u64 v[218:219], v[222:223], 0, s[22:23]
	s_mov_b32 m0, s67
	s_nop 0
	global_load_lds_dwordx4 v[218:219], off
	v_lshl_add_u64 v[218:219], v[224:225], 0, s[22:23]
	s_mov_b32 m0, s68
	s_nop 0
	global_load_lds_dwordx4 v[218:219], off
	s_waitcnt vmcnt(8)
	s_waitcnt lgkmcnt(0)
	s_barrier
	s_setprio 1
	s_waitcnt lgkmcnt(0)
	v_mfma_f32_16x16x32_bf16 v[64:67], v[144:147], v[178:181], v[64:67]
	v_mfma_f32_16x16x32_bf16 v[60:63], v[154:157], v[178:181], v[60:63]
	v_mfma_f32_16x16x32_bf16 v[48:51], v[144:147], v[188:191], v[48:51]
	v_mfma_f32_16x16x32_bf16 v[44:47], v[154:157], v[188:191], v[44:47]
	v_mfma_f32_16x16x32_bf16 v[32:35], v[144:147], v[196:199], v[32:35]
	v_mfma_f32_16x16x32_bf16 v[26:29], v[154:157], v[196:199], v[26:29]
	v_mfma_f32_16x16x32_bf16 v[14:17], v[144:147], v[210:213], v[14:17]
	v_mfma_f32_16x16x32_bf16 v[10:13], v[154:157], v[210:213], v[10:13]
	v_mfma_f32_16x16x32_bf16 v[64:67], v[150:153], v[184:187], v[64:67]
	v_mfma_f32_16x16x32_bf16 v[60:63], v[158:161], v[184:187], v[60:63]
	v_mfma_f32_16x16x32_bf16 v[48:51], v[150:153], v[192:195], v[48:51]
	v_mfma_f32_16x16x32_bf16 v[44:47], v[158:161], v[192:195], v[44:47]
	v_mfma_f32_16x16x32_bf16 v[32:35], v[150:153], v[206:209], v[32:35]
	v_mfma_f32_16x16x32_bf16 v[26:29], v[158:161], v[206:209], v[26:29]
	v_mfma_f32_16x16x32_bf16 v[14:17], v[150:153], v[214:217], v[14:17]
	v_mfma_f32_16x16x32_bf16 v[10:13], v[158:161], v[214:217], v[10:13]
	s_setprio 0
	s_setprio 1
	v_mfma_f32_16x16x32_bf16 v[56:59], v[162:165], v[178:181], v[56:59]
	v_mfma_f32_16x16x32_bf16 v[52:55], v[170:173], v[178:181], v[52:55]
	v_mfma_f32_16x16x32_bf16 v[40:43], v[162:165], v[188:191], v[40:43]
	v_mfma_f32_16x16x32_bf16 v[36:39], v[170:173], v[188:191], v[36:39]
	v_mfma_f32_16x16x32_bf16 v[22:25], v[162:165], v[196:199], v[22:25]
	v_mfma_f32_16x16x32_bf16 v[18:21], v[170:173], v[196:199], v[18:21]
	v_mfma_f32_16x16x32_bf16 v[6:9], v[162:165], v[210:213], v[6:9]
	v_mfma_f32_16x16x32_bf16 v[2:5], v[170:173], v[210:213], v[2:5]
	v_mfma_f32_16x16x32_bf16 v[56:59], v[166:169], v[184:187], v[56:59]
	v_mfma_f32_16x16x32_bf16 v[52:55], v[174:177], v[184:187], v[52:55]
	v_mfma_f32_16x16x32_bf16 v[40:43], v[166:169], v[192:195], v[40:43]
	v_mfma_f32_16x16x32_bf16 v[36:39], v[174:177], v[192:195], v[36:39]
	v_mfma_f32_16x16x32_bf16 v[22:25], v[166:169], v[206:209], v[22:25]
	v_mfma_f32_16x16x32_bf16 v[18:21], v[174:177], v[206:209], v[18:21]
	v_mfma_f32_16x16x32_bf16 v[6:9], v[166:169], v[214:217], v[6:9]
	v_mfma_f32_16x16x32_bf16 v[2:5], v[174:177], v[214:217], v[2:5]
	s_setprio 0
	s_add_u32 s42, s42, 0x100
	s_addc_u32 s43, s43, 0
	s_add_u32 s57, s57, 0x100
	s_addc_u32 s77, s77, 0
	s_cmp_ge_i32 s78, s4
	s_mov_b32 s44, s78
	s_barrier
	s_cbranch_scc0 .LBB0_367
	s_and_b64 vcc, exec, s[36:37]
	s_cbranch_vccz .LBB0_370

; #define G8_STAGE(bufoff, gbase, voff) do { _Pragma("unroll") for (int _i = 0; _i < 2; ++_i) \
;         __builtin_amdgcn_global_load_lds((const unsigned*)((const char*)(gbase) + (voff)[_i]), (LAS unsigned*)(lds + (bufoff) + ldsw + _i * 8192), 16, 0, 0); } while (0)
; #define G8_STAGE_A(bufoff, gbase, h_, nx_) do { if constexpr (Sched::GATHER) { unsigned vo_[2]; _Pragma("unroll") for (int q_ = 0; q_ < 2; ++q_) vo_[q_] = (nx_) ? gnxt[h_][q_] : goff[h_][q_]; G8_STAGE(bufoff, gbase, vo_); } \
;         else { G8_STAGE(bufoff, (gbase) + ((h_) ? hstepA : (size_t)0), voffA); } } while (0)
; #define G8_XLDA(b, h) do { if constexpr (Epi::FP8) { G8_LD8(A8, G8_SA(b, h) + aoff, 4); } else { G8_LDA(At, b, h); } } while (0)
; #define G8_XLDB0(b, h) do { if constexpr (Epi::FP8) { G8_LD8(B08, G8_SB(b, h) + boff, 2); } else { G8_LDB(B0, b, h); } } while (0)
; #define G8_XLDB1(b, h) do { if constexpr (Epi::FP8) { G8_LD8(B18, G8_SB(b, h) + boff, 2); } else { G8_LDB(B1, b, h); } } while (0)
; #define G8_MM0(ai, bj) do { if constexpr (Epi::FP8) { G8_MMA8(ai, bj, A8, B08); } else { G8_MMA(ai, bj, At, B0); } } while (0)
; #define G8_MM1(ai, bj) do { if constexpr (Epi::FP8) { G8_MMA8(ai, bj, A8, B18); } else { G8_MMA(ai, bj, At, B1); } } while (0)
; template <int lda, int ldb, class Epi, class Sched>
; __device__ __forceinline__ void gemm_phase(LAS unsigned char* lds, int wid, int lane, const char* baseA, const char* baseB, const Sched& S, const Epi& E) {
;     ...
;         for (int t = 0; t < nt; t += 2) {
;             const bool last = (t == nt - 2);
;             const char* a1 = cA + (size_t)(t + 1) * kstep;
;             const char* a2 = last ? nA : cA + (size_t)(t + 2) * kstep; const char* b2 = last ? nB : cB + (size_t)(t + 2) * kstep;
;             const char* a3 = a2 + kstep; const char* b3 = b2 + kstep;
;     ...
;             G8_XLDB0(0, 0); if constexpr (!Epi::HALFN) { G8_XLDB1(0, 1); } G8_SCHED; G8_XLDA(0, 0); G8_STAGE_A(G8_SA(1, 1), a1, 1, false);
;             G8_WAIT_VK; G8_WAIT_L(0); G8_BAR; G8_MM0(0, 0); if constexpr (!Epi::HALFN) { G8_MM1(0, 1); } G8_BAR; G8_SCHED;
;             G8_XLDA(0, 1); G8_STAGE(G8_SB(0, 0), b2, voffB); if constexpr (!Epi::HALFN) { G8_STAGE(G8_SB(0, 1), b2 + hstepB, voffB); } G8_STAGE_A(G8_SA(0, 0), a2, 0, last);
;             G8_WAIT_VK; G8_WAIT_L(0); G8_BAR; G8_MM0(1, 0); if constexpr (!Epi::HALFN) { G8_MM1(1, 1); } G8_BAR; G8_SCHED;
.LBB0_452:
	ds_read_b128 v[4:7], v178
	ds_read_b128 v[8:11], v179
	ds_read_b128 v[0:3], v148
	ds_read_b128 v[214:217], v151
	ds_read_b128 v[12:15], v180
	ds_read_b128 v[218:221], v181
	ds_read_b128 v[222:225], v205
	ds_read_b128 v[226:229], v206
	s_add_i32 s74, s46, 2
	s_add_u32 s47, s44, 0xfffe0080
	s_addc_u32 s48, s45, -1
	s_cmp_eq_u32 s71, s46
	s_cselect_b32 s46, s70, s72
	s_cselect_b32 s49, s21, s48
	s_cselect_b32 s48, s28, s47
	s_cselect_b32 s47, s29, s73
	v_lshl_add_u64 v[152:153], s[44:45], 0, v[166:167]
	s_add_i32 m0, s27, 0xc000
	ds_read_b128 v[168:171], v213
	ds_read_b128 v[172:175], v213 offset:1024
	ds_read_b128 v[230:233], v213 offset:2048
	ds_read_b128 v[234:237], v213 offset:3072
	ds_read_b128 v[238:241], v213 offset:4096
	ds_read_b128 v[242:245], v213 offset:5120
	ds_read_b128 v[192:195], v213 offset:6144
	ds_read_b128 v[196:199], v213 offset:7168
	global_load_lds_dwordx4 v[152:153], off
	v_lshl_add_u64 v[152:153], s[44:45], 0, v[164:165]
	s_add_i32 m0, s27, 0xe000
	s_nop 0
	global_load_lds_dwordx4 v[152:153], off
	s_waitcnt vmcnt(8)
	s_waitcnt lgkmcnt(0)
	s_barrier
	s_setprio 1
	s_waitcnt lgkmcnt(0)
	v_mfma_scale_f32_16x16x128_f8f6f4 v[144:147], v[0:7], v[168:175], v[144:147], v30, v30 op_sel_hi:[0,0,0]
	v_mfma_scale_f32_16x16x128_f8f6f4 v[140:143], v[8:15], v[168:175], v[140:143], v30, v30 op_sel_hi:[0,0,0]
	v_mfma_scale_f32_16x16x128_f8f6f4 v[136:139], v[0:7], v[230:237], v[136:139], v30, v30 op_sel_hi:[0,0,0]
	v_mfma_scale_f32_16x16x128_f8f6f4 v[132:135], v[8:15], v[230:237], v[132:135], v30, v30 op_sel_hi:[0,0,0]
	v_mfma_scale_f32_16x16x128_f8f6f4 v[128:131], v[0:7], v[238:245], v[128:131], v30, v30 op_sel_hi:[0,0,0]
	v_mfma_scale_f32_16x16x128_f8f6f4 v[124:127], v[8:15], v[238:245], v[124:127], v30, v30 op_sel_hi:[0,0,0]
	v_mfma_scale_f32_16x16x128_f8f6f4 v[120:123], v[0:7], v[192:199], v[120:123], v30, v30 op_sel_hi:[0,0,0]
	v_mfma_scale_f32_16x16x128_f8f6f4 v[116:119], v[8:15], v[192:199], v[116:119], v30, v30 op_sel_hi:[0,0,0]
	s_setprio 0
	s_setprio 1
	v_mfma_scale_f32_16x16x128_f8f6f4 v[80:83], v[214:221], v[168:175], v[80:83], v30, v30 op_sel_hi:[0,0,0]
	v_mfma_scale_f32_16x16x128_f8f6f4 v[76:79], v[222:229], v[168:175], v[76:79], v30, v30 op_sel_hi:[0,0,0]
	v_mfma_scale_f32_16x16x128_f8f6f4 v[72:75], v[214:221], v[230:237], v[72:75], v30, v30 op_sel_hi:[0,0,0]
	v_mfma_scale_f32_16x16x128_f8f6f4 v[68:71], v[222:229], v[230:237], v[68:71], v30, v30 op_sel_hi:[0,0,0]
	v_mfma_scale_f32_16x16x128_f8f6f4 v[64:67], v[214:221], v[238:245], v[64:67], v30, v30 op_sel_hi:[0,0,0]
	v_mfma_scale_f32_16x16x128_f8f6f4 v[60:63], v[222:229], v[238:245], v[60:63], v30, v30 op_sel_hi:[0,0,0]
	v_mfma_scale_f32_16x16x128_f8f6f4 v[56:59], v[214:221], v[192:199], v[56:59], v30, v30 op_sel_hi:[0,0,0]
	v_mfma_scale_f32_16x16x128_f8f6f4 v[52:55], v[222:229], v[192:199], v[52:55], v30, v30 op_sel_hi:[0,0,0]
	s_setprio 0
	s_barrier
	s_mov_b32 m0, s51
	v_lshl_add_u64 v[168:169], s[46:47], 0, v[160:161]
	s_add_u32 s76, s46, 0x20000
	ds_read_b128 v[192:195], v213 offset:16384
	ds_read_b128 v[196:199], v213 offset:17408
	ds_read_b128 v[230:233], v213 offset:18432
	ds_read_b128 v[234:237], v213 offset:19456
	ds_read_b128 v[238:241], v213 offset:20480
	ds_read_b128 v[242:245], v213 offset:21504
	ds_read_b128 v[184:187], v213 offset:22528
	ds_read_b128 v[188:191], v213 offset:23552
	global_load_lds_dwordx4 v[168:169], off
	v_lshl_add_u64 v[170:171], s[46:47], 0, v[156:157]
	s_mov_b32 m0, s52
	s_addc_u32 s77, s47, 0
	global_load_lds_dwordx4 v[170:171], off
	v_lshl_add_u64 v[152:153], s[76:77], 0, v[160:161]
	s_mov_b32 m0, s53
	v_lshl_add_u64 v[172:173], s[48:49], 0, v[162:163]
	global_load_lds_dwordx4 v[152:153], off
	v_lshl_add_u64 v[152:153], s[76:77], 0, v[156:157]
	s_mov_b32 m0, s54
	v_lshl_add_u64 v[174:175], s[48:49], 0, v[158:159]
	global_load_lds_dwordx4 v[152:153], off
	s_mov_b32 m0, s27
	s_nop 0
	global_load_lds_dwordx4 v[172:173], off
	s_mov_b32 m0, s55
	s_nop 0
	global_load_lds_dwordx4 v[174:175], off
	s_waitcnt vmcnt(8)
	s_waitcnt lgkmcnt(0)
	s_barrier
	s_setprio 1
	s_waitcnt lgkmcnt(0)
	v_mfma_scale_f32_16x16x128_f8f6f4 v[112:115], v[0:7], v[192:199], v[112:115], v30, v30 op_sel_hi:[0,0,0]
	v_mfma_scale_f32_16x16x128_f8f6f4 v[108:111], v[8:15], v[192:199], v[108:111], v30, v30 op_sel_hi:[0,0,0]
	v_mfma_scale_f32_16x16x128_f8f6f4 v[104:107], v[0:7], v[230:237], v[104:107], v30, v30 op_sel_hi:[0,0,0]
	v_mfma_scale_f32_16x16x128_f8f6f4 v[100:103], v[8:15], v[230:237], v[100:103], v30, v30 op_sel_hi:[0,0,0]
	v_mfma_scale_f32_16x16x128_f8f6f4 v[96:99], v[0:7], v[238:245], v[96:99], v30, v30 op_sel_hi:[0,0,0]
	v_mfma_scale_f32_16x16x128_f8f6f4 v[92:95], v[8:15], v[238:245], v[92:95], v30, v30 op_sel_hi:[0,0,0]
	v_mfma_scale_f32_16x16x128_f8f6f4 v[88:91], v[0:7], v[184:191], v[88:91], v30, v30 op_sel_hi:[0,0,0]
	v_mfma_scale_f32_16x16x128_f8f6f4 v[84:87], v[8:15], v[184:191], v[84:87], v30, v30 op_sel_hi:[0,0,0]
	s_setprio 0
	s_setprio 1
	v_mfma_scale_f32_16x16x128_f8f6f4 v[48:51], v[214:221], v[192:199], v[48:51], v30, v30 op_sel_hi:[0,0,0]
	v_mfma_scale_f32_16x16x128_f8f6f4 v[44:47], v[222:229], v[192:199], v[44:47], v30, v30 op_sel_hi:[0,0,0]
	v_mfma_scale_f32_16x16x128_f8f6f4 v[40:43], v[214:221], v[230:237], v[40:43], v30, v30 op_sel_hi:[0,0,0]
	v_mfma_scale_f32_16x16x128_f8f6f4 v[36:39], v[222:229], v[230:237], v[36:39], v30, v30 op_sel_hi:[0,0,0]
	v_mfma_scale_f32_16x16x128_f8f6f4 v[32:35], v[214:221], v[238:245], v[32:35], v30, v30 op_sel_hi:[0,0,0]
	v_mfma_scale_f32_16x16x128_f8f6f4 v[26:29], v[222:229], v[238:245], v[26:29], v30, v30 op_sel_hi:[0,0,0]
	v_mfma_scale_f32_16x16x128_f8f6f4 v[22:25], v[214:221], v[184:191], v[22:25], v30, v30 op_sel_hi:[0,0,0]
	v_mfma_scale_f32_16x16x128_f8f6f4 v[18:21], v[222:229], v[184:191], v[18:21], v30, v30 op_sel_hi:[0,0,0]
	s_setprio 0
	s_barrier
; #define G8_STAGE(bufoff, gbase, voff) do { _Pragma("unroll") for (int _i = 0; _i < 2; ++_i) \
;         __builtin_amdgcn_global_load_lds((const unsigned*)((const char*)(gbase) + (voff)[_i]), (LAS unsigned*)(lds + (bufoff) + ldsw + _i * 8192), 16, 0, 0); } while (0)
; #define G8_STAGE_A(bufoff, gbase, h_, nx_) do { if constexpr (Sched::GATHER) { unsigned vo_[2]; _Pragma("unroll") for (int q_ = 0; q_ < 2; ++q_) vo_[q_] = (nx_) ? gnxt[h_][q_] : goff[h_][q_]; G8_STAGE(bufoff, gbase, vo_); } \
;         else { G8_STAGE(bufoff, (gbase) + ((h_) ? hstepA : (size_t)0), voffA); } } while (0)
; #define G8_XLDA(b, h) do { if constexpr (Epi::FP8) { G8_LD8(A8, G8_SA(b, h) + aoff, 4); } else { G8_LDA(At, b, h); } } while (0)
; #define G8_XLDB0(b, h) do { if constexpr (Epi::FP8) { G8_LD8(B08, G8_SB(b, h) + boff, 2); } else { G8_LDB(B0, b, h); } } while (0)
; #define G8_XLDB1(b, h) do { if constexpr (Epi::FP8) { G8_LD8(B18, G8_SB(b, h) + boff, 2); } else { G8_LDB(B1, b, h); } } while (0)
; #define G8_MM0(ai, bj) do { if constexpr (Epi::FP8) { G8_MMA8(ai, bj, A8, B08); } else { G8_MMA(ai, bj, At, B0); } } while (0)
; #define G8_MM1(ai, bj) do { if constexpr (Epi::FP8) { G8_MMA8(ai, bj, A8, B18); } else { G8_MMA(ai, bj, At, B1); } } while (0)
; #define G8_WAIT_L(n) asm volatile("s_waitcnt lgkmcnt(" #n ")" ::: "memory")
; #define G8_BAR __builtin_amdgcn_s_barrier()
; #define G8_SCHED __builtin_amdgcn_sched_barrier(0)
; #define G8_WAIT_VK do { if constexpr (Epi::HALFN) { G8_WAIT_V(6); } else { G8_WAIT_V(8); } } while (0)
; template <int lda, int ldb, class Epi, class Sched>
; __device__ __forceinline__ void gemm_phase(LAS unsigned char* lds, int wid, int lane, const char* baseA, const char* baseB, const Sched& S, const Epi& E) {
;     ...
;             G8_XLDB0(1, 0); if constexpr (!Epi::HALFN) { G8_XLDB1(1, 1); } G8_SCHED; G8_XLDA(1, 0); G8_STAGE_A(G8_SA(0, 1), a2, 1, last);
;             G8_WAIT_VK; G8_WAIT_L(0); G8_BAR; G8_MM0(0, 0); if constexpr (!Epi::HALFN) { G8_MM1(0, 1); } G8_BAR; G8_SCHED;
;             G8_XLDA(1, 1); G8_STAGE(G8_SB(1, 0), b3, voffB); if constexpr (!Epi::HALFN) { G8_STAGE(G8_SB(1, 1), b3 + hstepB, voffB); } G8_STAGE_A(G8_SA(1, 0), a3, 0, last);
;             G8_WAIT_VK; G8_WAIT_L(0); G8_BAR; G8_MM0(1, 0); if constexpr (!Epi::HALFN) { G8_MM1(1, 1); } G8_BAR; G8_SCHED;
;         }
	ds_read_b128 v[12:15], v207
	ds_read_b128 v[184:187], v208
	ds_read_b128 v[8:11], v176
	ds_read_b128 v[0:3], v177
	ds_read_b128 v[188:191], v209
	ds_read_b128 v[4:7], v210
	ds_read_b128 v[192:195], v211
	ds_read_b128 v[196:199], v212
	s_add_u32 s48, s48, 0x20000
	s_addc_u32 s49, s49, 0
	s_mov_b32 m0, s56
	v_lshl_add_u64 v[152:153], s[48:49], 0, v[162:163]
	ds_read_b128 v[214:217], v213 offset:32768
	ds_read_b128 v[218:221], v213 offset:33792
	ds_read_b128 v[222:225], v213 offset:34816
	ds_read_b128 v[226:229], v213 offset:35840
	ds_read_b128 v[230:233], v213 offset:36864
	ds_read_b128 v[234:237], v213 offset:37888
	ds_read_b128 v[238:241], v213 offset:38912
	ds_read_b128 v[242:245], v213 offset:39936
	global_load_lds_dwordx4 v[152:153], off
	v_lshl_add_u64 v[152:153], s[48:49], 0, v[158:159]
	s_mov_b32 m0, s57
	s_nop 0
	global_load_lds_dwordx4 v[152:153], off
	s_waitcnt vmcnt(8)
	s_waitcnt lgkmcnt(0)
	s_barrier
	s_setprio 1
	s_waitcnt lgkmcnt(0)
	v_mfma_scale_f32_16x16x128_f8f6f4 v[144:147], v[8:15], v[214:221], v[144:147], v30, v30 op_sel_hi:[0,0,0]
	v_mfma_scale_f32_16x16x128_f8f6f4 v[140:143], v[184:191], v[214:221], v[140:143], v30, v30 op_sel_hi:[0,0,0]
	v_mfma_scale_f32_16x16x128_f8f6f4 v[136:139], v[8:15], v[222:229], v[136:139], v30, v30 op_sel_hi:[0,0,0]
	v_mfma_scale_f32_16x16x128_f8f6f4 v[132:135], v[184:191], v[222:229], v[132:135], v30, v30 op_sel_hi:[0,0,0]
	v_mfma_scale_f32_16x16x128_f8f6f4 v[128:131], v[8:15], v[230:237], v[128:131], v30, v30 op_sel_hi:[0,0,0]
	v_mfma_scale_f32_16x16x128_f8f6f4 v[124:127], v[184:191], v[230:237], v[124:127], v30, v30 op_sel_hi:[0,0,0]
	v_mfma_scale_f32_16x16x128_f8f6f4 v[120:123], v[8:15], v[238:245], v[120:123], v30, v30 op_sel_hi:[0,0,0]
	v_mfma_scale_f32_16x16x128_f8f6f4 v[116:119], v[184:191], v[238:245], v[116:119], v30, v30 op_sel_hi:[0,0,0]
	s_setprio 0
	s_setprio 1
	v_mfma_scale_f32_16x16x128_f8f6f4 v[80:83], v[0:7], v[214:221], v[80:83], v30, v30 op_sel_hi:[0,0,0]
	v_mfma_scale_f32_16x16x128_f8f6f4 v[76:79], v[192:199], v[214:221], v[76:79], v30, v30 op_sel_hi:[0,0,0]
	v_mfma_scale_f32_16x16x128_f8f6f4 v[72:75], v[0:7], v[222:229], v[72:75], v30, v30 op_sel_hi:[0,0,0]
	v_mfma_scale_f32_16x16x128_f8f6f4 v[68:71], v[192:199], v[222:229], v[68:71], v30, v30 op_sel_hi:[0,0,0]
	v_mfma_scale_f32_16x16x128_f8f6f4 v[64:67], v[0:7], v[230:237], v[64:67], v30, v30 op_sel_hi:[0,0,0]
	v_mfma_scale_f32_16x16x128_f8f6f4 v[60:63], v[192:199], v[230:237], v[60:63], v30, v30 op_sel_hi:[0,0,0]
	v_mfma_scale_f32_16x16x128_f8f6f4 v[56:59], v[0:7], v[238:245], v[56:59], v30, v30 op_sel_hi:[0,0,0]
	v_mfma_scale_f32_16x16x128_f8f6f4 v[52:55], v[192:199], v[238:245], v[52:55], v30, v30 op_sel_hi:[0,0,0]
	s_setprio 0
	s_barrier
	s_mov_b32 m0, s58
	v_lshl_add_u64 v[152:153], v[168:169], 0, s[22:23]
	s_add_u32 s46, s46, 0x20080
	ds_read_b128 v[214:217], v213 offset:49152
	ds_read_b128 v[218:221], v213 offset:50176
	ds_read_b128 v[222:225], v213 offset:51200
	ds_read_b128 v[226:229], v213 offset:52224
	ds_read_b128 v[230:233], v213 offset:53248
	ds_read_b128 v[234:237], v213 offset:54272
	ds_read_b128 v[238:241], v213 offset:55296
	ds_read_b128 v[242:245], v213 offset:56320
	global_load_lds_dwordx4 v[152:153], off
	v_lshl_add_u64 v[152:153], v[170:171], 0, s[22:23]
	s_mov_b32 m0, s59
	s_addc_u32 s47, s47, 0
	global_load_lds_dwordx4 v[152:153], off
	v_lshl_add_u64 v[152:153], s[46:47], 0, v[160:161]
	s_mov_b32 m0, s62
	s_nop 0
	global_load_lds_dwordx4 v[152:153], off
	v_lshl_add_u64 v[152:153], s[46:47], 0, v[156:157]
	s_mov_b32 m0, s63
	s_nop 0
	global_load_lds_dwordx4 v[152:153], off
	v_lshl_add_u64 v[152:153], v[172:173], 0, s[22:23]
	s_mov_b32 m0, s60
	s_nop 0
	global_load_lds_dwordx4 v[152:153], off
	v_lshl_add_u64 v[152:153], v[174:175], 0, s[22:23]
	s_mov_b32 m0, s61
	s_nop 0
	global_load_lds_dwordx4 v[152:153], off
	s_waitcnt vmcnt(8)
	s_waitcnt lgkmcnt(0)
	s_barrier
	s_setprio 1
	s_waitcnt lgkmcnt(0)
	v_mfma_scale_f32_16x16x128_f8f6f4 v[112:115], v[8:15], v[214:221], v[112:115], v30, v30 op_sel_hi:[0,0,0]
	v_mfma_scale_f32_16x16x128_f8f6f4 v[108:111], v[184:191], v[214:221], v[108:111], v30, v30 op_sel_hi:[0,0,0]
	v_mfma_scale_f32_16x16x128_f8f6f4 v[104:107], v[8:15], v[222:229], v[104:107], v30, v30 op_sel_hi:[0,0,0]
	v_mfma_scale_f32_16x16x128_f8f6f4 v[100:103], v[184:191], v[222:229], v[100:103], v30, v30 op_sel_hi:[0,0,0]
	v_mfma_scale_f32_16x16x128_f8f6f4 v[96:99], v[8:15], v[230:237], v[96:99], v30, v30 op_sel_hi:[0,0,0]
	v_mfma_scale_f32_16x16x128_f8f6f4 v[92:95], v[184:191], v[230:237], v[92:95], v30, v30 op_sel_hi:[0,0,0]
	v_mfma_scale_f32_16x16x128_f8f6f4 v[88:91], v[8:15], v[238:245], v[88:91], v30, v30 op_sel_hi:[0,0,0]
	v_mfma_scale_f32_16x16x128_f8f6f4 v[84:87], v[184:191], v[238:245], v[84:87], v30, v30 op_sel_hi:[0,0,0]
	s_setprio 0
	s_setprio 1
	v_mfma_scale_f32_16x16x128_f8f6f4 v[48:51], v[0:7], v[214:221], v[48:51], v30, v30 op_sel_hi:[0,0,0]
	v_mfma_scale_f32_16x16x128_f8f6f4 v[44:47], v[192:199], v[214:221], v[44:47], v30, v30 op_sel_hi:[0,0,0]
	v_mfma_scale_f32_16x16x128_f8f6f4 v[40:43], v[0:7], v[222:229], v[40:43], v30, v30 op_sel_hi:[0,0,0]
	v_mfma_scale_f32_16x16x128_f8f6f4 v[36:39], v[192:199], v[222:229], v[36:39], v30, v30 op_sel_hi:[0,0,0]
	v_mfma_scale_f32_16x16x128_f8f6f4 v[32:35], v[0:7], v[230:237], v[32:35], v30, v30 op_sel_hi:[0,0,0]
	v_mfma_scale_f32_16x16x128_f8f6f4 v[26:29], v[192:199], v[230:237], v[26:29], v30, v30 op_sel_hi:[0,0,0]
	v_mfma_scale_f32_16x16x128_f8f6f4 v[22:25], v[0:7], v[238:245], v[22:25], v30, v30 op_sel_hi:[0,0,0]
	v_mfma_scale_f32_16x16x128_f8f6f4 v[18:21], v[192:199], v[238:245], v[18:21], v30, v30 op_sel_hi:[0,0,0]
	s_setprio 0
	s_add_u32 s72, s72, 0x100
	s_addc_u32 s73, s73, 0
	s_add_u32 s44, s44, 0x100
	s_addc_u32 s45, s45, 0
	s_cmp_ge_i32 s74, s4
	s_mov_b32 s46, s74
	s_barrier
	s_cbranch_scc0 .LBB0_452
	s_mov_b32 s76, 0x9800
	s_mov_b32 s72, s94
	s_and_b64 vcc, exec, s[36:37]
	s_cbranch_vccz .LBB0_455

; #define G8_STAGE(bufoff, gbase, voff) do { _Pragma("unroll") for (int _i = 0; _i < 2; ++_i) \
;         __builtin_amdgcn_global_load_lds((const unsigned*)((const char*)(gbase) + (voff)[_i]), (LAS unsigned*)(lds + (bufoff) + ldsw + _i * 8192), 16, 0, 0); } while (0)
; #define G8_STAGE_A(bufoff, gbase, h_, nx_) do { if constexpr (Sched::GATHER) { unsigned vo_[2]; _Pragma("unroll") for (int q_ = 0; q_ < 2; ++q_) vo_[q_] = (nx_) ? gnxt[h_][q_] : goff[h_][q_]; G8_STAGE(bufoff, gbase, vo_); } \
;         else { G8_STAGE(bufoff, (gbase) + ((h_) ? hstepA : (size_t)0), voffA); } } while (0)
; #define G8_XLDA(b, h) do { if constexpr (Epi::FP8) { G8_LD8(A8, G8_SA(b, h) + aoff, 4); } else { G8_LDA(At, b, h); } } while (0)
; #define G8_XLDB0(b, h) do { if constexpr (Epi::FP8) { G8_LD8(B08, G8_SB(b, h) + boff, 2); } else { G8_LDB(B0, b, h); } } while (0)
; #define G8_XLDB1(b, h) do { if constexpr (Epi::FP8) { G8_LD8(B18, G8_SB(b, h) + boff, 2); } else { G8_LDB(B1, b, h); } } while (0)
; #define G8_MM0(ai, bj) do { if constexpr (Epi::FP8) { G8_MMA8(ai, bj, A8, B08); } else { G8_MMA(ai, bj, At, B0); } } while (0)
; #define G8_MM1(ai, bj) do { if constexpr (Epi::FP8) { G8_MMA8(ai, bj, A8, B18); } else { G8_MMA(ai, bj, At, B1); } } while (0)
; #define G8_WAIT_L(n) asm volatile("s_waitcnt lgkmcnt(" #n ")" ::: "memory")
; #define G8_BAR __builtin_amdgcn_s_barrier()
; template <int lda, int ldb, class Epi, class Sched>
; __device__ __forceinline__ void gemm_phase(LAS unsigned char* lds, int wid, int lane, const char* baseA, const char* baseB, const Sched& S, const Epi& E) {
;     ...
;         for (int t = 0; t < nt; t += 2) {
;             const bool last = (t == nt - 2);
;             const char* a1 = cA + (size_t)(t + 1) * kstep;
;             const char* a2 = last ? nA : cA + (size_t)(t + 2) * kstep; const char* b2 = last ? nB : cB + (size_t)(t + 2) * kstep;
;             const char* a3 = a2 + kstep; const char* b3 = b2 + kstep;
;     ...
;             G8_XLDB0(0, 0); if constexpr (!Epi::HALFN) { G8_XLDB1(0, 1); } G8_SCHED; G8_XLDA(0, 0); G8_STAGE_A(G8_SA(1, 1), a1, 1, false);
;             G8_WAIT_VK; G8_WAIT_L(0); G8_BAR; G8_MM0(0, 0); if constexpr (!Epi::HALFN) { G8_MM1(0, 1); } G8_BAR; G8_SCHED;
;             G8_XLDA(0, 1); G8_STAGE(G8_SB(0, 0), b2, voffB); if constexpr (!Epi::HALFN) { G8_STAGE(G8_SB(0, 1), b2 + hstepB, voffB); } G8_STAGE_A(G8_SA(0, 0), a2, 0, last);
.LBB0_533:
	v_add_u32_e32 v5, 0x10000, v151
	ds_read_b128 v[132:135], v5
	ds_read_b128 v[136:139], v5 offset:1024
	ds_read_b128 v[152:155], v5 offset:2048
	ds_read_b128 v[178:181], v5 offset:3072
	v_add_u32_e32 v5, 0x14000, v151
	ds_read_b128 v[184:187], v5
	ds_read_b128 v[188:191], v5 offset:1024
	ds_read_b128 v[192:195], v5 offset:2048
	ds_read_b128 v[196:199], v5 offset:3072
	s_add_i32 s85, s16, 2
	s_add_u32 s14, s10, 0x100
	s_addc_u32 s15, s11, 0
	s_cmp_eq_u32 s82, s16
	s_cselect_b32 s16, s81, s83
	s_cselect_b32 s35, s21, s15
	s_cselect_b32 s34, s28, s14
	s_cselect_b32 s17, s29, s84
	v_lshl_add_u64 v[164:165], s[10:11], 0, v[156:157]
	s_add_i32 m0, s27, 0xc000
	ds_read_b128 v[206:209], v148
	ds_read_b128 v[210:213], v148 offset:1024
	ds_read_b128 v[214:217], v148 offset:2048
	ds_read_b128 v[218:221], v148 offset:3072
	ds_read_b128 v[222:225], v148 offset:4096
	ds_read_b128 v[226:229], v148 offset:5120
	ds_read_b128 v[230:233], v148 offset:6144
	ds_read_b128 v[234:237], v148 offset:7168
	global_load_lds_dwordx4 v[164:165], off
	v_lshl_add_u64 v[164:165], s[10:11], 0, v[158:159]
	s_add_i32 m0, s27, 0xe000
	s_nop 0
	global_load_lds_dwordx4 v[164:165], off
	s_waitcnt vmcnt(8)
	s_waitcnt lgkmcnt(0)
	s_barrier
	s_setprio 1
	s_waitcnt lgkmcnt(0)
	v_mfma_f32_16x16x32_bf16 v[128:131], v[132:135], v[206:209], v[128:131]
	v_mfma_f32_16x16x32_bf16 v[124:127], v[152:155], v[206:209], v[124:127]
	v_mfma_f32_16x16x32_bf16 v[112:115], v[132:135], v[214:217], v[112:115]
	v_mfma_f32_16x16x32_bf16 v[108:111], v[152:155], v[214:217], v[108:111]
	v_mfma_f32_16x16x32_bf16 v[96:99], v[132:135], v[222:225], v[96:99]
	v_mfma_f32_16x16x32_bf16 v[92:95], v[152:155], v[222:225], v[92:95]
	v_mfma_f32_16x16x32_bf16 v[80:83], v[132:135], v[230:233], v[80:83]
	v_mfma_f32_16x16x32_bf16 v[76:79], v[152:155], v[230:233], v[76:79]
	v_mfma_f32_16x16x32_bf16 v[128:131], v[136:139], v[210:213], v[128:131]
	v_mfma_f32_16x16x32_bf16 v[124:127], v[178:181], v[210:213], v[124:127]
	v_mfma_f32_16x16x32_bf16 v[112:115], v[136:139], v[218:221], v[112:115]
	v_mfma_f32_16x16x32_bf16 v[108:111], v[178:181], v[218:221], v[108:111]
	v_mfma_f32_16x16x32_bf16 v[96:99], v[136:139], v[226:229], v[96:99]
	v_mfma_f32_16x16x32_bf16 v[92:95], v[178:181], v[226:229], v[92:95]
	v_mfma_f32_16x16x32_bf16 v[80:83], v[136:139], v[234:237], v[80:83]
	v_mfma_f32_16x16x32_bf16 v[76:79], v[178:181], v[234:237], v[76:79]
	s_setprio 0
	s_setprio 1
	v_mfma_f32_16x16x32_bf16 v[120:123], v[184:187], v[206:209], v[120:123]
	v_mfma_f32_16x16x32_bf16 v[116:119], v[192:195], v[206:209], v[116:119]
	v_mfma_f32_16x16x32_bf16 v[104:107], v[184:187], v[214:217], v[104:107]
	v_mfma_f32_16x16x32_bf16 v[100:103], v[192:195], v[214:217], v[100:103]
	v_mfma_f32_16x16x32_bf16 v[88:91], v[184:187], v[222:225], v[88:91]
	v_mfma_f32_16x16x32_bf16 v[84:87], v[192:195], v[222:225], v[84:87]
	v_mfma_f32_16x16x32_bf16 v[72:75], v[184:187], v[230:233], v[72:75]
	v_mfma_f32_16x16x32_bf16 v[68:71], v[192:195], v[230:233], v[68:71]
	v_mfma_f32_16x16x32_bf16 v[120:123], v[188:191], v[210:213], v[120:123]
	v_mfma_f32_16x16x32_bf16 v[116:119], v[196:199], v[210:213], v[116:119]
	v_mfma_f32_16x16x32_bf16 v[104:107], v[188:191], v[218:221], v[104:107]
	v_mfma_f32_16x16x32_bf16 v[100:103], v[196:199], v[218:221], v[100:103]
	v_mfma_f32_16x16x32_bf16 v[88:91], v[188:191], v[226:229], v[88:91]
	v_mfma_f32_16x16x32_bf16 v[84:87], v[196:199], v[226:229], v[84:87]
	v_mfma_f32_16x16x32_bf16 v[72:75], v[188:191], v[234:237], v[72:75]
	v_mfma_f32_16x16x32_bf16 v[68:71], v[196:199], v[234:237], v[68:71]
	s_setprio 0
	s_barrier
	s_mov_b32 m0, s13
	v_lshl_add_u64 v[164:165], s[16:17], 0, v[142:143]
	s_add_u32 s10, s16, 0x18000
	ds_read_b128 v[206:209], v148 offset:16384
	ds_read_b128 v[210:213], v148 offset:17408
	ds_read_b128 v[214:217], v148 offset:18432
	ds_read_b128 v[218:221], v148 offset:19456
	ds_read_b128 v[222:225], v148 offset:20480
	ds_read_b128 v[226:229], v148 offset:21504
	ds_read_b128 v[230:233], v148 offset:22528
	ds_read_b128 v[234:237], v148 offset:23552
	global_load_lds_dwordx4 v[164:165], off
	v_lshl_add_u64 v[238:239], s[16:17], 0, v[146:147]
	s_mov_b32 m0, s31
	s_addc_u32 s11, s17, 0
	global_load_lds_dwordx4 v[238:239], off
	v_lshl_add_u64 v[240:241], s[10:11], 0, v[142:143]
	s_mov_b32 m0, s62
	v_lshl_add_u64 v[242:243], s[34:35], 0, v[144:145]
	global_load_lds_dwordx4 v[240:241], off
	v_lshl_add_u64 v[240:241], s[10:11], 0, v[146:147]
	s_mov_b32 m0, s63
	s_nop 0
	global_load_lds_dwordx4 v[240:241], off
	v_lshl_add_u64 v[240:241], s[34:35], 0, v[140:141]
	s_mov_b32 m0, s27
	s_nop 0
	global_load_lds_dwordx4 v[240:241], off
	s_mov_b32 m0, s64
	s_nop 0
	global_load_lds_dwordx4 v[242:243], off
	s_waitcnt vmcnt(8)
	s_waitcnt lgkmcnt(0)
	s_barrier
; #define G8_STAGE_A(bufoff, gbase, h_, nx_) do { if constexpr (Sched::GATHER) { unsigned vo_[2]; _Pragma("unroll") for (int q_ = 0; q_ < 2; ++q_) vo_[q_] = (nx_) ? gnxt[h_][q_] : goff[h_][q_]; G8_STAGE(bufoff, gbase, vo_); } \
;         else { G8_STAGE(bufoff, (gbase) + ((h_) ? hstepA : (size_t)0), voffA); } } while (0)
; #define G8_XLDA(b, h) do { if constexpr (Epi::FP8) { G8_LD8(A8, G8_SA(b, h) + aoff, 4); } else { G8_LDA(At, b, h); } } while (0)
; #define G8_XLDB0(b, h) do { if constexpr (Epi::FP8) { G8_LD8(B08, G8_SB(b, h) + boff, 2); } else { G8_LDB(B0, b, h); } } while (0)
; #define G8_XLDB1(b, h) do { if constexpr (Epi::FP8) { G8_LD8(B18, G8_SB(b, h) + boff, 2); } else { G8_LDB(B1, b, h); } } while (0)
; #define G8_MM0(ai, bj) do { if constexpr (Epi::FP8) { G8_MMA8(ai, bj, A8, B08); } else { G8_MMA(ai, bj, At, B0); } } while (0)
; #define G8_MM1(ai, bj) do { if constexpr (Epi::FP8) { G8_MMA8(ai, bj, A8, B18); } else { G8_MMA(ai, bj, At, B1); } } while (0)
; #define G8_WAIT_L(n) asm volatile("s_waitcnt lgkmcnt(" #n ")" ::: "memory")
; #define G8_BAR __builtin_amdgcn_s_barrier()
; #define G8_SCHED __builtin_amdgcn_sched_barrier(0)
; #define G8_WAIT_VK do { if constexpr (Epi::HALFN) { G8_WAIT_V(6); } else { G8_WAIT_V(8); } } while (0)
; template <int lda, int ldb, class Epi, class Sched>
; __device__ __forceinline__ void gemm_phase(LAS unsigned char* lds, int wid, int lane, const char* baseA, const char* baseB, const Sched& S, const Epi& E) {
;     ...
;             G8_WAIT_VK; G8_WAIT_L(0); G8_BAR; G8_MM0(1, 0); if constexpr (!Epi::HALFN) { G8_MM1(1, 1); } G8_BAR; G8_SCHED;
;             G8_XLDB0(1, 0); if constexpr (!Epi::HALFN) { G8_XLDB1(1, 1); } G8_SCHED; G8_XLDA(1, 0); G8_STAGE_A(G8_SA(0, 1), a2, 1, last);
;             G8_WAIT_VK; G8_WAIT_L(0); G8_BAR; G8_MM0(0, 0); if constexpr (!Epi::HALFN) { G8_MM1(0, 1); } G8_BAR; G8_SCHED;
	s_setprio 1
	s_waitcnt lgkmcnt(0)
	v_mfma_f32_16x16x32_bf16 v[64:67], v[132:135], v[206:209], v[64:67]
	v_mfma_f32_16x16x32_bf16 v[60:63], v[152:155], v[206:209], v[60:63]
	v_mfma_f32_16x16x32_bf16 v[48:51], v[132:135], v[214:217], v[48:51]
	v_mfma_f32_16x16x32_bf16 v[44:47], v[152:155], v[214:217], v[44:47]
	v_mfma_f32_16x16x32_bf16 v[32:35], v[132:135], v[222:225], v[32:35]
	v_mfma_f32_16x16x32_bf16 v[26:29], v[152:155], v[222:225], v[26:29]
	v_mfma_f32_16x16x32_bf16 v[14:17], v[132:135], v[230:233], v[14:17]
	v_mfma_f32_16x16x32_bf16 v[10:13], v[152:155], v[230:233], v[10:13]
	v_mfma_f32_16x16x32_bf16 v[64:67], v[136:139], v[210:213], v[64:67]
	v_mfma_f32_16x16x32_bf16 v[60:63], v[178:181], v[210:213], v[60:63]
	v_mfma_f32_16x16x32_bf16 v[48:51], v[136:139], v[218:221], v[48:51]
	v_mfma_f32_16x16x32_bf16 v[44:47], v[178:181], v[218:221], v[44:47]
	v_mfma_f32_16x16x32_bf16 v[32:35], v[136:139], v[226:229], v[32:35]
	v_mfma_f32_16x16x32_bf16 v[26:29], v[178:181], v[226:229], v[26:29]
	v_mfma_f32_16x16x32_bf16 v[14:17], v[136:139], v[234:237], v[14:17]
	v_mfma_f32_16x16x32_bf16 v[10:13], v[178:181], v[234:237], v[10:13]
	s_setprio 0
	s_setprio 1
	v_mfma_f32_16x16x32_bf16 v[56:59], v[184:187], v[206:209], v[56:59]
	v_mfma_f32_16x16x32_bf16 v[52:55], v[192:195], v[206:209], v[52:55]
	v_mfma_f32_16x16x32_bf16 v[40:43], v[184:187], v[214:217], v[40:43]
	v_mfma_f32_16x16x32_bf16 v[36:39], v[192:195], v[214:217], v[36:39]
	v_mfma_f32_16x16x32_bf16 v[22:25], v[184:187], v[222:225], v[22:25]
	v_mfma_f32_16x16x32_bf16 v[18:21], v[192:195], v[222:225], v[18:21]
	v_mfma_f32_16x16x32_bf16 v[6:9], v[184:187], v[230:233], v[6:9]
	v_mfma_f32_16x16x32_bf16 v[0:3], v[192:195], v[230:233], v[0:3]
	v_mfma_f32_16x16x32_bf16 v[56:59], v[188:191], v[210:213], v[56:59]
	v_mfma_f32_16x16x32_bf16 v[52:55], v[196:199], v[210:213], v[52:55]
	v_mfma_f32_16x16x32_bf16 v[40:43], v[188:191], v[218:221], v[40:43]
	v_mfma_f32_16x16x32_bf16 v[36:39], v[196:199], v[218:221], v[36:39]
	v_mfma_f32_16x16x32_bf16 v[22:25], v[188:191], v[226:229], v[22:25]
	v_mfma_f32_16x16x32_bf16 v[18:21], v[196:199], v[226:229], v[18:21]
	v_mfma_f32_16x16x32_bf16 v[6:9], v[188:191], v[234:237], v[6:9]
	v_mfma_f32_16x16x32_bf16 v[0:3], v[196:199], v[234:237], v[0:3]
	s_setprio 0
	s_barrier
	v_add_u32_e32 v5, 0x18000, v151
	ds_read_b128 v[132:135], v5
	ds_read_b128 v[136:139], v5 offset:1024
	ds_read_b128 v[152:155], v5 offset:2048
	ds_read_b128 v[178:181], v5 offset:3072
	v_add_u32_e32 v5, 0x1c000, v151
	ds_read_b128 v[184:187], v5
	ds_read_b128 v[188:191], v5 offset:1024
	ds_read_b128 v[192:195], v5 offset:2048
	ds_read_b128 v[196:199], v5 offset:3072
	s_add_u32 s10, s34, 0xb0000
	s_addc_u32 s11, s35, 0
	s_mov_b32 m0, s65
	v_lshl_add_u64 v[244:245], s[10:11], 0, v[140:141]
	ds_read_b128 v[206:209], v148 offset:32768
	ds_read_b128 v[210:213], v148 offset:33792
	ds_read_b128 v[214:217], v148 offset:34816
	ds_read_b128 v[218:221], v148 offset:35840
	ds_read_b128 v[222:225], v148 offset:36864
	ds_read_b128 v[226:229], v148 offset:37888
	ds_read_b128 v[230:233], v148 offset:38912
	ds_read_b128 v[234:237], v148 offset:39936
	global_load_lds_dwordx4 v[244:245], off
	v_lshl_add_u64 v[244:245], s[10:11], 0, v[144:145]
	s_mov_b32 m0, s66
	s_nop 0
	global_load_lds_dwordx4 v[244:245], off
	s_waitcnt vmcnt(8)
	s_waitcnt lgkmcnt(0)
	s_barrier
	s_setprio 1
	s_waitcnt lgkmcnt(0)
	v_mfma_f32_16x16x32_bf16 v[128:131], v[132:135], v[206:209], v[128:131]
	v_mfma_f32_16x16x32_bf16 v[124:127], v[152:155], v[206:209], v[124:127]
	v_mfma_f32_16x16x32_bf16 v[112:115], v[132:135], v[214:217], v[112:115]
	v_mfma_f32_16x16x32_bf16 v[108:111], v[152:155], v[214:217], v[108:111]
	v_mfma_f32_16x16x32_bf16 v[96:99], v[132:135], v[222:225], v[96:99]
	v_mfma_f32_16x16x32_bf16 v[92:95], v[152:155], v[222:225], v[92:95]
	v_mfma_f32_16x16x32_bf16 v[80:83], v[132:135], v[230:233], v[80:83]
	v_mfma_f32_16x16x32_bf16 v[76:79], v[152:155], v[230:233], v[76:79]
	v_mfma_f32_16x16x32_bf16 v[128:131], v[136:139], v[210:213], v[128:131]
	v_mfma_f32_16x16x32_bf16 v[124:127], v[178:181], v[210:213], v[124:127]
	v_mfma_f32_16x16x32_bf16 v[112:115], v[136:139], v[218:221], v[112:115]
	v_mfma_f32_16x16x32_bf16 v[108:111], v[178:181], v[218:221], v[108:111]
	v_mfma_f32_16x16x32_bf16 v[96:99], v[136:139], v[226:229], v[96:99]
	v_mfma_f32_16x16x32_bf16 v[92:95], v[178:181], v[226:229], v[92:95]
	v_mfma_f32_16x16x32_bf16 v[80:83], v[136:139], v[234:237], v[80:83]
	v_mfma_f32_16x16x32_bf16 v[76:79], v[178:181], v[234:237], v[76:79]
	s_setprio 0
	s_setprio 1
	v_mfma_f32_16x16x32_bf16 v[120:123], v[184:187], v[206:209], v[120:123]
	v_mfma_f32_16x16x32_bf16 v[116:119], v[192:195], v[206:209], v[116:119]
	v_mfma_f32_16x16x32_bf16 v[104:107], v[184:187], v[214:217], v[104:107]
	v_mfma_f32_16x16x32_bf16 v[100:103], v[192:195], v[214:217], v[100:103]
	v_mfma_f32_16x16x32_bf16 v[88:91], v[184:187], v[222:225], v[88:91]
	v_mfma_f32_16x16x32_bf16 v[84:87], v[192:195], v[222:225], v[84:87]
	v_mfma_f32_16x16x32_bf16 v[72:75], v[184:187], v[230:233], v[72:75]
	v_mfma_f32_16x16x32_bf16 v[68:71], v[192:195], v[230:233], v[68:71]
	v_mfma_f32_16x16x32_bf16 v[120:123], v[188:191], v[210:213], v[120:123]
	v_mfma_f32_16x16x32_bf16 v[116:119], v[196:199], v[210:213], v[116:119]
	v_mfma_f32_16x16x32_bf16 v[104:107], v[188:191], v[218:221], v[104:107]
	v_mfma_f32_16x16x32_bf16 v[100:103], v[196:199], v[218:221], v[100:103]
	v_mfma_f32_16x16x32_bf16 v[88:91], v[188:191], v[226:229], v[88:91]
	v_mfma_f32_16x16x32_bf16 v[84:87], v[196:199], v[226:229], v[84:87]
	v_mfma_f32_16x16x32_bf16 v[72:75], v[188:191], v[234:237], v[72:75]
	v_mfma_f32_16x16x32_bf16 v[68:71], v[196:199], v[234:237], v[68:71]
	s_setprio 0
	s_barrier
; #define G8_STAGE(bufoff, gbase, voff) do { _Pragma("unroll") for (int _i = 0; _i < 2; ++_i) \
;         __builtin_amdgcn_global_load_lds((const unsigned*)((const char*)(gbase) + (voff)[_i]), (LAS unsigned*)(lds + (bufoff) + ldsw + _i * 8192), 16, 0, 0); } while (0)
; #define G8_STAGE_A(bufoff, gbase, h_, nx_) do { if constexpr (Sched::GATHER) { unsigned vo_[2]; _Pragma("unroll") for (int q_ = 0; q_ < 2; ++q_) vo_[q_] = (nx_) ? gnxt[h_][q_] : goff[h_][q_]; G8_STAGE(bufoff, gbase, vo_); } \
;         else { G8_STAGE(bufoff, (gbase) + ((h_) ? hstepA : (size_t)0), voffA); } } while (0)
; #define G8_XLDA(b, h) do { if constexpr (Epi::FP8) { G8_LD8(A8, G8_SA(b, h) + aoff, 4); } else { G8_LDA(At, b, h); } } while (0)
; #define G8_MM0(ai, bj) do { if constexpr (Epi::FP8) { G8_MMA8(ai, bj, A8, B08); } else { G8_MMA(ai, bj, At, B0); } } while (0)
; #define G8_MM1(ai, bj) do { if constexpr (Epi::FP8) { G8_MMA8(ai, bj, A8, B18); } else { G8_MMA(ai, bj, At, B1); } } while (0)
; #define G8_WAIT_L(n) asm volatile("s_waitcnt lgkmcnt(" #n ")" ::: "memory")
; #define G8_BAR __builtin_amdgcn_s_barrier()
; #define G8_SCHED __builtin_amdgcn_sched_barrier(0)
; #define G8_WAIT_VK do { if constexpr (Epi::HALFN) { G8_WAIT_V(6); } else { G8_WAIT_V(8); } } while (0)
; template <int lda, int ldb, class Epi, class Sched>
; __device__ __forceinline__ void gemm_phase(LAS unsigned char* lds, int wid, int lane, const char* baseA, const char* baseB, const Sched& S, const Epi& E) {
;     ...
;         for (int t = 0; t < nt; t += 2) {
;     ...
;             G8_XLDA(1, 1); G8_STAGE(G8_SB(1, 0), b3, voffB); if constexpr (!Epi::HALFN) { G8_STAGE(G8_SB(1, 1), b3 + hstepB, voffB); } G8_STAGE_A(G8_SA(1, 0), a3, 0, last);
;             G8_WAIT_VK; G8_WAIT_L(0); G8_BAR; G8_MM0(1, 0); if constexpr (!Epi::HALFN) { G8_MM1(1, 1); } G8_BAR; G8_SCHED;
;         }
	s_mov_b32 m0, s68
	v_lshl_add_u64 v[164:165], v[164:165], 0, s[22:23]
	s_add_u32 s10, s16, 0x18080
	ds_read_b128 v[206:209], v148 offset:49152
	ds_read_b128 v[210:213], v148 offset:50176
	ds_read_b128 v[214:217], v148 offset:51200
	ds_read_b128 v[218:221], v148 offset:52224
	ds_read_b128 v[222:225], v148 offset:53248
	ds_read_b128 v[226:229], v148 offset:54272
	ds_read_b128 v[230:233], v148 offset:55296
	ds_read_b128 v[234:237], v148 offset:56320
	global_load_lds_dwordx4 v[164:165], off
	v_lshl_add_u64 v[164:165], v[238:239], 0, s[22:23]
	s_mov_b32 m0, s69
	s_addc_u32 s11, s17, 0
	global_load_lds_dwordx4 v[164:165], off
	v_lshl_add_u64 v[164:165], s[10:11], 0, v[142:143]
	s_mov_b32 m0, s72
	s_nop 0
	global_load_lds_dwordx4 v[164:165], off
	v_lshl_add_u64 v[164:165], s[10:11], 0, v[146:147]
	s_mov_b32 m0, s73
	s_nop 0
	global_load_lds_dwordx4 v[164:165], off
	v_lshl_add_u64 v[164:165], v[240:241], 0, s[22:23]
	s_mov_b32 m0, s70
	s_nop 0
	global_load_lds_dwordx4 v[164:165], off
	v_lshl_add_u64 v[164:165], v[242:243], 0, s[22:23]
	s_mov_b32 m0, s71
	s_nop 0
	global_load_lds_dwordx4 v[164:165], off
	s_waitcnt vmcnt(8)
	s_waitcnt lgkmcnt(0)
	s_barrier
	s_setprio 1
	s_waitcnt lgkmcnt(0)
	v_mfma_f32_16x16x32_bf16 v[64:67], v[132:135], v[206:209], v[64:67]
	v_mfma_f32_16x16x32_bf16 v[60:63], v[152:155], v[206:209], v[60:63]
	v_mfma_f32_16x16x32_bf16 v[48:51], v[132:135], v[214:217], v[48:51]
	v_mfma_f32_16x16x32_bf16 v[44:47], v[152:155], v[214:217], v[44:47]
	v_mfma_f32_16x16x32_bf16 v[32:35], v[132:135], v[222:225], v[32:35]
	v_mfma_f32_16x16x32_bf16 v[26:29], v[152:155], v[222:225], v[26:29]
	v_mfma_f32_16x16x32_bf16 v[14:17], v[132:135], v[230:233], v[14:17]
	v_mfma_f32_16x16x32_bf16 v[10:13], v[152:155], v[230:233], v[10:13]
	v_mfma_f32_16x16x32_bf16 v[64:67], v[136:139], v[210:213], v[64:67]
	v_mfma_f32_16x16x32_bf16 v[60:63], v[178:181], v[210:213], v[60:63]
	v_mfma_f32_16x16x32_bf16 v[48:51], v[136:139], v[218:221], v[48:51]
	v_mfma_f32_16x16x32_bf16 v[44:47], v[178:181], v[218:221], v[44:47]
	v_mfma_f32_16x16x32_bf16 v[32:35], v[136:139], v[226:229], v[32:35]
	v_mfma_f32_16x16x32_bf16 v[26:29], v[178:181], v[226:229], v[26:29]
	v_mfma_f32_16x16x32_bf16 v[14:17], v[136:139], v[234:237], v[14:17]
	v_mfma_f32_16x16x32_bf16 v[10:13], v[178:181], v[234:237], v[10:13]
	s_setprio 0
	s_setprio 1
	v_mfma_f32_16x16x32_bf16 v[56:59], v[184:187], v[206:209], v[56:59]
	v_mfma_f32_16x16x32_bf16 v[52:55], v[192:195], v[206:209], v[52:55]
	v_mfma_f32_16x16x32_bf16 v[40:43], v[184:187], v[214:217], v[40:43]
	v_mfma_f32_16x16x32_bf16 v[36:39], v[192:195], v[214:217], v[36:39]
	v_mfma_f32_16x16x32_bf16 v[22:25], v[184:187], v[222:225], v[22:25]
	v_mfma_f32_16x16x32_bf16 v[18:21], v[192:195], v[222:225], v[18:21]
	v_mfma_f32_16x16x32_bf16 v[6:9], v[184:187], v[230:233], v[6:9]
	v_mfma_f32_16x16x32_bf16 v[0:3], v[192:195], v[230:233], v[0:3]
	v_mfma_f32_16x16x32_bf16 v[56:59], v[188:191], v[210:213], v[56:59]
	v_mfma_f32_16x16x32_bf16 v[52:55], v[196:199], v[210:213], v[52:55]
	v_mfma_f32_16x16x32_bf16 v[40:43], v[188:191], v[218:221], v[40:43]
	v_mfma_f32_16x16x32_bf16 v[36:39], v[196:199], v[218:221], v[36:39]
	v_mfma_f32_16x16x32_bf16 v[22:25], v[188:191], v[226:229], v[22:25]
	v_mfma_f32_16x16x32_bf16 v[18:21], v[196:199], v[226:229], v[18:21]
	v_mfma_f32_16x16x32_bf16 v[6:9], v[188:191], v[234:237], v[6:9]
	v_mfma_f32_16x16x32_bf16 v[0:3], v[196:199], v[234:237], v[0:3]
	s_setprio 0
	s_add_u32 s83, s83, 0x100
	s_addc_u32 s84, s84, 0
	s_cmp_ge_i32 s85, s20
	s_mov_b64 s[10:11], s[14:15]
	s_mov_b32 s16, s85
	s_barrier
	s_cbranch_scc0 .LBB0_533
	s_and_b64 vcc, exec, s[36:37]
	s_cbranch_vccz .LBB0_536

; #define G8_STAGE(bufoff, gbase, voff) do { _Pragma("unroll") for (int _i = 0; _i < 2; ++_i) \
;         __builtin_amdgcn_global_load_lds((const unsigned*)((const char*)(gbase) + (voff)[_i]), (LAS unsigned*)(lds + (bufoff) + ldsw + _i * 8192), 16, 0, 0); } while (0)
; #define G8_STAGE_A(bufoff, gbase, h_, nx_) do { if constexpr (Sched::GATHER) { unsigned vo_[2]; _Pragma("unroll") for (int q_ = 0; q_ < 2; ++q_) vo_[q_] = (nx_) ? gnxt[h_][q_] : goff[h_][q_]; G8_STAGE(bufoff, gbase, vo_); } \
;         else { G8_STAGE(bufoff, (gbase) + ((h_) ? hstepA : (size_t)0), voffA); } } while (0)
; #define G8_XLDA(b, h) do { if constexpr (Epi::FP8) { G8_LD8(A8, G8_SA(b, h) + aoff, 4); } else { G8_LDA(At, b, h); } } while (0)
; #define G8_XLDB0(b, h) do { if constexpr (Epi::FP8) { G8_LD8(B08, G8_SB(b, h) + boff, 2); } else { G8_LDB(B0, b, h); } } while (0)
; #define G8_XLDB1(b, h) do { if constexpr (Epi::FP8) { G8_LD8(B18, G8_SB(b, h) + boff, 2); } else { G8_LDB(B1, b, h); } } while (0)
; #define G8_MM0(ai, bj) do { if constexpr (Epi::FP8) { G8_MMA8(ai, bj, A8, B08); } else { G8_MMA(ai, bj, At, B0); } } while (0)
; #define G8_MM1(ai, bj) do { if constexpr (Epi::FP8) { G8_MMA8(ai, bj, A8, B18); } else { G8_MMA(ai, bj, At, B1); } } while (0)
; template <int lda, int ldb, class Epi, class Sched>
; __device__ __forceinline__ void gemm_phase(LAS unsigned char* lds, int wid, int lane, const char* baseA, const char* baseB, const Sched& S, const Epi& E) {
;     ...
;         for (int t = 0; t < nt; t += 2) {
;             const bool last = (t == nt - 2);
;             const char* a1 = cA + (size_t)(t + 1) * kstep;
;             const char* a2 = last ? nA : cA + (size_t)(t + 2) * kstep; const char* b2 = last ? nB : cB + (size_t)(t + 2) * kstep;
;             const char* a3 = a2 + kstep; const char* b3 = b2 + kstep;
;     ...
;             G8_XLDB0(0, 0); if constexpr (!Epi::HALFN) { G8_XLDB1(0, 1); } G8_SCHED; G8_XLDA(0, 0); G8_STAGE_A(G8_SA(1, 1), a1, 1, false);
;             G8_WAIT_VK; G8_WAIT_L(0); G8_BAR; G8_MM0(0, 0); if constexpr (!Epi::HALFN) { G8_MM1(0, 1); } G8_BAR; G8_SCHED;
;             G8_XLDA(0, 1); G8_STAGE(G8_SB(0, 0), b2, voffB); if constexpr (!Epi::HALFN) { G8_STAGE(G8_SB(0, 1), b2 + hstepB, voffB); } G8_STAGE_A(G8_SA(0, 0), a2, 0, last);
;             G8_WAIT_VK; G8_WAIT_L(0); G8_BAR; G8_MM0(1, 0); if constexpr (!Epi::HALFN) { G8_MM1(1, 1); } G8_BAR; G8_SCHED;
.LBB0_1085:
	ds_read_b128 v[4:7], v177
	ds_read_b128 v[8:11], v178
	ds_read_b128 v[0:3], v30
	ds_read_b128 v[184:187], v148
	ds_read_b128 v[12:15], v179
	ds_read_b128 v[188:191], v180
	ds_read_b128 v[192:195], v181
	ds_read_b128 v[196:199], v205
	s_add_i32 s83, s54, 2
	s_add_u32 s55, s52, 0xfffe0080
	s_addc_u32 s56, s53, -1
	s_cmp_eq_u32 s80, s54
	s_cselect_b32 s54, s79, s81
	s_cselect_b32 s57, s21, s56
	s_cselect_b32 s56, s28, s55
	s_cselect_b32 s55, s29, s82
	v_lshl_add_u64 v[152:153], s[52:53], 0, v[166:167]
	s_add_i32 m0, s27, 0xc000
	ds_read_b128 v[168:171], v212
	ds_read_b128 v[172:175], v212 offset:1024
	ds_read_b128 v[214:217], v212 offset:2048
	ds_read_b128 v[218:221], v212 offset:3072
	ds_read_b128 v[222:225], v212 offset:4096
	ds_read_b128 v[226:229], v212 offset:5120
	ds_read_b128 v[230:233], v212 offset:6144
	ds_read_b128 v[234:237], v212 offset:7168
	global_load_lds_dwordx4 v[152:153], off
	v_lshl_add_u64 v[152:153], s[52:53], 0, v[164:165]
	s_add_i32 m0, s27, 0xe000
	s_nop 0
	global_load_lds_dwordx4 v[152:153], off
	s_waitcnt vmcnt(8)
	s_waitcnt lgkmcnt(0)
	s_barrier
	s_setprio 1
	s_waitcnt lgkmcnt(0)
	v_mfma_scale_f32_16x16x128_f8f6f4 v[144:147], v[0:7], v[168:175], v[144:147], v213, v213 op_sel_hi:[0,0,0]
	v_mfma_scale_f32_16x16x128_f8f6f4 v[140:143], v[8:15], v[168:175], v[140:143], v213, v213 op_sel_hi:[0,0,0]
	v_mfma_scale_f32_16x16x128_f8f6f4 v[136:139], v[0:7], v[214:221], v[136:139], v213, v213 op_sel_hi:[0,0,0]
	v_mfma_scale_f32_16x16x128_f8f6f4 v[132:135], v[8:15], v[214:221], v[132:135], v213, v213 op_sel_hi:[0,0,0]
	v_mfma_scale_f32_16x16x128_f8f6f4 v[128:131], v[0:7], v[222:229], v[128:131], v213, v213 op_sel_hi:[0,0,0]
	v_mfma_scale_f32_16x16x128_f8f6f4 v[124:127], v[8:15], v[222:229], v[124:127], v213, v213 op_sel_hi:[0,0,0]
	v_mfma_scale_f32_16x16x128_f8f6f4 v[120:123], v[0:7], v[230:237], v[120:123], v213, v213 op_sel_hi:[0,0,0]
	v_mfma_scale_f32_16x16x128_f8f6f4 v[116:119], v[8:15], v[230:237], v[116:119], v213, v213 op_sel_hi:[0,0,0]
	s_setprio 0
	s_setprio 1
	v_mfma_scale_f32_16x16x128_f8f6f4 v[80:83], v[184:191], v[168:175], v[80:83], v213, v213 op_sel_hi:[0,0,0]
	v_mfma_scale_f32_16x16x128_f8f6f4 v[76:79], v[192:199], v[168:175], v[76:79], v213, v213 op_sel_hi:[0,0,0]
	v_mfma_scale_f32_16x16x128_f8f6f4 v[72:75], v[184:191], v[214:221], v[72:75], v213, v213 op_sel_hi:[0,0,0]
	v_mfma_scale_f32_16x16x128_f8f6f4 v[68:71], v[192:199], v[214:221], v[68:71], v213, v213 op_sel_hi:[0,0,0]
	v_mfma_scale_f32_16x16x128_f8f6f4 v[64:67], v[184:191], v[222:229], v[64:67], v213, v213 op_sel_hi:[0,0,0]
	v_mfma_scale_f32_16x16x128_f8f6f4 v[60:63], v[192:199], v[222:229], v[60:63], v213, v213 op_sel_hi:[0,0,0]
	v_mfma_scale_f32_16x16x128_f8f6f4 v[56:59], v[184:191], v[230:237], v[56:59], v213, v213 op_sel_hi:[0,0,0]
	v_mfma_scale_f32_16x16x128_f8f6f4 v[52:55], v[192:199], v[230:237], v[52:55], v213, v213 op_sel_hi:[0,0,0]
	s_setprio 0
	s_barrier
	s_mov_b32 m0, s60
	v_lshl_add_u64 v[168:169], s[54:55], 0, v[160:161]
	s_add_u32 s84, s54, 0x20000
	ds_read_b128 v[214:217], v212 offset:16384
	ds_read_b128 v[218:221], v212 offset:17408
	ds_read_b128 v[222:225], v212 offset:18432
	ds_read_b128 v[226:229], v212 offset:19456
	ds_read_b128 v[230:233], v212 offset:20480
	ds_read_b128 v[234:237], v212 offset:21504
	ds_read_b128 v[238:241], v212 offset:22528
	ds_read_b128 v[242:245], v212 offset:23552
	global_load_lds_dwordx4 v[168:169], off
	v_lshl_add_u64 v[170:171], s[54:55], 0, v[156:157]
	s_mov_b32 m0, s61
	s_addc_u32 s85, s55, 0
	global_load_lds_dwordx4 v[170:171], off
	v_lshl_add_u64 v[152:153], s[84:85], 0, v[160:161]
	s_mov_b32 m0, s62
	v_lshl_add_u64 v[172:173], s[56:57], 0, v[162:163]
	global_load_lds_dwordx4 v[152:153], off
	v_lshl_add_u64 v[152:153], s[84:85], 0, v[156:157]
	s_mov_b32 m0, s63
	v_lshl_add_u64 v[174:175], s[56:57], 0, v[158:159]
	global_load_lds_dwordx4 v[152:153], off
	s_mov_b32 m0, s27
	s_nop 0
	global_load_lds_dwordx4 v[172:173], off
	s_mov_b32 m0, s64
	s_nop 0
	global_load_lds_dwordx4 v[174:175], off
	s_waitcnt vmcnt(8)
	s_waitcnt lgkmcnt(0)
	s_barrier
	s_setprio 1
	s_waitcnt lgkmcnt(0)
	v_mfma_scale_f32_16x16x128_f8f6f4 v[112:115], v[0:7], v[214:221], v[112:115], v213, v213 op_sel_hi:[0,0,0]
	v_mfma_scale_f32_16x16x128_f8f6f4 v[108:111], v[8:15], v[214:221], v[108:111], v213, v213 op_sel_hi:[0,0,0]
	v_mfma_scale_f32_16x16x128_f8f6f4 v[104:107], v[0:7], v[222:229], v[104:107], v213, v213 op_sel_hi:[0,0,0]
	v_mfma_scale_f32_16x16x128_f8f6f4 v[100:103], v[8:15], v[222:229], v[100:103], v213, v213 op_sel_hi:[0,0,0]
	v_mfma_scale_f32_16x16x128_f8f6f4 v[96:99], v[0:7], v[230:237], v[96:99], v213, v213 op_sel_hi:[0,0,0]
	v_mfma_scale_f32_16x16x128_f8f6f4 v[92:95], v[8:15], v[230:237], v[92:95], v213, v213 op_sel_hi:[0,0,0]
	v_mfma_scale_f32_16x16x128_f8f6f4 v[88:91], v[0:7], v[238:245], v[88:91], v213, v213 op_sel_hi:[0,0,0]
	v_mfma_scale_f32_16x16x128_f8f6f4 v[84:87], v[8:15], v[238:245], v[84:87], v213, v213 op_sel_hi:[0,0,0]
	s_setprio 0
	s_setprio 1
	v_mfma_scale_f32_16x16x128_f8f6f4 v[48:51], v[184:191], v[214:221], v[48:51], v213, v213 op_sel_hi:[0,0,0]
	v_mfma_scale_f32_16x16x128_f8f6f4 v[44:47], v[192:199], v[214:221], v[44:47], v213, v213 op_sel_hi:[0,0,0]
	v_mfma_scale_f32_16x16x128_f8f6f4 v[40:43], v[184:191], v[222:229], v[40:43], v213, v213 op_sel_hi:[0,0,0]
	v_mfma_scale_f32_16x16x128_f8f6f4 v[36:39], v[192:199], v[222:229], v[36:39], v213, v213 op_sel_hi:[0,0,0]
	v_mfma_scale_f32_16x16x128_f8f6f4 v[32:35], v[184:191], v[230:237], v[32:35], v213, v213 op_sel_hi:[0,0,0]
	v_mfma_scale_f32_16x16x128_f8f6f4 v[26:29], v[192:199], v[230:237], v[26:29], v213, v213 op_sel_hi:[0,0,0]
	v_mfma_scale_f32_16x16x128_f8f6f4 v[22:25], v[184:191], v[238:245], v[22:25], v213, v213 op_sel_hi:[0,0,0]
	v_mfma_scale_f32_16x16x128_f8f6f4 v[18:21], v[192:199], v[238:245], v[18:21], v213, v213 op_sel_hi:[0,0,0]
	s_setprio 0
	s_barrier
; #define G8_STAGE(bufoff, gbase, voff) do { _Pragma("unroll") for (int _i = 0; _i < 2; ++_i) \
;         __builtin_amdgcn_global_load_lds((const unsigned*)((const char*)(gbase) + (voff)[_i]), (LAS unsigned*)(lds + (bufoff) + ldsw + _i * 8192), 16, 0, 0); } while (0)
; #define G8_STAGE_A(bufoff, gbase, h_, nx_) do { if constexpr (Sched::GATHER) { unsigned vo_[2]; _Pragma("unroll") for (int q_ = 0; q_ < 2; ++q_) vo_[q_] = (nx_) ? gnxt[h_][q_] : goff[h_][q_]; G8_STAGE(bufoff, gbase, vo_); } \
;         else { G8_STAGE(bufoff, (gbase) + ((h_) ? hstepA : (size_t)0), voffA); } } while (0)
; #define G8_XLDA(b, h) do { if constexpr (Epi::FP8) { G8_LD8(A8, G8_SA(b, h) + aoff, 4); } else { G8_LDA(At, b, h); } } while (0)
; #define G8_XLDB0(b, h) do { if constexpr (Epi::FP8) { G8_LD8(B08, G8_SB(b, h) + boff, 2); } else { G8_LDB(B0, b, h); } } while (0)
; #define G8_XLDB1(b, h) do { if constexpr (Epi::FP8) { G8_LD8(B18, G8_SB(b, h) + boff, 2); } else { G8_LDB(B1, b, h); } } while (0)
; #define G8_MM0(ai, bj) do { if constexpr (Epi::FP8) { G8_MMA8(ai, bj, A8, B08); } else { G8_MMA(ai, bj, At, B0); } } while (0)
; #define G8_MM1(ai, bj) do { if constexpr (Epi::FP8) { G8_MMA8(ai, bj, A8, B18); } else { G8_MMA(ai, bj, At, B1); } } while (0)
; #define G8_WAIT_L(n) asm volatile("s_waitcnt lgkmcnt(" #n ")" ::: "memory")
; #define G8_BAR __builtin_amdgcn_s_barrier()
; #define G8_SCHED __builtin_amdgcn_sched_barrier(0)
; #define G8_WAIT_VK do { if constexpr (Epi::HALFN) { G8_WAIT_V(6); } else { G8_WAIT_V(8); } } while (0)
; template <int lda, int ldb, class Epi, class Sched>
; __device__ __forceinline__ void gemm_phase(LAS unsigned char* lds, int wid, int lane, const char* baseA, const char* baseB, const Sched& S, const Epi& E) {
;     ...
;             G8_XLDB0(1, 0); if constexpr (!Epi::HALFN) { G8_XLDB1(1, 1); } G8_SCHED; G8_XLDA(1, 0); G8_STAGE_A(G8_SA(0, 1), a2, 1, last);
;             G8_WAIT_VK; G8_WAIT_L(0); G8_BAR; G8_MM0(0, 0); if constexpr (!Epi::HALFN) { G8_MM1(0, 1); } G8_BAR; G8_SCHED;
;             G8_XLDA(1, 1); G8_STAGE(G8_SB(1, 0), b3, voffB); if constexpr (!Epi::HALFN) { G8_STAGE(G8_SB(1, 1), b3 + hstepB, voffB); } G8_STAGE_A(G8_SA(1, 0), a3, 0, last);
;             G8_WAIT_VK; G8_WAIT_L(0); G8_BAR; G8_MM0(1, 0); if constexpr (!Epi::HALFN) { G8_MM1(1, 1); } G8_BAR; G8_SCHED;
;         }
	ds_read_b128 v[12:15], v206
	ds_read_b128 v[184:187], v207
	ds_read_b128 v[8:11], v151
	ds_read_b128 v[0:3], v176
	ds_read_b128 v[188:191], v208
	ds_read_b128 v[4:7], v209
	ds_read_b128 v[192:195], v210
	ds_read_b128 v[196:199], v211
	s_add_u32 s56, s56, 0x20000
	s_addc_u32 s57, s57, 0
	s_mov_b32 m0, s65
	v_lshl_add_u64 v[152:153], s[56:57], 0, v[162:163]
	ds_read_b128 v[214:217], v212 offset:32768
	ds_read_b128 v[218:221], v212 offset:33792
	ds_read_b128 v[222:225], v212 offset:34816
	ds_read_b128 v[226:229], v212 offset:35840
	ds_read_b128 v[230:233], v212 offset:36864
	ds_read_b128 v[234:237], v212 offset:37888
	ds_read_b128 v[238:241], v212 offset:38912
	ds_read_b128 v[242:245], v212 offset:39936
	global_load_lds_dwordx4 v[152:153], off
	v_lshl_add_u64 v[152:153], s[56:57], 0, v[158:159]
	s_mov_b32 m0, s66
	s_nop 0
	global_load_lds_dwordx4 v[152:153], off
	s_waitcnt vmcnt(8)
	s_waitcnt lgkmcnt(0)
	s_barrier
	s_setprio 1
	s_waitcnt lgkmcnt(0)
	v_mfma_scale_f32_16x16x128_f8f6f4 v[144:147], v[8:15], v[214:221], v[144:147], v213, v213 op_sel_hi:[0,0,0]
	v_mfma_scale_f32_16x16x128_f8f6f4 v[140:143], v[184:191], v[214:221], v[140:143], v213, v213 op_sel_hi:[0,0,0]
	v_mfma_scale_f32_16x16x128_f8f6f4 v[136:139], v[8:15], v[222:229], v[136:139], v213, v213 op_sel_hi:[0,0,0]
	v_mfma_scale_f32_16x16x128_f8f6f4 v[132:135], v[184:191], v[222:229], v[132:135], v213, v213 op_sel_hi:[0,0,0]
	v_mfma_scale_f32_16x16x128_f8f6f4 v[128:131], v[8:15], v[230:237], v[128:131], v213, v213 op_sel_hi:[0,0,0]
	v_mfma_scale_f32_16x16x128_f8f6f4 v[124:127], v[184:191], v[230:237], v[124:127], v213, v213 op_sel_hi:[0,0,0]
	v_mfma_scale_f32_16x16x128_f8f6f4 v[120:123], v[8:15], v[238:245], v[120:123], v213, v213 op_sel_hi:[0,0,0]
	v_mfma_scale_f32_16x16x128_f8f6f4 v[116:119], v[184:191], v[238:245], v[116:119], v213, v213 op_sel_hi:[0,0,0]
	s_setprio 0
	s_setprio 1
	v_mfma_scale_f32_16x16x128_f8f6f4 v[80:83], v[0:7], v[214:221], v[80:83], v213, v213 op_sel_hi:[0,0,0]
	v_mfma_scale_f32_16x16x128_f8f6f4 v[76:79], v[192:199], v[214:221], v[76:79], v213, v213 op_sel_hi:[0,0,0]
	v_mfma_scale_f32_16x16x128_f8f6f4 v[72:75], v[0:7], v[222:229], v[72:75], v213, v213 op_sel_hi:[0,0,0]
	v_mfma_scale_f32_16x16x128_f8f6f4 v[68:71], v[192:199], v[222:229], v[68:71], v213, v213 op_sel_hi:[0,0,0]
	v_mfma_scale_f32_16x16x128_f8f6f4 v[64:67], v[0:7], v[230:237], v[64:67], v213, v213 op_sel_hi:[0,0,0]
	v_mfma_scale_f32_16x16x128_f8f6f4 v[60:63], v[192:199], v[230:237], v[60:63], v213, v213 op_sel_hi:[0,0,0]
	v_mfma_scale_f32_16x16x128_f8f6f4 v[56:59], v[0:7], v[238:245], v[56:59], v213, v213 op_sel_hi:[0,0,0]
	v_mfma_scale_f32_16x16x128_f8f6f4 v[52:55], v[192:199], v[238:245], v[52:55], v213, v213 op_sel_hi:[0,0,0]
	s_setprio 0
	s_barrier
	s_mov_b32 m0, s67
	v_lshl_add_u64 v[152:153], v[168:169], 0, s[22:23]
	s_add_u32 s54, s54, 0x20080
	ds_read_b128 v[214:217], v212 offset:49152
	ds_read_b128 v[218:221], v212 offset:50176
	ds_read_b128 v[222:225], v212 offset:51200
	ds_read_b128 v[226:229], v212 offset:52224
	ds_read_b128 v[230:233], v212 offset:53248
	ds_read_b128 v[234:237], v212 offset:54272
	ds_read_b128 v[238:241], v212 offset:55296
	ds_read_b128 v[242:245], v212 offset:56320
	global_load_lds_dwordx4 v[152:153], off
	v_lshl_add_u64 v[152:153], v[170:171], 0, s[22:23]
	s_mov_b32 m0, s68
	s_addc_u32 s55, s55, 0
	global_load_lds_dwordx4 v[152:153], off
	v_lshl_add_u64 v[152:153], s[54:55], 0, v[160:161]
	s_mov_b32 m0, s71
	s_nop 0
	global_load_lds_dwordx4 v[152:153], off
	v_lshl_add_u64 v[152:153], s[54:55], 0, v[156:157]
	s_mov_b32 m0, s72
	s_nop 0
	global_load_lds_dwordx4 v[152:153], off
	v_lshl_add_u64 v[152:153], v[172:173], 0, s[22:23]
	s_mov_b32 m0, s69
	s_nop 0
	global_load_lds_dwordx4 v[152:153], off
	v_lshl_add_u64 v[152:153], v[174:175], 0, s[22:23]
	s_mov_b32 m0, s70
	s_nop 0
	global_load_lds_dwordx4 v[152:153], off
	s_waitcnt vmcnt(8)
	s_waitcnt lgkmcnt(0)
	s_barrier
	s_setprio 1
	s_waitcnt lgkmcnt(0)
	v_mfma_scale_f32_16x16x128_f8f6f4 v[112:115], v[8:15], v[214:221], v[112:115], v213, v213 op_sel_hi:[0,0,0]
	v_mfma_scale_f32_16x16x128_f8f6f4 v[108:111], v[184:191], v[214:221], v[108:111], v213, v213 op_sel_hi:[0,0,0]
	v_mfma_scale_f32_16x16x128_f8f6f4 v[104:107], v[8:15], v[222:229], v[104:107], v213, v213 op_sel_hi:[0,0,0]
	v_mfma_scale_f32_16x16x128_f8f6f4 v[100:103], v[184:191], v[222:229], v[100:103], v213, v213 op_sel_hi:[0,0,0]
	v_mfma_scale_f32_16x16x128_f8f6f4 v[96:99], v[8:15], v[230:237], v[96:99], v213, v213 op_sel_hi:[0,0,0]
	v_mfma_scale_f32_16x16x128_f8f6f4 v[92:95], v[184:191], v[230:237], v[92:95], v213, v213 op_sel_hi:[0,0,0]
	v_mfma_scale_f32_16x16x128_f8f6f4 v[88:91], v[8:15], v[238:245], v[88:91], v213, v213 op_sel_hi:[0,0,0]
	v_mfma_scale_f32_16x16x128_f8f6f4 v[84:87], v[184:191], v[238:245], v[84:87], v213, v213 op_sel_hi:[0,0,0]
	s_setprio 0
	s_setprio 1
	v_mfma_scale_f32_16x16x128_f8f6f4 v[48:51], v[0:7], v[214:221], v[48:51], v213, v213 op_sel_hi:[0,0,0]
	v_mfma_scale_f32_16x16x128_f8f6f4 v[44:47], v[192:199], v[214:221], v[44:47], v213, v213 op_sel_hi:[0,0,0]
	v_mfma_scale_f32_16x16x128_f8f6f4 v[40:43], v[0:7], v[222:229], v[40:43], v213, v213 op_sel_hi:[0,0,0]
	v_mfma_scale_f32_16x16x128_f8f6f4 v[36:39], v[192:199], v[222:229], v[36:39], v213, v213 op_sel_hi:[0,0,0]
	v_mfma_scale_f32_16x16x128_f8f6f4 v[32:35], v[0:7], v[230:237], v[32:35], v213, v213 op_sel_hi:[0,0,0]
	v_mfma_scale_f32_16x16x128_f8f6f4 v[26:29], v[192:199], v[230:237], v[26:29], v213, v213 op_sel_hi:[0,0,0]
	v_mfma_scale_f32_16x16x128_f8f6f4 v[22:25], v[0:7], v[238:245], v[22:25], v213, v213 op_sel_hi:[0,0,0]
	v_mfma_scale_f32_16x16x128_f8f6f4 v[18:21], v[192:199], v[238:245], v[18:21], v213, v213 op_sel_hi:[0,0,0]
	s_setprio 0
	s_add_u32 s81, s81, 0x100
	s_addc_u32 s82, s82, 0
	s_add_u32 s52, s52, 0x100
	s_addc_u32 s53, s53, 0
	s_cmp_ge_i32 s83, s4
	s_mov_b32 s54, s83
	s_barrier
	s_cbranch_scc0 .LBB0_1085
	s_and_b64 vcc, exec, s[36:37]
	s_cbranch_vccz .LBB0_1088

; #define G8_STAGE(bufoff, gbase, voff) do { _Pragma("unroll") for (int _i = 0; _i < 2; ++_i) \
;         __builtin_amdgcn_global_load_lds((const unsigned*)((const char*)(gbase) + (voff)[_i]), (LAS unsigned*)(lds + (bufoff) + ldsw + _i * 8192), 16, 0, 0); } while (0)
; #define G8_STAGE_A(bufoff, gbase, h_, nx_) do { if constexpr (Sched::GATHER) { unsigned vo_[2]; _Pragma("unroll") for (int q_ = 0; q_ < 2; ++q_) vo_[q_] = (nx_) ? gnxt[h_][q_] : goff[h_][q_]; G8_STAGE(bufoff, gbase, vo_); } \
;         else { G8_STAGE(bufoff, (gbase) + ((h_) ? hstepA : (size_t)0), voffA); } } while (0)
; #define G8_XLDA(b, h) do { if constexpr (Epi::FP8) { G8_LD8(A8, G8_SA(b, h) + aoff, 4); } else { G8_LDA(At, b, h); } } while (0)
; #define G8_XLDB0(b, h) do { if constexpr (Epi::FP8) { G8_LD8(B08, G8_SB(b, h) + boff, 2); } else { G8_LDB(B0, b, h); } } while (0)
; #define G8_XLDB1(b, h) do { if constexpr (Epi::FP8) { G8_LD8(B18, G8_SB(b, h) + boff, 2); } else { G8_LDB(B1, b, h); } } while (0)
; #define G8_MM0(ai, bj) do { if constexpr (Epi::FP8) { G8_MMA8(ai, bj, A8, B08); } else { G8_MMA(ai, bj, At, B0); } } while (0)
; #define G8_MM1(ai, bj) do { if constexpr (Epi::FP8) { G8_MMA8(ai, bj, A8, B18); } else { G8_MMA(ai, bj, At, B1); } } while (0)
; template <int lda, int ldb, class Epi, class Sched>
; __device__ __forceinline__ void gemm_phase(LAS unsigned char* lds, int wid, int lane, const char* baseA, const char* baseB, const Sched& S, const Epi& E) {
;     ...
;         for (int t = 0; t < nt; t += 2) {
;             const bool last = (t == nt - 2);
;             const char* a1 = cA + (size_t)(t + 1) * kstep;
;             const char* a2 = last ? nA : cA + (size_t)(t + 2) * kstep; const char* b2 = last ? nB : cB + (size_t)(t + 2) * kstep;
;             const char* a3 = a2 + kstep; const char* b3 = b2 + kstep;
;     ...
;             G8_XLDB0(0, 0); if constexpr (!Epi::HALFN) { G8_XLDB1(0, 1); } G8_SCHED; G8_XLDA(0, 0); G8_STAGE_A(G8_SA(1, 1), a1, 1, false);
;             G8_WAIT_VK; G8_WAIT_L(0); G8_BAR; G8_MM0(0, 0); if constexpr (!Epi::HALFN) { G8_MM1(0, 1); } G8_BAR; G8_SCHED;
;             G8_XLDA(0, 1); G8_STAGE(G8_SB(0, 0), b2, voffB); if constexpr (!Epi::HALFN) { G8_STAGE(G8_SB(0, 1), b2 + hstepB, voffB); } G8_STAGE_A(G8_SA(0, 0), a2, 0, last);
;             G8_WAIT_VK; G8_WAIT_L(0); G8_BAR; G8_MM0(1, 0); if constexpr (!Epi::HALFN) { G8_MM1(1, 1); } G8_BAR; G8_SCHED;
.LBB0_1190:
	v_add_u32_e32 v1, 0x10000, v148
	ds_read_b128 v[150:153], v1
	ds_read_b128 v[168:171], v1 offset:1024
	ds_read_b128 v[172:175], v1 offset:2048
	ds_read_b128 v[176:179], v1 offset:3072
	s_add_i32 s70, s46, 2
	s_add_u32 s44, s42, 0x100
	s_addc_u32 s45, s43, 0
	s_cmp_eq_u32 s67, s46
	s_cselect_b32 s46, s64, s44
	s_cselect_b32 s47, s63, s45
	s_cselect_b32 s73, s65, s69
	s_cselect_b32 s72, s66, s68
	v_lshl_add_u64 v[154:155], s[42:43], 0, v[76:77]
	s_add_i32 m0, s27, 0xc000
	ds_read_b128 v[184:187], v30
	ds_read_b128 v[188:191], v30 offset:1024
	ds_read_b128 v[192:195], v30 offset:2048
	ds_read_b128 v[196:199], v30 offset:3072
	ds_read_b128 v[206:209], v30 offset:4096
	ds_read_b128 v[210:213], v30 offset:5120
	ds_read_b128 v[214:217], v30 offset:6144
	ds_read_b128 v[218:221], v30 offset:7168
	global_load_lds_dwordx4 v[154:155], off
	v_lshl_add_u64 v[154:155], s[42:43], 0, v[78:79]
	s_add_i32 m0, s27, 0xe000
	s_nop 0
	global_load_lds_dwordx4 v[154:155], off
	s_waitcnt vmcnt(6)
	s_waitcnt lgkmcnt(0)
	s_barrier
	s_setprio 1
	s_waitcnt lgkmcnt(0)
	v_mfma_f32_16x16x32_bf16 v[64:67], v[150:153], v[184:187], v[64:67]
	v_mfma_f32_16x16x32_bf16 v[60:63], v[172:175], v[184:187], v[60:63]
	v_mfma_f32_16x16x32_bf16 v[56:59], v[150:153], v[192:195], v[56:59]
	v_mfma_f32_16x16x32_bf16 v[52:55], v[172:175], v[192:195], v[52:55]
	v_mfma_f32_16x16x32_bf16 v[48:51], v[150:153], v[206:209], v[48:51]
	v_mfma_f32_16x16x32_bf16 v[44:47], v[172:175], v[206:209], v[44:47]
	v_mfma_f32_16x16x32_bf16 v[40:43], v[150:153], v[214:217], v[40:43]
	v_mfma_f32_16x16x32_bf16 v[36:39], v[172:175], v[214:217], v[36:39]
	v_mfma_f32_16x16x32_bf16 v[64:67], v[168:171], v[188:191], v[64:67]
	v_mfma_f32_16x16x32_bf16 v[60:63], v[176:179], v[188:191], v[60:63]
	v_mfma_f32_16x16x32_bf16 v[56:59], v[168:171], v[196:199], v[56:59]
	v_mfma_f32_16x16x32_bf16 v[52:55], v[176:179], v[196:199], v[52:55]
	v_mfma_f32_16x16x32_bf16 v[48:51], v[168:171], v[210:213], v[48:51]
	v_mfma_f32_16x16x32_bf16 v[44:47], v[176:179], v[210:213], v[44:47]
	v_mfma_f32_16x16x32_bf16 v[40:43], v[168:171], v[218:221], v[40:43]
	v_mfma_f32_16x16x32_bf16 v[36:39], v[176:179], v[218:221], v[36:39]
	s_setprio 0
	s_barrier
	s_mov_b32 m0, s21
	v_lshl_add_u64 v[154:155], s[72:73], 0, v[70:71]
	ds_read_b128 v[184:187], v30 offset:16384
	ds_read_b128 v[188:191], v30 offset:17408
	ds_read_b128 v[192:195], v30 offset:18432
	ds_read_b128 v[196:199], v30 offset:19456
	ds_read_b128 v[206:209], v30 offset:20480
	ds_read_b128 v[210:213], v30 offset:21504
	ds_read_b128 v[214:217], v30 offset:22528
	ds_read_b128 v[218:221], v30 offset:23552
	global_load_lds_dwordx4 v[154:155], off
	v_lshl_add_u64 v[180:181], s[72:73], 0, v[74:75]
	s_mov_b32 m0, s28
	v_lshl_add_u64 v[222:223], s[46:47], 0, v[68:69]
	global_load_lds_dwordx4 v[180:181], off
	s_mov_b32 m0, s27
	v_lshl_add_u64 v[224:225], s[46:47], 0, v[72:73]
	global_load_lds_dwordx4 v[222:223], off
	s_mov_b32 m0, s29
	s_nop 0
	global_load_lds_dwordx4 v[224:225], off
	s_waitcnt vmcnt(6)
	s_waitcnt lgkmcnt(0)
	s_barrier
	s_setprio 1
	s_waitcnt lgkmcnt(0)
	v_mfma_f32_16x16x32_bf16 v[32:35], v[150:153], v[184:187], v[32:35]
	v_mfma_f32_16x16x32_bf16 v[26:29], v[172:175], v[184:187], v[26:29]
	v_mfma_f32_16x16x32_bf16 v[22:25], v[150:153], v[192:195], v[22:25]
	v_mfma_f32_16x16x32_bf16 v[18:21], v[172:175], v[192:195], v[18:21]
	v_mfma_f32_16x16x32_bf16 v[14:17], v[150:153], v[206:209], v[14:17]
	v_mfma_f32_16x16x32_bf16 v[10:13], v[172:175], v[206:209], v[10:13]
	v_mfma_f32_16x16x32_bf16 v[6:9], v[150:153], v[214:217], v[6:9]
	v_mfma_f32_16x16x32_bf16 v[2:5], v[172:175], v[214:217], v[2:5]
	v_mfma_f32_16x16x32_bf16 v[32:35], v[168:171], v[188:191], v[32:35]
	v_mfma_f32_16x16x32_bf16 v[26:29], v[176:179], v[188:191], v[26:29]
	v_mfma_f32_16x16x32_bf16 v[22:25], v[168:171], v[196:199], v[22:25]
	v_mfma_f32_16x16x32_bf16 v[18:21], v[176:179], v[196:199], v[18:21]
	v_mfma_f32_16x16x32_bf16 v[14:17], v[168:171], v[210:213], v[14:17]
	v_mfma_f32_16x16x32_bf16 v[10:13], v[176:179], v[210:213], v[10:13]
	v_mfma_f32_16x16x32_bf16 v[6:9], v[168:171], v[218:221], v[6:9]
	v_mfma_f32_16x16x32_bf16 v[2:5], v[176:179], v[218:221], v[2:5]
	s_setprio 0
	s_barrier
; #define G8_STAGE(bufoff, gbase, voff) do { _Pragma("unroll") for (int _i = 0; _i < 2; ++_i) \
;         __builtin_amdgcn_global_load_lds((const unsigned*)((const char*)(gbase) + (voff)[_i]), (LAS unsigned*)(lds + (bufoff) + ldsw + _i * 8192), 16, 0, 0); } while (0)
; #define G8_STAGE_A(bufoff, gbase, h_, nx_) do { if constexpr (Sched::GATHER) { unsigned vo_[2]; _Pragma("unroll") for (int q_ = 0; q_ < 2; ++q_) vo_[q_] = (nx_) ? gnxt[h_][q_] : goff[h_][q_]; G8_STAGE(bufoff, gbase, vo_); } \
;         else { G8_STAGE(bufoff, (gbase) + ((h_) ? hstepA : (size_t)0), voffA); } } while (0)
; #define G8_XLDA(b, h) do { if constexpr (Epi::FP8) { G8_LD8(A8, G8_SA(b, h) + aoff, 4); } else { G8_LDA(At, b, h); } } while (0)
; #define G8_XLDB0(b, h) do { if constexpr (Epi::FP8) { G8_LD8(B08, G8_SB(b, h) + boff, 2); } else { G8_LDB(B0, b, h); } } while (0)
; #define G8_XLDB1(b, h) do { if constexpr (Epi::FP8) { G8_LD8(B18, G8_SB(b, h) + boff, 2); } else { G8_LDB(B1, b, h); } } while (0)
; #define G8_MM0(ai, bj) do { if constexpr (Epi::FP8) { G8_MMA8(ai, bj, A8, B08); } else { G8_MMA(ai, bj, At, B0); } } while (0)
; #define G8_MM1(ai, bj) do { if constexpr (Epi::FP8) { G8_MMA8(ai, bj, A8, B18); } else { G8_MMA(ai, bj, At, B1); } } while (0)
; #define G8_WAIT_L(n) asm volatile("s_waitcnt lgkmcnt(" #n ")" ::: "memory")
; #define G8_BAR __builtin_amdgcn_s_barrier()
; #define G8_SCHED __builtin_amdgcn_sched_barrier(0)
; #define G8_WAIT_VK do { if constexpr (Epi::HALFN) { G8_WAIT_V(6); } else { G8_WAIT_V(8); } } while (0)
; template <int lda, int ldb, class Epi, class Sched>
; __device__ __forceinline__ void gemm_phase(LAS unsigned char* lds, int wid, int lane, const char* baseA, const char* baseB, const Sched& S, const Epi& E) {
;     ...
;             G8_XLDB0(1, 0); if constexpr (!Epi::HALFN) { G8_XLDB1(1, 1); } G8_SCHED; G8_XLDA(1, 0); G8_STAGE_A(G8_SA(0, 1), a2, 1, last);
;             G8_WAIT_VK; G8_WAIT_L(0); G8_BAR; G8_MM0(0, 0); if constexpr (!Epi::HALFN) { G8_MM1(0, 1); } G8_BAR; G8_SCHED;
;             G8_XLDA(1, 1); G8_STAGE(G8_SB(1, 0), b3, voffB); if constexpr (!Epi::HALFN) { G8_STAGE(G8_SB(1, 1), b3 + hstepB, voffB); } G8_STAGE_A(G8_SA(1, 0), a3, 0, last);
;             G8_WAIT_VK; G8_WAIT_L(0); G8_BAR; G8_MM0(1, 0); if constexpr (!Epi::HALFN) { G8_MM1(1, 1); } G8_BAR; G8_SCHED;
;         }
	v_add_u32_e32 v1, 0x18000, v148
	ds_read_b128 v[150:153], v1
	ds_read_b128 v[168:171], v1 offset:1024
	ds_read_b128 v[172:175], v1 offset:2048
	ds_read_b128 v[176:179], v1 offset:3072
	s_add_u32 s42, s46, 0x50000
	s_addc_u32 s43, s47, 0
	s_mov_b32 m0, s31
	v_lshl_add_u64 v[226:227], s[42:43], 0, v[68:69]
	ds_read_b128 v[184:187], v30 offset:32768
	ds_read_b128 v[188:191], v30 offset:33792
	ds_read_b128 v[192:195], v30 offset:34816
	ds_read_b128 v[196:199], v30 offset:35840
	ds_read_b128 v[206:209], v30 offset:36864
	ds_read_b128 v[210:213], v30 offset:37888
	ds_read_b128 v[214:217], v30 offset:38912
	ds_read_b128 v[218:221], v30 offset:39936
	global_load_lds_dwordx4 v[226:227], off
	v_lshl_add_u64 v[226:227], s[42:43], 0, v[72:73]
	s_mov_b32 m0, s48
	s_nop 0
	global_load_lds_dwordx4 v[226:227], off
	s_waitcnt vmcnt(6)
	s_waitcnt lgkmcnt(0)
	s_barrier
	s_setprio 1
	s_waitcnt lgkmcnt(0)
	v_mfma_f32_16x16x32_bf16 v[64:67], v[150:153], v[184:187], v[64:67]
	v_mfma_f32_16x16x32_bf16 v[60:63], v[172:175], v[184:187], v[60:63]
	v_mfma_f32_16x16x32_bf16 v[56:59], v[150:153], v[192:195], v[56:59]
	v_mfma_f32_16x16x32_bf16 v[52:55], v[172:175], v[192:195], v[52:55]
	v_mfma_f32_16x16x32_bf16 v[48:51], v[150:153], v[206:209], v[48:51]
	v_mfma_f32_16x16x32_bf16 v[44:47], v[172:175], v[206:209], v[44:47]
	v_mfma_f32_16x16x32_bf16 v[40:43], v[150:153], v[214:217], v[40:43]
	v_mfma_f32_16x16x32_bf16 v[36:39], v[172:175], v[214:217], v[36:39]
	v_mfma_f32_16x16x32_bf16 v[64:67], v[168:171], v[188:191], v[64:67]
	v_mfma_f32_16x16x32_bf16 v[60:63], v[176:179], v[188:191], v[60:63]
	v_mfma_f32_16x16x32_bf16 v[56:59], v[168:171], v[196:199], v[56:59]
	v_mfma_f32_16x16x32_bf16 v[52:55], v[176:179], v[196:199], v[52:55]
	v_mfma_f32_16x16x32_bf16 v[48:51], v[168:171], v[210:213], v[48:51]
	v_mfma_f32_16x16x32_bf16 v[44:47], v[176:179], v[210:213], v[44:47]
	v_mfma_f32_16x16x32_bf16 v[40:43], v[168:171], v[218:221], v[40:43]
	v_mfma_f32_16x16x32_bf16 v[36:39], v[176:179], v[218:221], v[36:39]
	s_setprio 0
	s_barrier
	s_mov_b32 m0, s49
	v_lshl_add_u64 v[154:155], v[154:155], 0, s[22:23]
	ds_read_b128 v[184:187], v30 offset:49152
	ds_read_b128 v[188:191], v30 offset:50176
	ds_read_b128 v[192:195], v30 offset:51200
	ds_read_b128 v[196:199], v30 offset:52224
	ds_read_b128 v[206:209], v30 offset:53248
	ds_read_b128 v[210:213], v30 offset:54272
	ds_read_b128 v[214:217], v30 offset:55296
	ds_read_b128 v[218:221], v30 offset:56320
	global_load_lds_dwordx4 v[154:155], off
	v_lshl_add_u64 v[154:155], v[180:181], 0, s[22:23]
	s_mov_b32 m0, s50
	s_nop 0
	global_load_lds_dwordx4 v[154:155], off
	v_lshl_add_u64 v[154:155], v[222:223], 0, s[22:23]
	s_mov_b32 m0, s51
	s_nop 0
	global_load_lds_dwordx4 v[154:155], off
	v_lshl_add_u64 v[154:155], v[224:225], 0, s[22:23]
	s_mov_b32 m0, s52
	s_nop 0
	global_load_lds_dwordx4 v[154:155], off
	s_waitcnt vmcnt(6)
	s_waitcnt lgkmcnt(0)
	s_barrier
	s_setprio 1
	s_waitcnt lgkmcnt(0)
	v_mfma_f32_16x16x32_bf16 v[32:35], v[150:153], v[184:187], v[32:35]
	v_mfma_f32_16x16x32_bf16 v[26:29], v[172:175], v[184:187], v[26:29]
	v_mfma_f32_16x16x32_bf16 v[22:25], v[150:153], v[192:195], v[22:25]
	v_mfma_f32_16x16x32_bf16 v[18:21], v[172:175], v[192:195], v[18:21]
	v_mfma_f32_16x16x32_bf16 v[14:17], v[150:153], v[206:209], v[14:17]
	v_mfma_f32_16x16x32_bf16 v[10:13], v[172:175], v[206:209], v[10:13]
	v_mfma_f32_16x16x32_bf16 v[6:9], v[150:153], v[214:217], v[6:9]
	v_mfma_f32_16x16x32_bf16 v[2:5], v[172:175], v[214:217], v[2:5]
	v_mfma_f32_16x16x32_bf16 v[32:35], v[168:171], v[188:191], v[32:35]
	v_mfma_f32_16x16x32_bf16 v[26:29], v[176:179], v[188:191], v[26:29]
	v_mfma_f32_16x16x32_bf16 v[22:25], v[168:171], v[196:199], v[22:25]
	v_mfma_f32_16x16x32_bf16 v[18:21], v[176:179], v[196:199], v[18:21]
	v_mfma_f32_16x16x32_bf16 v[14:17], v[168:171], v[210:213], v[14:17]
	v_mfma_f32_16x16x32_bf16 v[10:13], v[176:179], v[210:213], v[10:13]
	v_mfma_f32_16x16x32_bf16 v[6:9], v[168:171], v[218:221], v[6:9]
	v_mfma_f32_16x16x32_bf16 v[2:5], v[176:179], v[218:221], v[2:5]
	s_setprio 0
	s_add_u32 s68, s68, 0x100
	s_addc_u32 s69, s69, 0
	s_cmp_ge_i32 s70, s62
	s_mov_b64 s[42:43], s[44:45]
	s_mov_b32 s46, s70
	s_barrier
	s_cbranch_scc0 .LBB0_1190
	s_mov_b32 s72, s82
	s_and_b64 vcc, exec, s[36:37]
	s_cbranch_vccz .LBB0_1193

; #define G8_STAGE(bufoff, gbase, voff) do { _Pragma("unroll") for (int _i = 0; _i < 2; ++_i) \
;         __builtin_amdgcn_global_load_lds((const unsigned*)((const char*)(gbase) + (voff)[_i]), (LAS unsigned*)(lds + (bufoff) + ldsw + _i * 8192), 16, 0, 0); } while (0)
; #define G8_STAGE_A(bufoff, gbase, h_, nx_) do { if constexpr (Sched::GATHER) { unsigned vo_[2]; _Pragma("unroll") for (int q_ = 0; q_ < 2; ++q_) vo_[q_] = (nx_) ? gnxt[h_][q_] : goff[h_][q_]; G8_STAGE(bufoff, gbase, vo_); } \
;         else { G8_STAGE(bufoff, (gbase) + ((h_) ? hstepA : (size_t)0), voffA); } } while (0)
; #define G8_XLDA(b, h) do { if constexpr (Epi::FP8) { G8_LD8(A8, G8_SA(b, h) + aoff, 4); } else { G8_LDA(At, b, h); } } while (0)
; #define G8_XLDB0(b, h) do { if constexpr (Epi::FP8) { G8_LD8(B08, G8_SB(b, h) + boff, 2); } else { G8_LDB(B0, b, h); } } while (0)
; #define G8_XLDB1(b, h) do { if constexpr (Epi::FP8) { G8_LD8(B18, G8_SB(b, h) + boff, 2); } else { G8_LDB(B1, b, h); } } while (0)
; #define G8_MM0(ai, bj) do { if constexpr (Epi::FP8) { G8_MMA8(ai, bj, A8, B08); } else { G8_MMA(ai, bj, At, B0); } } while (0)
; #define G8_MM1(ai, bj) do { if constexpr (Epi::FP8) { G8_MMA8(ai, bj, A8, B18); } else { G8_MMA(ai, bj, At, B1); } } while (0)
; #define G8_WAIT_L(n) asm volatile("s_waitcnt lgkmcnt(" #n ")" ::: "memory")
; #define G8_BAR __builtin_amdgcn_s_barrier()
; template <int lda, int ldb, class Epi, class Sched>
; __device__ __forceinline__ void gemm_phase(LAS unsigned char* lds, int wid, int lane, const char* baseA, const char* baseB, const Sched& S, const Epi& E) {
;     ...
;         for (int t = 0; t < nt; t += 2) {
;             const bool last = (t == nt - 2);
;             const char* a1 = cA + (size_t)(t + 1) * kstep;
;             const char* a2 = last ? nA : cA + (size_t)(t + 2) * kstep; const char* b2 = last ? nB : cB + (size_t)(t + 2) * kstep;
;             const char* a3 = a2 + kstep; const char* b3 = b2 + kstep;
;     ...
;             G8_XLDB0(0, 0); if constexpr (!Epi::HALFN) { G8_XLDB1(0, 1); } G8_SCHED; G8_XLDA(0, 0); G8_STAGE_A(G8_SA(1, 1), a1, 1, false);
;             G8_WAIT_VK; G8_WAIT_L(0); G8_BAR; G8_MM0(0, 0); if constexpr (!Epi::HALFN) { G8_MM1(0, 1); } G8_BAR; G8_SCHED;
;             G8_XLDA(0, 1); G8_STAGE(G8_SB(0, 0), b2, voffB); if constexpr (!Epi::HALFN) { G8_STAGE(G8_SB(0, 1), b2 + hstepB, voffB); } G8_STAGE_A(G8_SA(0, 0), a2, 0, last);
.LBB0_1285:
	v_add_u32_e32 v1, 0x10000, v148
	ds_read_b128 v[144:147], v1
	ds_read_b128 v[150:153], v1 offset:1024
	ds_read_b128 v[154:157], v1 offset:2048
	ds_read_b128 v[158:161], v1 offset:3072
	v_add_u32_e32 v1, 0x14000, v148
	ds_read_b128 v[162:165], v1
	ds_read_b128 v[166:169], v1 offset:1024
	ds_read_b128 v[170:173], v1 offset:2048
	ds_read_b128 v[174:177], v1 offset:3072
	s_add_i32 s72, s44, 2
	s_add_u32 s45, s42, 0xfffc0080
	s_addc_u32 s46, s43, -1
	s_cmp_eq_u32 s69, s44
	s_cselect_b32 s44, s68, s70
	s_cselect_b32 s47, s65, s46
	s_cselect_b32 s46, s66, s45
	s_cselect_b32 s45, s67, s71
	v_lshl_add_u64 v[218:219], s[42:43], 0, v[140:141]
	s_add_i32 m0, s27, 0xc000
	ds_read_b128 v[178:181], v30
	ds_read_b128 v[184:187], v30 offset:1024
	ds_read_b128 v[188:191], v30 offset:2048
	ds_read_b128 v[192:195], v30 offset:3072
	ds_read_b128 v[196:199], v30 offset:4096
	ds_read_b128 v[206:209], v30 offset:5120
	ds_read_b128 v[210:213], v30 offset:6144
	ds_read_b128 v[214:217], v30 offset:7168
	global_load_lds_dwordx4 v[218:219], off
	v_lshl_add_u64 v[218:219], s[42:43], 0, v[142:143]
	s_add_i32 m0, s27, 0xe000
	s_nop 0
	global_load_lds_dwordx4 v[218:219], off
	s_waitcnt vmcnt(8)
	s_waitcnt lgkmcnt(0)
	s_barrier
	s_setprio 1
	s_waitcnt lgkmcnt(0)
	v_mfma_f32_16x16x32_bf16 v[128:131], v[144:147], v[178:181], v[128:131]
	v_mfma_f32_16x16x32_bf16 v[124:127], v[154:157], v[178:181], v[124:127]
	v_mfma_f32_16x16x32_bf16 v[112:115], v[144:147], v[188:191], v[112:115]
	v_mfma_f32_16x16x32_bf16 v[108:111], v[154:157], v[188:191], v[108:111]
	v_mfma_f32_16x16x32_bf16 v[96:99], v[144:147], v[196:199], v[96:99]
	v_mfma_f32_16x16x32_bf16 v[92:95], v[154:157], v[196:199], v[92:95]
	v_mfma_f32_16x16x32_bf16 v[80:83], v[144:147], v[210:213], v[80:83]
	v_mfma_f32_16x16x32_bf16 v[76:79], v[154:157], v[210:213], v[76:79]
	v_mfma_f32_16x16x32_bf16 v[128:131], v[150:153], v[184:187], v[128:131]
	v_mfma_f32_16x16x32_bf16 v[124:127], v[158:161], v[184:187], v[124:127]
	v_mfma_f32_16x16x32_bf16 v[112:115], v[150:153], v[192:195], v[112:115]
	v_mfma_f32_16x16x32_bf16 v[108:111], v[158:161], v[192:195], v[108:111]
	v_mfma_f32_16x16x32_bf16 v[96:99], v[150:153], v[206:209], v[96:99]
	v_mfma_f32_16x16x32_bf16 v[92:95], v[158:161], v[206:209], v[92:95]
	v_mfma_f32_16x16x32_bf16 v[80:83], v[150:153], v[214:217], v[80:83]
	v_mfma_f32_16x16x32_bf16 v[76:79], v[158:161], v[214:217], v[76:79]
	s_setprio 0
	s_setprio 1
	v_mfma_f32_16x16x32_bf16 v[120:123], v[162:165], v[178:181], v[120:123]
	v_mfma_f32_16x16x32_bf16 v[116:119], v[170:173], v[178:181], v[116:119]
	v_mfma_f32_16x16x32_bf16 v[104:107], v[162:165], v[188:191], v[104:107]
	v_mfma_f32_16x16x32_bf16 v[100:103], v[170:173], v[188:191], v[100:103]
	v_mfma_f32_16x16x32_bf16 v[88:91], v[162:165], v[196:199], v[88:91]
	v_mfma_f32_16x16x32_bf16 v[84:87], v[170:173], v[196:199], v[84:87]
	v_mfma_f32_16x16x32_bf16 v[72:75], v[162:165], v[210:213], v[72:75]
	v_mfma_f32_16x16x32_bf16 v[68:71], v[170:173], v[210:213], v[68:71]
	v_mfma_f32_16x16x32_bf16 v[120:123], v[166:169], v[184:187], v[120:123]
	v_mfma_f32_16x16x32_bf16 v[116:119], v[174:177], v[184:187], v[116:119]
	v_mfma_f32_16x16x32_bf16 v[104:107], v[166:169], v[192:195], v[104:107]
	v_mfma_f32_16x16x32_bf16 v[100:103], v[174:177], v[192:195], v[100:103]
	v_mfma_f32_16x16x32_bf16 v[88:91], v[166:169], v[206:209], v[88:91]
	v_mfma_f32_16x16x32_bf16 v[84:87], v[174:177], v[206:209], v[84:87]
	v_mfma_f32_16x16x32_bf16 v[72:75], v[166:169], v[214:217], v[72:75]
	v_mfma_f32_16x16x32_bf16 v[68:71], v[174:177], v[214:217], v[68:71]
	s_setprio 0
	s_barrier
	s_mov_b32 m0, s20
	v_lshl_add_u64 v[218:219], s[44:45], 0, v[136:137]
	s_add_u32 s74, s44, 0x40000
	ds_read_b128 v[178:181], v30 offset:16384
	ds_read_b128 v[184:187], v30 offset:17408
	ds_read_b128 v[188:191], v30 offset:18432
	ds_read_b128 v[192:195], v30 offset:19456
	ds_read_b128 v[196:199], v30 offset:20480
	ds_read_b128 v[206:209], v30 offset:21504
	ds_read_b128 v[210:213], v30 offset:22528
	ds_read_b128 v[214:217], v30 offset:23552
	global_load_lds_dwordx4 v[218:219], off
	v_lshl_add_u64 v[220:221], s[44:45], 0, v[132:133]
	s_mov_b32 m0, s21
	s_addc_u32 s75, s45, 0
	global_load_lds_dwordx4 v[220:221], off
	v_lshl_add_u64 v[222:223], s[74:75], 0, v[136:137]
	s_mov_b32 m0, s28
	v_lshl_add_u64 v[224:225], s[46:47], 0, v[134:135]
	global_load_lds_dwordx4 v[222:223], off
	v_lshl_add_u64 v[222:223], s[74:75], 0, v[132:133]
	s_mov_b32 m0, s29
	s_nop 0
	global_load_lds_dwordx4 v[222:223], off
	v_lshl_add_u64 v[222:223], s[46:47], 0, v[138:139]
	s_mov_b32 m0, s27
	s_nop 0
	global_load_lds_dwordx4 v[222:223], off
	s_mov_b32 m0, s31
	s_nop 0
	global_load_lds_dwordx4 v[224:225], off
	s_waitcnt vmcnt(8)
	s_waitcnt lgkmcnt(0)
	s_barrier
; #define G8_STAGE(bufoff, gbase, voff) do { _Pragma("unroll") for (int _i = 0; _i < 2; ++_i) \
;         __builtin_amdgcn_global_load_lds((const unsigned*)((const char*)(gbase) + (voff)[_i]), (LAS unsigned*)(lds + (bufoff) + ldsw + _i * 8192), 16, 0, 0); } while (0)
; #define G8_STAGE_A(bufoff, gbase, h_, nx_) do { if constexpr (Sched::GATHER) { unsigned vo_[2]; _Pragma("unroll") for (int q_ = 0; q_ < 2; ++q_) vo_[q_] = (nx_) ? gnxt[h_][q_] : goff[h_][q_]; G8_STAGE(bufoff, gbase, vo_); } \
;         else { G8_STAGE(bufoff, (gbase) + ((h_) ? hstepA : (size_t)0), voffA); } } while (0)
; #define G8_XLDA(b, h) do { if constexpr (Epi::FP8) { G8_LD8(A8, G8_SA(b, h) + aoff, 4); } else { G8_LDA(At, b, h); } } while (0)
; #define G8_XLDB0(b, h) do { if constexpr (Epi::FP8) { G8_LD8(B08, G8_SB(b, h) + boff, 2); } else { G8_LDB(B0, b, h); } } while (0)
; #define G8_XLDB1(b, h) do { if constexpr (Epi::FP8) { G8_LD8(B18, G8_SB(b, h) + boff, 2); } else { G8_LDB(B1, b, h); } } while (0)
; #define G8_MM0(ai, bj) do { if constexpr (Epi::FP8) { G8_MMA8(ai, bj, A8, B08); } else { G8_MMA(ai, bj, At, B0); } } while (0)
; #define G8_MM1(ai, bj) do { if constexpr (Epi::FP8) { G8_MMA8(ai, bj, A8, B18); } else { G8_MMA(ai, bj, At, B1); } } while (0)
; #define G8_WAIT_L(n) asm volatile("s_waitcnt lgkmcnt(" #n ")" ::: "memory")
; #define G8_BAR __builtin_amdgcn_s_barrier()
; #define G8_SCHED __builtin_amdgcn_sched_barrier(0)
; template <int lda, int ldb, class Epi, class Sched>
; __device__ __forceinline__ void gemm_phase(LAS unsigned char* lds, int wid, int lane, const char* baseA, const char* baseB, const Sched& S, const Epi& E) {
;     ...
;             G8_WAIT_VK; G8_WAIT_L(0); G8_BAR; G8_MM0(0, 0); if constexpr (!Epi::HALFN) { G8_MM1(0, 1); } G8_BAR; G8_SCHED;
;             G8_XLDA(0, 1); G8_STAGE(G8_SB(0, 0), b2, voffB); if constexpr (!Epi::HALFN) { G8_STAGE(G8_SB(0, 1), b2 + hstepB, voffB); } G8_STAGE_A(G8_SA(0, 0), a2, 0, last);
;             G8_WAIT_VK; G8_WAIT_L(0); G8_BAR; G8_MM0(1, 0); if constexpr (!Epi::HALFN) { G8_MM1(1, 1); } G8_BAR; G8_SCHED;
;             G8_XLDB0(1, 0); if constexpr (!Epi::HALFN) { G8_XLDB1(1, 1); } G8_SCHED; G8_XLDA(1, 0); G8_STAGE_A(G8_SA(0, 1), a2, 1, last);
;             G8_WAIT_VK; G8_WAIT_L(0); G8_BAR; G8_MM0(0, 0); if constexpr (!Epi::HALFN) { G8_MM1(0, 1); } G8_BAR; G8_SCHED;
	s_setprio 1
	s_waitcnt lgkmcnt(0)
	v_mfma_f32_16x16x32_bf16 v[64:67], v[144:147], v[178:181], v[64:67]
	v_mfma_f32_16x16x32_bf16 v[60:63], v[154:157], v[178:181], v[60:63]
	v_mfma_f32_16x16x32_bf16 v[48:51], v[144:147], v[188:191], v[48:51]
	v_mfma_f32_16x16x32_bf16 v[44:47], v[154:157], v[188:191], v[44:47]
	v_mfma_f32_16x16x32_bf16 v[32:35], v[144:147], v[196:199], v[32:35]
	v_mfma_f32_16x16x32_bf16 v[26:29], v[154:157], v[196:199], v[26:29]
	v_mfma_f32_16x16x32_bf16 v[14:17], v[144:147], v[210:213], v[14:17]
	v_mfma_f32_16x16x32_bf16 v[10:13], v[154:157], v[210:213], v[10:13]
	v_mfma_f32_16x16x32_bf16 v[64:67], v[150:153], v[184:187], v[64:67]
	v_mfma_f32_16x16x32_bf16 v[60:63], v[158:161], v[184:187], v[60:63]
	v_mfma_f32_16x16x32_bf16 v[48:51], v[150:153], v[192:195], v[48:51]
	v_mfma_f32_16x16x32_bf16 v[44:47], v[158:161], v[192:195], v[44:47]
	v_mfma_f32_16x16x32_bf16 v[32:35], v[150:153], v[206:209], v[32:35]
	v_mfma_f32_16x16x32_bf16 v[26:29], v[158:161], v[206:209], v[26:29]
	v_mfma_f32_16x16x32_bf16 v[14:17], v[150:153], v[214:217], v[14:17]
	v_mfma_f32_16x16x32_bf16 v[10:13], v[158:161], v[214:217], v[10:13]
	s_setprio 0
	s_setprio 1
	v_mfma_f32_16x16x32_bf16 v[56:59], v[162:165], v[178:181], v[56:59]
	v_mfma_f32_16x16x32_bf16 v[52:55], v[170:173], v[178:181], v[52:55]
	v_mfma_f32_16x16x32_bf16 v[40:43], v[162:165], v[188:191], v[40:43]
	v_mfma_f32_16x16x32_bf16 v[36:39], v[170:173], v[188:191], v[36:39]
	v_mfma_f32_16x16x32_bf16 v[22:25], v[162:165], v[196:199], v[22:25]
	v_mfma_f32_16x16x32_bf16 v[18:21], v[170:173], v[196:199], v[18:21]
	v_mfma_f32_16x16x32_bf16 v[6:9], v[162:165], v[210:213], v[6:9]
	v_mfma_f32_16x16x32_bf16 v[2:5], v[170:173], v[210:213], v[2:5]
	v_mfma_f32_16x16x32_bf16 v[56:59], v[166:169], v[184:187], v[56:59]
	v_mfma_f32_16x16x32_bf16 v[52:55], v[174:177], v[184:187], v[52:55]
	v_mfma_f32_16x16x32_bf16 v[40:43], v[166:169], v[192:195], v[40:43]
	v_mfma_f32_16x16x32_bf16 v[36:39], v[174:177], v[192:195], v[36:39]
	v_mfma_f32_16x16x32_bf16 v[22:25], v[166:169], v[206:209], v[22:25]
	v_mfma_f32_16x16x32_bf16 v[18:21], v[174:177], v[206:209], v[18:21]
	v_mfma_f32_16x16x32_bf16 v[6:9], v[166:169], v[214:217], v[6:9]
	v_mfma_f32_16x16x32_bf16 v[2:5], v[174:177], v[214:217], v[2:5]
	s_setprio 0
	s_barrier
	v_add_u32_e32 v1, 0x18000, v148
	ds_read_b128 v[144:147], v1
	ds_read_b128 v[150:153], v1 offset:1024
	ds_read_b128 v[154:157], v1 offset:2048
	ds_read_b128 v[158:161], v1 offset:3072
	v_add_u32_e32 v1, 0x1c000, v148
	ds_read_b128 v[162:165], v1
	ds_read_b128 v[166:169], v1 offset:1024
	ds_read_b128 v[170:173], v1 offset:2048
	ds_read_b128 v[174:177], v1 offset:3072
	s_add_u32 s46, s46, 0x40000
	s_addc_u32 s47, s47, 0
	s_mov_b32 m0, s48
	v_lshl_add_u64 v[226:227], s[46:47], 0, v[138:139]
	ds_read_b128 v[178:181], v30 offset:32768
	ds_read_b128 v[184:187], v30 offset:33792
	ds_read_b128 v[188:191], v30 offset:34816
	ds_read_b128 v[192:195], v30 offset:35840
	ds_read_b128 v[196:199], v30 offset:36864
	ds_read_b128 v[206:209], v30 offset:37888
	ds_read_b128 v[210:213], v30 offset:38912
	ds_read_b128 v[214:217], v30 offset:39936
	global_load_lds_dwordx4 v[226:227], off
	v_lshl_add_u64 v[226:227], s[46:47], 0, v[134:135]
	s_mov_b32 m0, s49
	s_nop 0
	global_load_lds_dwordx4 v[226:227], off
	s_waitcnt vmcnt(8)
	s_waitcnt lgkmcnt(0)
	s_barrier
	s_setprio 1
	s_waitcnt lgkmcnt(0)
	v_mfma_f32_16x16x32_bf16 v[128:131], v[144:147], v[178:181], v[128:131]
	v_mfma_f32_16x16x32_bf16 v[124:127], v[154:157], v[178:181], v[124:127]
	v_mfma_f32_16x16x32_bf16 v[112:115], v[144:147], v[188:191], v[112:115]
	v_mfma_f32_16x16x32_bf16 v[108:111], v[154:157], v[188:191], v[108:111]
	v_mfma_f32_16x16x32_bf16 v[96:99], v[144:147], v[196:199], v[96:99]
	v_mfma_f32_16x16x32_bf16 v[92:95], v[154:157], v[196:199], v[92:95]
	v_mfma_f32_16x16x32_bf16 v[80:83], v[144:147], v[210:213], v[80:83]
	v_mfma_f32_16x16x32_bf16 v[76:79], v[154:157], v[210:213], v[76:79]
	v_mfma_f32_16x16x32_bf16 v[128:131], v[150:153], v[184:187], v[128:131]
	v_mfma_f32_16x16x32_bf16 v[124:127], v[158:161], v[184:187], v[124:127]
	v_mfma_f32_16x16x32_bf16 v[112:115], v[150:153], v[192:195], v[112:115]
	v_mfma_f32_16x16x32_bf16 v[108:111], v[158:161], v[192:195], v[108:111]
	v_mfma_f32_16x16x32_bf16 v[96:99], v[150:153], v[206:209], v[96:99]
	v_mfma_f32_16x16x32_bf16 v[92:95], v[158:161], v[206:209], v[92:95]
	v_mfma_f32_16x16x32_bf16 v[80:83], v[150:153], v[214:217], v[80:83]
	v_mfma_f32_16x16x32_bf16 v[76:79], v[158:161], v[214:217], v[76:79]
	s_setprio 0
	s_setprio 1
	v_mfma_f32_16x16x32_bf16 v[120:123], v[162:165], v[178:181], v[120:123]
	v_mfma_f32_16x16x32_bf16 v[116:119], v[170:173], v[178:181], v[116:119]
	v_mfma_f32_16x16x32_bf16 v[104:107], v[162:165], v[188:191], v[104:107]
	v_mfma_f32_16x16x32_bf16 v[100:103], v[170:173], v[188:191], v[100:103]
	v_mfma_f32_16x16x32_bf16 v[88:91], v[162:165], v[196:199], v[88:91]
	v_mfma_f32_16x16x32_bf16 v[84:87], v[170:173], v[196:199], v[84:87]
	v_mfma_f32_16x16x32_bf16 v[72:75], v[162:165], v[210:213], v[72:75]
	v_mfma_f32_16x16x32_bf16 v[68:71], v[170:173], v[210:213], v[68:71]
	v_mfma_f32_16x16x32_bf16 v[120:123], v[166:169], v[184:187], v[120:123]
	v_mfma_f32_16x16x32_bf16 v[116:119], v[174:177], v[184:187], v[116:119]
	v_mfma_f32_16x16x32_bf16 v[104:107], v[166:169], v[192:195], v[104:107]
	v_mfma_f32_16x16x32_bf16 v[100:103], v[174:177], v[192:195], v[100:103]
	v_mfma_f32_16x16x32_bf16 v[88:91], v[166:169], v[206:209], v[88:91]
	v_mfma_f32_16x16x32_bf16 v[84:87], v[174:177], v[206:209], v[84:87]
	v_mfma_f32_16x16x32_bf16 v[72:75], v[166:169], v[214:217], v[72:75]
	v_mfma_f32_16x16x32_bf16 v[68:71], v[174:177], v[214:217], v[68:71]
	s_setprio 0
	s_barrier
; #define G8_STAGE(bufoff, gbase, voff) do { _Pragma("unroll") for (int _i = 0; _i < 2; ++_i) \
;         __builtin_amdgcn_global_load_lds((const unsigned*)((const char*)(gbase) + (voff)[_i]), (LAS unsigned*)(lds + (bufoff) + ldsw + _i * 8192), 16, 0, 0); } while (0)
; #define G8_STAGE_A(bufoff, gbase, h_, nx_) do { if constexpr (Sched::GATHER) { unsigned vo_[2]; _Pragma("unroll") for (int q_ = 0; q_ < 2; ++q_) vo_[q_] = (nx_) ? gnxt[h_][q_] : goff[h_][q_]; G8_STAGE(bufoff, gbase, vo_); } \
;         else { G8_STAGE(bufoff, (gbase) + ((h_) ? hstepA : (size_t)0), voffA); } } while (0)
; #define G8_XLDA(b, h) do { if constexpr (Epi::FP8) { G8_LD8(A8, G8_SA(b, h) + aoff, 4); } else { G8_LDA(At, b, h); } } while (0)
; #define G8_MM0(ai, bj) do { if constexpr (Epi::FP8) { G8_MMA8(ai, bj, A8, B08); } else { G8_MMA(ai, bj, At, B0); } } while (0)
; #define G8_MM1(ai, bj) do { if constexpr (Epi::FP8) { G8_MMA8(ai, bj, A8, B18); } else { G8_MMA(ai, bj, At, B1); } } while (0)
; #define G8_WAIT_L(n) asm volatile("s_waitcnt lgkmcnt(" #n ")" ::: "memory")
; #define G8_BAR __builtin_amdgcn_s_barrier()
; #define G8_SCHED __builtin_amdgcn_sched_barrier(0)
; #define G8_WAIT_VK do { if constexpr (Epi::HALFN) { G8_WAIT_V(6); } else { G8_WAIT_V(8); } } while (0)
; template <int lda, int ldb, class Epi, class Sched>
; __device__ __forceinline__ void gemm_phase(LAS unsigned char* lds, int wid, int lane, const char* baseA, const char* baseB, const Sched& S, const Epi& E) {
;     ...
;             G8_XLDA(1, 1); G8_STAGE(G8_SB(1, 0), b3, voffB); if constexpr (!Epi::HALFN) { G8_STAGE(G8_SB(1, 1), b3 + hstepB, voffB); } G8_STAGE_A(G8_SA(1, 0), a3, 0, last);
;             G8_WAIT_VK; G8_WAIT_L(0); G8_BAR; G8_MM0(1, 0); if constexpr (!Epi::HALFN) { G8_MM1(1, 1); } G8_BAR; G8_SCHED;
;         }
	s_mov_b32 m0, s50
	v_lshl_add_u64 v[218:219], v[218:219], 0, s[22:23]
	s_add_u32 s44, s44, 0x40080
	ds_read_b128 v[178:181], v30 offset:49152
	ds_read_b128 v[184:187], v30 offset:50176
	ds_read_b128 v[188:191], v30 offset:51200
	ds_read_b128 v[192:195], v30 offset:52224
	ds_read_b128 v[196:199], v30 offset:53248
	ds_read_b128 v[206:209], v30 offset:54272
	ds_read_b128 v[210:213], v30 offset:55296
	ds_read_b128 v[214:217], v30 offset:56320
	global_load_lds_dwordx4 v[218:219], off
	v_lshl_add_u64 v[218:219], v[220:221], 0, s[22:23]
	s_mov_b32 m0, s51
	s_addc_u32 s45, s45, 0
	global_load_lds_dwordx4 v[218:219], off
	v_lshl_add_u64 v[218:219], s[44:45], 0, v[136:137]
	s_mov_b32 m0, s54
	s_nop 0
	global_load_lds_dwordx4 v[218:219], off
	v_lshl_add_u64 v[218:219], s[44:45], 0, v[132:133]
	s_mov_b32 m0, s55
	s_nop 0
	global_load_lds_dwordx4 v[218:219], off
	v_lshl_add_u64 v[218:219], v[222:223], 0, s[22:23]
	s_mov_b32 m0, s52
	s_nop 0
	global_load_lds_dwordx4 v[218:219], off
	v_lshl_add_u64 v[218:219], v[224:225], 0, s[22:23]
	s_mov_b32 m0, s53
	s_nop 0
	global_load_lds_dwordx4 v[218:219], off
	s_waitcnt vmcnt(8)
	s_waitcnt lgkmcnt(0)
	s_barrier
	s_setprio 1
	s_waitcnt lgkmcnt(0)
	v_mfma_f32_16x16x32_bf16 v[64:67], v[144:147], v[178:181], v[64:67]
	v_mfma_f32_16x16x32_bf16 v[60:63], v[154:157], v[178:181], v[60:63]
	v_mfma_f32_16x16x32_bf16 v[48:51], v[144:147], v[188:191], v[48:51]
	v_mfma_f32_16x16x32_bf16 v[44:47], v[154:157], v[188:191], v[44:47]
	v_mfma_f32_16x16x32_bf16 v[32:35], v[144:147], v[196:199], v[32:35]
	v_mfma_f32_16x16x32_bf16 v[26:29], v[154:157], v[196:199], v[26:29]
	v_mfma_f32_16x16x32_bf16 v[14:17], v[144:147], v[210:213], v[14:17]
	v_mfma_f32_16x16x32_bf16 v[10:13], v[154:157], v[210:213], v[10:13]
	v_mfma_f32_16x16x32_bf16 v[64:67], v[150:153], v[184:187], v[64:67]
	v_mfma_f32_16x16x32_bf16 v[60:63], v[158:161], v[184:187], v[60:63]
	v_mfma_f32_16x16x32_bf16 v[48:51], v[150:153], v[192:195], v[48:51]
	v_mfma_f32_16x16x32_bf16 v[44:47], v[158:161], v[192:195], v[44:47]
	v_mfma_f32_16x16x32_bf16 v[32:35], v[150:153], v[206:209], v[32:35]
	v_mfma_f32_16x16x32_bf16 v[26:29], v[158:161], v[206:209], v[26:29]
	v_mfma_f32_16x16x32_bf16 v[14:17], v[150:153], v[214:217], v[14:17]
	v_mfma_f32_16x16x32_bf16 v[10:13], v[158:161], v[214:217], v[10:13]
	s_setprio 0
	s_setprio 1
	v_mfma_f32_16x16x32_bf16 v[56:59], v[162:165], v[178:181], v[56:59]
	v_mfma_f32_16x16x32_bf16 v[52:55], v[170:173], v[178:181], v[52:55]
	v_mfma_f32_16x16x32_bf16 v[40:43], v[162:165], v[188:191], v[40:43]
	v_mfma_f32_16x16x32_bf16 v[36:39], v[170:173], v[188:191], v[36:39]
	v_mfma_f32_16x16x32_bf16 v[22:25], v[162:165], v[196:199], v[22:25]
	v_mfma_f32_16x16x32_bf16 v[18:21], v[170:173], v[196:199], v[18:21]
	v_mfma_f32_16x16x32_bf16 v[6:9], v[162:165], v[210:213], v[6:9]
	v_mfma_f32_16x16x32_bf16 v[2:5], v[170:173], v[210:213], v[2:5]
	v_mfma_f32_16x16x32_bf16 v[56:59], v[166:169], v[184:187], v[56:59]
	v_mfma_f32_16x16x32_bf16 v[52:55], v[174:177], v[184:187], v[52:55]
	v_mfma_f32_16x16x32_bf16 v[40:43], v[166:169], v[192:195], v[40:43]
	v_mfma_f32_16x16x32_bf16 v[36:39], v[174:177], v[192:195], v[36:39]
	v_mfma_f32_16x16x32_bf16 v[22:25], v[166:169], v[206:209], v[22:25]
	v_mfma_f32_16x16x32_bf16 v[18:21], v[174:177], v[206:209], v[18:21]
	v_mfma_f32_16x16x32_bf16 v[6:9], v[166:169], v[214:217], v[6:9]
	v_mfma_f32_16x16x32_bf16 v[2:5], v[174:177], v[214:217], v[2:5]
	s_setprio 0
	s_add_u32 s42, s42, 0x100
	s_addc_u32 s43, s43, 0
	s_add_u32 s70, s70, 0x100
	s_addc_u32 s71, s71, 0
	s_cmp_ge_i32 s72, s64
	s_mov_b32 s44, s72
	s_barrier
	s_cbranch_scc0 .LBB0_1285
	s_mov_b32 s75, 0x43800000
	s_mov_b32 s72, s82
	s_and_b64 vcc, exec, s[36:37]
	s_cbranch_vccz .LBB0_1288

; #define G8_STAGE(bufoff, gbase, voff) do { _Pragma("unroll") for (int _i = 0; _i < 2; ++_i) \
;         __builtin_amdgcn_global_load_lds((const unsigned*)((const char*)(gbase) + (voff)[_i]), (LAS unsigned*)(lds + (bufoff) + ldsw + _i * 8192), 16, 0, 0); } while (0)
; #define G8_STAGE_A(bufoff, gbase, h_, nx_) do { if constexpr (Sched::GATHER) { unsigned vo_[2]; _Pragma("unroll") for (int q_ = 0; q_ < 2; ++q_) vo_[q_] = (nx_) ? gnxt[h_][q_] : goff[h_][q_]; G8_STAGE(bufoff, gbase, vo_); } \
;         else { G8_STAGE(bufoff, (gbase) + ((h_) ? hstepA : (size_t)0), voffA); } } while (0)
; #define G8_XLDA(b, h) do { if constexpr (Epi::FP8) { G8_LD8(A8, G8_SA(b, h) + aoff, 4); } else { G8_LDA(At, b, h); } } while (0)
; #define G8_XLDB0(b, h) do { if constexpr (Epi::FP8) { G8_LD8(B08, G8_SB(b, h) + boff, 2); } else { G8_LDB(B0, b, h); } } while (0)
; #define G8_XLDB1(b, h) do { if constexpr (Epi::FP8) { G8_LD8(B18, G8_SB(b, h) + boff, 2); } else { G8_LDB(B1, b, h); } } while (0)
; #define G8_MM0(ai, bj) do { if constexpr (Epi::FP8) { G8_MMA8(ai, bj, A8, B08); } else { G8_MMA(ai, bj, At, B0); } } while (0)
; #define G8_MM1(ai, bj) do { if constexpr (Epi::FP8) { G8_MMA8(ai, bj, A8, B18); } else { G8_MMA(ai, bj, At, B1); } } while (0)
; #define G8_WAIT_L(n) asm volatile("s_waitcnt lgkmcnt(" #n ")" ::: "memory")
; #define G8_BAR __builtin_amdgcn_s_barrier()
; #define G8_SCHED __builtin_amdgcn_sched_barrier(0)
; #define G8_WAIT_VK do { if constexpr (Epi::HALFN) { G8_WAIT_V(6); } else { G8_WAIT_V(8); } } while (0)
; template <int lda, int ldb, class Epi, class Sched>
; __device__ __forceinline__ void gemm_phase(LAS unsigned char* lds, int wid, int lane, const char* baseA, const char* baseB, const Sched& S, const Epi& E) {
;     ...
;             G8_XLDB0(0, 0); if constexpr (!Epi::HALFN) { G8_XLDB1(0, 1); } G8_SCHED; G8_XLDA(0, 0); G8_STAGE_A(G8_SA(1, 1), a1, 1, false);
;             G8_WAIT_VK; G8_WAIT_L(0); G8_BAR; G8_MM0(0, 0); if constexpr (!Epi::HALFN) { G8_MM1(0, 1); } G8_BAR; G8_SCHED;
;             G8_XLDA(0, 1); G8_STAGE(G8_SB(0, 0), b2, voffB); if constexpr (!Epi::HALFN) { G8_STAGE(G8_SB(0, 1), b2 + hstepB, voffB); } G8_STAGE_A(G8_SA(0, 0), a2, 0, last);
;             G8_WAIT_VK; G8_WAIT_L(0); G8_BAR; G8_MM0(1, 0); if constexpr (!Epi::HALFN) { G8_MM1(1, 1); } G8_BAR; G8_SCHED;
.LBB0_1572:
	ds_read_b128 v[4:7], v173
	ds_read_b128 v[184:187], v174
	ds_read_b128 v[0:3], v145
	ds_read_b128 v[192:195], v147
	ds_read_b128 v[188:191], v175
	ds_read_b128 v[196:199], v176
	ds_read_b128 v[214:217], v177
	ds_read_b128 v[218:221], v178
	s_add_i32 s78, s58, 2
	s_add_u32 s60, s52, s54
	s_addc_u32 s61, s53, s55
	s_cmp_eq_u32 s77, s58
	s_cselect_b64 vcc, -1, 0
	s_and_b64 s[58:59], vcc, exec
	s_cselect_b32 s80, 0, s54
	s_cselect_b32 s79, 0, s55
	s_cselect_b32 s58, s76, s60
	s_cselect_b32 s59, s51, s61
	s_add_u32 s60, s16, s80
	s_addc_u32 s61, s17, s79
	v_lshl_add_u64 v[148:149], s[56:57], 0, v[156:157]
	s_add_i32 m0, s27, 0xc000
	ds_read_b128 v[160:163], v208
	ds_read_b128 v[164:167], v208 offset:1024
	ds_read_b128 v[222:225], v208 offset:2048
	ds_read_b128 v[226:229], v208 offset:3072
	ds_read_b128 v[230:233], v208 offset:4096
	ds_read_b128 v[234:237], v208 offset:5120
	ds_read_b128 v[238:241], v208 offset:6144
	ds_read_b128 v[242:245], v208 offset:7168
	global_load_lds_dwordx4 v[148:149], off
	v_lshl_add_u64 v[148:149], s[56:57], 0, v[158:159]
	s_add_i32 m0, s27, 0xe000
	s_nop 0
	global_load_lds_dwordx4 v[148:149], off
	s_waitcnt vmcnt(8)
	s_waitcnt lgkmcnt(0)
	s_barrier
	s_setprio 1
	s_waitcnt lgkmcnt(0)
	v_mfma_scale_f32_16x16x128_f8f6f4 v[132:135], v[0:7], v[160:167], v[132:135], v168, v168 op_sel_hi:[0,0,0]
	v_mfma_scale_f32_16x16x128_f8f6f4 v[124:127], v[184:191], v[160:167], v[124:127], v168, v168 op_sel_hi:[0,0,0]
	v_mfma_scale_f32_16x16x128_f8f6f4 v[116:119], v[0:7], v[222:229], v[116:119], v168, v168 op_sel_hi:[0,0,0]
	v_mfma_scale_f32_16x16x128_f8f6f4 v[108:111], v[184:191], v[222:229], v[108:111], v168, v168 op_sel_hi:[0,0,0]
	v_mfma_scale_f32_16x16x128_f8f6f4 v[100:103], v[0:7], v[230:237], v[100:103], v168, v168 op_sel_hi:[0,0,0]
	v_mfma_scale_f32_16x16x128_f8f6f4 v[92:95], v[184:191], v[230:237], v[92:95], v168, v168 op_sel_hi:[0,0,0]
	v_mfma_scale_f32_16x16x128_f8f6f4 v[84:87], v[0:7], v[238:245], v[84:87], v168, v168 op_sel_hi:[0,0,0]
	v_mfma_scale_f32_16x16x128_f8f6f4 v[76:79], v[184:191], v[238:245], v[76:79], v168, v168 op_sel_hi:[0,0,0]
	s_setprio 0
	s_setprio 1
	v_mfma_scale_f32_16x16x128_f8f6f4 v[136:139], v[192:199], v[160:167], v[136:139], v168, v168 op_sel_hi:[0,0,0]
	v_mfma_scale_f32_16x16x128_f8f6f4 v[128:131], v[214:221], v[160:167], v[128:131], v168, v168 op_sel_hi:[0,0,0]
	v_mfma_scale_f32_16x16x128_f8f6f4 v[120:123], v[192:199], v[222:229], v[120:123], v168, v168 op_sel_hi:[0,0,0]
	v_mfma_scale_f32_16x16x128_f8f6f4 v[112:115], v[214:221], v[222:229], v[112:115], v168, v168 op_sel_hi:[0,0,0]
	v_mfma_scale_f32_16x16x128_f8f6f4 v[104:107], v[192:199], v[230:237], v[104:107], v168, v168 op_sel_hi:[0,0,0]
	v_mfma_scale_f32_16x16x128_f8f6f4 v[96:99], v[214:221], v[230:237], v[96:99], v168, v168 op_sel_hi:[0,0,0]
	v_mfma_scale_f32_16x16x128_f8f6f4 v[88:91], v[192:199], v[238:245], v[88:91], v168, v168 op_sel_hi:[0,0,0]
	v_mfma_scale_f32_16x16x128_f8f6f4 v[80:83], v[214:221], v[238:245], v[80:83], v168, v168 op_sel_hi:[0,0,0]
	s_setprio 0
	s_barrier
	s_mov_b32 m0, s29
	v_lshl_add_u64 v[160:161], s[58:59], 0, v[142:143]
	s_add_u32 s80, s58, 0x20000
	ds_read_b128 v[222:225], v208 offset:16384
	ds_read_b128 v[226:229], v208 offset:17408
	ds_read_b128 v[230:233], v208 offset:18432
	ds_read_b128 v[234:237], v208 offset:19456
	ds_read_b128 v[238:241], v208 offset:20480
	ds_read_b128 v[242:245], v208 offset:21504
	ds_read_b128 v[148:151], v208 offset:22528
	ds_read_b128 v[152:155], v208 offset:23552
	global_load_lds_dwordx4 v[160:161], off
	v_lshl_add_u64 v[162:163], s[58:59], 0, v[140:141]
	s_mov_b32 m0, s62
	s_addc_u32 s81, s59, 0
	global_load_lds_dwordx4 v[162:163], off
	v_lshl_add_u64 v[164:165], s[80:81], 0, v[142:143]
	s_mov_b32 m0, s63
	v_cndmask_b32_e32 v30, v144, v209, vcc
	global_load_lds_dwordx4 v[164:165], off
	v_lshl_add_u64 v[164:165], s[80:81], 0, v[140:141]
	s_mov_b32 m0, s64
	v_lshl_add_u64 v[166:167], s[60:61], 0, v[30:31]
	global_load_lds_dwordx4 v[164:165], off
	s_mov_b32 m0, s27
	v_cndmask_b32_e32 v164, v146, v210, vcc
	global_load_lds_dwordx4 v30, s[60:61]
	s_mov_b32 m0, s65
	v_mov_b32_e32 v165, v31
	global_load_lds_dwordx4 v164, s[60:61]
	s_waitcnt vmcnt(8)
	s_waitcnt lgkmcnt(0)
	v_lshl_add_u64 v[164:165], s[60:61], 0, v[164:165]
	s_barrier
	s_setprio 1
	s_waitcnt lgkmcnt(0)
	v_mfma_scale_f32_16x16x128_f8f6f4 v[68:71], v[0:7], v[222:229], v[68:71], v168, v168 op_sel_hi:[0,0,0]
	v_mfma_scale_f32_16x16x128_f8f6f4 v[64:67], v[184:191], v[222:229], v[64:67], v168, v168 op_sel_hi:[0,0,0]
	v_mfma_scale_f32_16x16x128_f8f6f4 v[60:63], v[0:7], v[230:237], v[60:63], v168, v168 op_sel_hi:[0,0,0]
	v_mfma_scale_f32_16x16x128_f8f6f4 v[52:55], v[184:191], v[230:237], v[52:55], v168, v168 op_sel_hi:[0,0,0]
	v_mfma_scale_f32_16x16x128_f8f6f4 v[44:47], v[0:7], v[238:245], v[44:47], v168, v168 op_sel_hi:[0,0,0]
	v_mfma_scale_f32_16x16x128_f8f6f4 v[32:35], v[184:191], v[238:245], v[32:35], v168, v168 op_sel_hi:[0,0,0]
	v_mfma_scale_f32_16x16x128_f8f6f4 v[22:25], v[0:7], v[148:155], v[22:25], v168, v168 op_sel_hi:[0,0,0]
	v_mfma_scale_f32_16x16x128_f8f6f4 v[14:17], v[184:191], v[148:155], v[14:17], v168, v168 op_sel_hi:[0,0,0]
	s_setprio 0
	s_setprio 1
	v_mfma_scale_f32_16x16x128_f8f6f4 v[72:75], v[192:199], v[222:229], v[72:75], v168, v168 op_sel_hi:[0,0,0]
	v_mfma_scale_f32_16x16x128_f8f6f4 v[36:39], v[214:221], v[222:229], v[36:39], v168, v168 op_sel_hi:[0,0,0]
	v_mfma_scale_f32_16x16x128_f8f6f4 v[56:59], v[192:199], v[230:237], v[56:59], v168, v168 op_sel_hi:[0,0,0]
	v_mfma_scale_f32_16x16x128_f8f6f4 v[48:51], v[214:221], v[230:237], v[48:51], v168, v168 op_sel_hi:[0,0,0]
	v_mfma_scale_f32_16x16x128_f8f6f4 v[40:43], v[192:199], v[238:245], v[40:43], v168, v168 op_sel_hi:[0,0,0]
	v_mfma_scale_f32_16x16x128_f8f6f4 v[26:29], v[214:221], v[238:245], v[26:29], v168, v168 op_sel_hi:[0,0,0]
	v_mfma_scale_f32_16x16x128_f8f6f4 v[18:21], v[192:199], v[148:155], v[18:21], v168, v168 op_sel_hi:[0,0,0]
	v_mfma_scale_f32_16x16x128_f8f6f4 v[10:13], v[214:221], v[148:155], v[10:13], v168, v168 op_sel_hi:[0,0,0]
	s_setprio 0
	s_barrier
; #define G8_STAGE(bufoff, gbase, voff) do { _Pragma("unroll") for (int _i = 0; _i < 2; ++_i) \
;         __builtin_amdgcn_global_load_lds((const unsigned*)((const char*)(gbase) + (voff)[_i]), (LAS unsigned*)(lds + (bufoff) + ldsw + _i * 8192), 16, 0, 0); } while (0)
; #define G8_STAGE_A(bufoff, gbase, h_, nx_) do { if constexpr (Sched::GATHER) { unsigned vo_[2]; _Pragma("unroll") for (int q_ = 0; q_ < 2; ++q_) vo_[q_] = (nx_) ? gnxt[h_][q_] : goff[h_][q_]; G8_STAGE(bufoff, gbase, vo_); } \
;         else { G8_STAGE(bufoff, (gbase) + ((h_) ? hstepA : (size_t)0), voffA); } } while (0)
; #define G8_XLDA(b, h) do { if constexpr (Epi::FP8) { G8_LD8(A8, G8_SA(b, h) + aoff, 4); } else { G8_LDA(At, b, h); } } while (0)
; #define G8_XLDB0(b, h) do { if constexpr (Epi::FP8) { G8_LD8(B08, G8_SB(b, h) + boff, 2); } else { G8_LDB(B0, b, h); } } while (0)
; #define G8_XLDB1(b, h) do { if constexpr (Epi::FP8) { G8_LD8(B18, G8_SB(b, h) + boff, 2); } else { G8_LDB(B1, b, h); } } while (0)
; #define G8_MM0(ai, bj) do { if constexpr (Epi::FP8) { G8_MMA8(ai, bj, A8, B08); } else { G8_MMA(ai, bj, At, B0); } } while (0)
; #define G8_MM1(ai, bj) do { if constexpr (Epi::FP8) { G8_MMA8(ai, bj, A8, B18); } else { G8_MMA(ai, bj, At, B1); } } while (0)
; #define G8_WAIT_L(n) asm volatile("s_waitcnt lgkmcnt(" #n ")" ::: "memory")
; #define G8_BAR __builtin_amdgcn_s_barrier()
; #define G8_SCHED __builtin_amdgcn_sched_barrier(0)
; #define G8_WAIT_VK do { if constexpr (Epi::HALFN) { G8_WAIT_V(6); } else { G8_WAIT_V(8); } } while (0)
; template <int lda, int ldb, class Epi, class Sched>
; __device__ __forceinline__ void gemm_phase(LAS unsigned char* lds, int wid, int lane, const char* baseA, const char* baseB, const Sched& S, const Epi& E) {
;     ...
;             G8_XLDB0(1, 0); if constexpr (!Epi::HALFN) { G8_XLDB1(1, 1); } G8_SCHED; G8_XLDA(1, 0); G8_STAGE_A(G8_SA(0, 1), a2, 1, last);
;             G8_WAIT_VK; G8_WAIT_L(0); G8_BAR; G8_MM0(0, 0); if constexpr (!Epi::HALFN) { G8_MM1(0, 1); } G8_BAR; G8_SCHED;
;             G8_XLDA(1, 1); G8_STAGE(G8_SB(1, 0), b3, voffB); if constexpr (!Epi::HALFN) { G8_STAGE(G8_SB(1, 1), b3 + hstepB, voffB); } G8_STAGE_A(G8_SA(1, 0), a3, 0, last);
;             G8_WAIT_VK; G8_WAIT_L(0); G8_BAR; G8_MM0(1, 0); if constexpr (!Epi::HALFN) { G8_MM1(1, 1); } G8_BAR; G8_SCHED;
;         }
	ds_read_b128 v[152:155], v179
	ds_read_b128 v[184:187], v180
	ds_read_b128 v[148:151], v171
	ds_read_b128 v[0:3], v172
	ds_read_b128 v[188:191], v181
	ds_read_b128 v[4:7], v205
	ds_read_b128 v[192:195], v206
	ds_read_b128 v[196:199], v207
	s_mov_b32 m0, s66
	v_cndmask_b32_e32 v9, v156, v211, vcc
	ds_read_b128 v[214:217], v208 offset:32768
	ds_read_b128 v[218:221], v208 offset:33792
	ds_read_b128 v[222:225], v208 offset:34816
	ds_read_b128 v[226:229], v208 offset:35840
	ds_read_b128 v[230:233], v208 offset:36864
	ds_read_b128 v[234:237], v208 offset:37888
	ds_read_b128 v[238:241], v208 offset:38912
	ds_read_b128 v[242:245], v208 offset:39936
	v_cndmask_b32_e32 v30, v158, v212, vcc
	global_load_lds_dwordx4 v9, s[60:61]
	s_mov_b32 m0, s67
	s_nop 0
	global_load_lds_dwordx4 v30, s[60:61]
	s_waitcnt vmcnt(8)
	s_waitcnt lgkmcnt(0)
	s_barrier
	s_setprio 1
	s_waitcnt lgkmcnt(0)
	v_mfma_scale_f32_16x16x128_f8f6f4 v[132:135], v[148:155], v[214:221], v[132:135], v168, v168 op_sel_hi:[0,0,0]
	v_mfma_scale_f32_16x16x128_f8f6f4 v[124:127], v[184:191], v[214:221], v[124:127], v168, v168 op_sel_hi:[0,0,0]
	v_mfma_scale_f32_16x16x128_f8f6f4 v[116:119], v[148:155], v[222:229], v[116:119], v168, v168 op_sel_hi:[0,0,0]
	v_mfma_scale_f32_16x16x128_f8f6f4 v[108:111], v[184:191], v[222:229], v[108:111], v168, v168 op_sel_hi:[0,0,0]
	v_mfma_scale_f32_16x16x128_f8f6f4 v[100:103], v[148:155], v[230:237], v[100:103], v168, v168 op_sel_hi:[0,0,0]
	v_mfma_scale_f32_16x16x128_f8f6f4 v[92:95], v[184:191], v[230:237], v[92:95], v168, v168 op_sel_hi:[0,0,0]
	v_mfma_scale_f32_16x16x128_f8f6f4 v[84:87], v[148:155], v[238:245], v[84:87], v168, v168 op_sel_hi:[0,0,0]
	v_mfma_scale_f32_16x16x128_f8f6f4 v[76:79], v[184:191], v[238:245], v[76:79], v168, v168 op_sel_hi:[0,0,0]
	s_setprio 0
	s_setprio 1
	v_mfma_scale_f32_16x16x128_f8f6f4 v[136:139], v[0:7], v[214:221], v[136:139], v168, v168 op_sel_hi:[0,0,0]
	v_mfma_scale_f32_16x16x128_f8f6f4 v[128:131], v[192:199], v[214:221], v[128:131], v168, v168 op_sel_hi:[0,0,0]
	v_mfma_scale_f32_16x16x128_f8f6f4 v[120:123], v[0:7], v[222:229], v[120:123], v168, v168 op_sel_hi:[0,0,0]
	v_mfma_scale_f32_16x16x128_f8f6f4 v[112:115], v[192:199], v[222:229], v[112:115], v168, v168 op_sel_hi:[0,0,0]
	v_mfma_scale_f32_16x16x128_f8f6f4 v[104:107], v[0:7], v[230:237], v[104:107], v168, v168 op_sel_hi:[0,0,0]
	v_mfma_scale_f32_16x16x128_f8f6f4 v[96:99], v[192:199], v[230:237], v[96:99], v168, v168 op_sel_hi:[0,0,0]
	v_mfma_scale_f32_16x16x128_f8f6f4 v[88:91], v[0:7], v[238:245], v[88:91], v168, v168 op_sel_hi:[0,0,0]
	v_mfma_scale_f32_16x16x128_f8f6f4 v[80:83], v[192:199], v[238:245], v[80:83], v168, v168 op_sel_hi:[0,0,0]
	s_setprio 0
	s_barrier
	s_mov_b32 m0, s68
	v_lshl_add_u64 v[160:161], v[160:161], 0, s[22:23]
	s_add_u32 s58, s58, 0x20080
	ds_read_b128 v[214:217], v208 offset:49152
	ds_read_b128 v[218:221], v208 offset:50176
	ds_read_b128 v[222:225], v208 offset:51200
	ds_read_b128 v[226:229], v208 offset:52224
	ds_read_b128 v[230:233], v208 offset:53248
	ds_read_b128 v[234:237], v208 offset:54272
	ds_read_b128 v[238:241], v208 offset:55296
	ds_read_b128 v[242:245], v208 offset:56320
	global_load_lds_dwordx4 v[160:161], off
	v_lshl_add_u64 v[160:161], v[162:163], 0, s[22:23]
	s_mov_b32 m0, s69
	s_addc_u32 s59, s59, 0
	global_load_lds_dwordx4 v[160:161], off
	v_lshl_add_u64 v[160:161], s[58:59], 0, v[142:143]
	s_mov_b32 m0, s72
	s_nop 0
	global_load_lds_dwordx4 v[160:161], off
	v_lshl_add_u64 v[160:161], s[58:59], 0, v[140:141]
	s_mov_b32 m0, s73
	s_nop 0
	global_load_lds_dwordx4 v[160:161], off
	v_lshl_add_u64 v[160:161], v[166:167], 0, s[22:23]
	s_mov_b32 m0, s70
	s_nop 0
	global_load_lds_dwordx4 v[160:161], off
	v_lshl_add_u64 v[160:161], v[164:165], 0, s[22:23]
	s_mov_b32 m0, s71
	s_nop 0
	global_load_lds_dwordx4 v[160:161], off
	s_waitcnt vmcnt(8)
	s_waitcnt lgkmcnt(0)
	s_barrier
	s_setprio 1
	s_waitcnt lgkmcnt(0)
	v_mfma_scale_f32_16x16x128_f8f6f4 v[68:71], v[148:155], v[214:221], v[68:71], v168, v168 op_sel_hi:[0,0,0]
	v_mfma_scale_f32_16x16x128_f8f6f4 v[64:67], v[184:191], v[214:221], v[64:67], v168, v168 op_sel_hi:[0,0,0]
	v_mfma_scale_f32_16x16x128_f8f6f4 v[60:63], v[148:155], v[222:229], v[60:63], v168, v168 op_sel_hi:[0,0,0]
	v_mfma_scale_f32_16x16x128_f8f6f4 v[52:55], v[184:191], v[222:229], v[52:55], v168, v168 op_sel_hi:[0,0,0]
	v_mfma_scale_f32_16x16x128_f8f6f4 v[44:47], v[148:155], v[230:237], v[44:47], v168, v168 op_sel_hi:[0,0,0]
	v_mfma_scale_f32_16x16x128_f8f6f4 v[32:35], v[184:191], v[230:237], v[32:35], v168, v168 op_sel_hi:[0,0,0]
	v_mfma_scale_f32_16x16x128_f8f6f4 v[22:25], v[148:155], v[238:245], v[22:25], v168, v168 op_sel_hi:[0,0,0]
	v_mfma_scale_f32_16x16x128_f8f6f4 v[14:17], v[184:191], v[238:245], v[14:17], v168, v168 op_sel_hi:[0,0,0]
	s_setprio 0
	s_setprio 1
	v_mfma_scale_f32_16x16x128_f8f6f4 v[72:75], v[0:7], v[214:221], v[72:75], v168, v168 op_sel_hi:[0,0,0]
	v_mfma_scale_f32_16x16x128_f8f6f4 v[36:39], v[192:199], v[214:221], v[36:39], v168, v168 op_sel_hi:[0,0,0]
	v_mfma_scale_f32_16x16x128_f8f6f4 v[56:59], v[0:7], v[222:229], v[56:59], v168, v168 op_sel_hi:[0,0,0]
	v_mfma_scale_f32_16x16x128_f8f6f4 v[48:51], v[192:199], v[222:229], v[48:51], v168, v168 op_sel_hi:[0,0,0]
	v_mfma_scale_f32_16x16x128_f8f6f4 v[40:43], v[0:7], v[230:237], v[40:43], v168, v168 op_sel_hi:[0,0,0]
	v_mfma_scale_f32_16x16x128_f8f6f4 v[26:29], v[192:199], v[230:237], v[26:29], v168, v168 op_sel_hi:[0,0,0]
	v_mfma_scale_f32_16x16x128_f8f6f4 v[18:21], v[0:7], v[238:245], v[18:21], v168, v168 op_sel_hi:[0,0,0]
	v_mfma_scale_f32_16x16x128_f8f6f4 v[10:13], v[192:199], v[238:245], v[10:13], v168, v168 op_sel_hi:[0,0,0]
	s_setprio 0
	s_add_u32 s54, s54, 0x100
	s_addc_u32 s55, s55, 0
	s_add_u32 s56, s56, 0x100
	s_addc_u32 s57, s57, 0
	s_cmp_ge_i32 s78, s31
	s_mov_b32 s58, s78
	s_barrier
	s_cbranch_scc0 .LBB0_1572
	s_mov_b32 s76, 0x9800
	s_and_b64 vcc, exec, s[36:37]
	s_cbranch_vccz .LBB0_1575

; #define G8_STAGE(bufoff, gbase, voff) do { _Pragma("unroll") for (int _i = 0; _i < 2; ++_i) \
;         __builtin_amdgcn_global_load_lds((const unsigned*)((const char*)(gbase) + (voff)[_i]), (LAS unsigned*)(lds + (bufoff) + ldsw + _i * 8192), 16, 0, 0); } while (0)
; #define G8_STAGE_A(bufoff, gbase, h_, nx_) do { if constexpr (Sched::GATHER) { unsigned vo_[2]; _Pragma("unroll") for (int q_ = 0; q_ < 2; ++q_) vo_[q_] = (nx_) ? gnxt[h_][q_] : goff[h_][q_]; G8_STAGE(bufoff, gbase, vo_); } \
;         else { G8_STAGE(bufoff, (gbase) + ((h_) ? hstepA : (size_t)0), voffA); } } while (0)
; #define G8_XLDA(b, h) do { if constexpr (Epi::FP8) { G8_LD8(A8, G8_SA(b, h) + aoff, 4); } else { G8_LDA(At, b, h); } } while (0)
; #define G8_XLDB0(b, h) do { if constexpr (Epi::FP8) { G8_LD8(B08, G8_SB(b, h) + boff, 2); } else { G8_LDB(B0, b, h); } } while (0)
; #define G8_XLDB1(b, h) do { if constexpr (Epi::FP8) { G8_LD8(B18, G8_SB(b, h) + boff, 2); } else { G8_LDB(B1, b, h); } } while (0)
; #define G8_MM0(ai, bj) do { if constexpr (Epi::FP8) { G8_MMA8(ai, bj, A8, B08); } else { G8_MMA(ai, bj, At, B0); } } while (0)
; #define G8_MM1(ai, bj) do { if constexpr (Epi::FP8) { G8_MMA8(ai, bj, A8, B18); } else { G8_MMA(ai, bj, At, B1); } } while (0)
; #define G8_WAIT_L(n) asm volatile("s_waitcnt lgkmcnt(" #n ")" ::: "memory")
; #define G8_BAR __builtin_amdgcn_s_barrier()
; #define G8_SCHED __builtin_amdgcn_sched_barrier(0)
; #define G8_WAIT_VK do { if constexpr (Epi::HALFN) { G8_WAIT_V(6); } else { G8_WAIT_V(8); } } while (0)
; template <int lda, int ldb, class Epi, class Sched>
; __device__ __forceinline__ void gemm_phase(LAS unsigned char* lds, int wid, int lane, const char* baseA, const char* baseB, const Sched& S, const Epi& E) {
;     ...
;             G8_XLDB0(0, 0); if constexpr (!Epi::HALFN) { G8_XLDB1(0, 1); } G8_SCHED; G8_XLDA(0, 0); G8_STAGE_A(G8_SA(1, 1), a1, 1, false);
;             G8_WAIT_VK; G8_WAIT_L(0); G8_BAR; G8_MM0(0, 0); if constexpr (!Epi::HALFN) { G8_MM1(0, 1); } G8_BAR; G8_SCHED;
;             G8_XLDA(0, 1); G8_STAGE(G8_SB(0, 0), b2, voffB); if constexpr (!Epi::HALFN) { G8_STAGE(G8_SB(0, 1), b2 + hstepB, voffB); } G8_STAGE_A(G8_SA(0, 0), a2, 0, last);
;             G8_WAIT_VK; G8_WAIT_L(0); G8_BAR; G8_MM0(1, 0); if constexpr (!Epi::HALFN) { G8_MM1(1, 1); } G8_BAR; G8_SCHED;
.LBB0_1728:
	ds_read_b128 v[4:7], v178
	ds_read_b128 v[8:11], v179
	ds_read_b128 v[0:3], v148
	ds_read_b128 v[184:187], v151
	ds_read_b128 v[12:15], v180
	ds_read_b128 v[188:191], v181
	ds_read_b128 v[192:195], v205
	ds_read_b128 v[196:199], v206
	s_add_i32 s77, s50, 2
	s_add_u32 s51, s46, 0xffff8080
	s_addc_u32 s52, s47, -1
	s_cmp_eq_u32 s74, s50
	s_cselect_b32 s50, s73, s75
	s_cselect_b32 s53, s70, s52
	s_cselect_b32 s52, s71, s51
	s_cselect_b32 s51, s72, s76
	v_lshl_add_u64 v[152:153], s[46:47], 0, v[164:165]
	s_add_i32 m0, s27, 0xc000
	ds_read_b128 v[168:171], v213
	ds_read_b128 v[172:175], v213 offset:1024
	ds_read_b128 v[214:217], v213 offset:2048
	ds_read_b128 v[218:221], v213 offset:3072
	ds_read_b128 v[222:225], v213 offset:4096
	ds_read_b128 v[226:229], v213 offset:5120
	ds_read_b128 v[230:233], v213 offset:6144
	ds_read_b128 v[234:237], v213 offset:7168
	global_load_lds_dwordx4 v[152:153], off
	v_lshl_add_u64 v[152:153], s[46:47], 0, v[166:167]
	s_add_i32 m0, s27, 0xe000
	s_nop 0
	global_load_lds_dwordx4 v[152:153], off
	s_waitcnt vmcnt(8)
	s_waitcnt lgkmcnt(0)
	s_barrier
	s_setprio 1
	s_waitcnt lgkmcnt(0)
	v_mfma_scale_f32_16x16x128_f8f6f4 v[144:147], v[0:7], v[168:175], v[144:147], v30, v30 op_sel_hi:[0,0,0]
	v_mfma_scale_f32_16x16x128_f8f6f4 v[140:143], v[8:15], v[168:175], v[140:143], v30, v30 op_sel_hi:[0,0,0]
	v_mfma_scale_f32_16x16x128_f8f6f4 v[128:131], v[0:7], v[214:221], v[128:131], v30, v30 op_sel_hi:[0,0,0]
	v_mfma_scale_f32_16x16x128_f8f6f4 v[124:127], v[8:15], v[214:221], v[124:127], v30, v30 op_sel_hi:[0,0,0]
	v_mfma_scale_f32_16x16x128_f8f6f4 v[112:115], v[0:7], v[222:229], v[112:115], v30, v30 op_sel_hi:[0,0,0]
	v_mfma_scale_f32_16x16x128_f8f6f4 v[108:111], v[8:15], v[222:229], v[108:111], v30, v30 op_sel_hi:[0,0,0]
	v_mfma_scale_f32_16x16x128_f8f6f4 v[96:99], v[0:7], v[230:237], v[96:99], v30, v30 op_sel_hi:[0,0,0]
	v_mfma_scale_f32_16x16x128_f8f6f4 v[92:95], v[8:15], v[230:237], v[92:95], v30, v30 op_sel_hi:[0,0,0]
	s_setprio 0
	s_setprio 1
	v_mfma_scale_f32_16x16x128_f8f6f4 v[136:139], v[184:191], v[168:175], v[136:139], v30, v30 op_sel_hi:[0,0,0]
	v_mfma_scale_f32_16x16x128_f8f6f4 v[132:135], v[192:199], v[168:175], v[132:135], v30, v30 op_sel_hi:[0,0,0]
	v_mfma_scale_f32_16x16x128_f8f6f4 v[120:123], v[184:191], v[214:221], v[120:123], v30, v30 op_sel_hi:[0,0,0]
	v_mfma_scale_f32_16x16x128_f8f6f4 v[116:119], v[192:199], v[214:221], v[116:119], v30, v30 op_sel_hi:[0,0,0]
	v_mfma_scale_f32_16x16x128_f8f6f4 v[104:107], v[184:191], v[222:229], v[104:107], v30, v30 op_sel_hi:[0,0,0]
	v_mfma_scale_f32_16x16x128_f8f6f4 v[100:103], v[192:199], v[222:229], v[100:103], v30, v30 op_sel_hi:[0,0,0]
	v_mfma_scale_f32_16x16x128_f8f6f4 v[88:91], v[184:191], v[230:237], v[88:91], v30, v30 op_sel_hi:[0,0,0]
	v_mfma_scale_f32_16x16x128_f8f6f4 v[84:87], v[192:199], v[230:237], v[84:87], v30, v30 op_sel_hi:[0,0,0]
	s_setprio 0
	s_barrier
	s_mov_b32 m0, s31
	v_lshl_add_u64 v[168:169], s[50:51], 0, v[160:161]
	s_add_u32 s78, s50, 0x8000
	ds_read_b128 v[214:217], v213 offset:16384
	ds_read_b128 v[218:221], v213 offset:17408
	ds_read_b128 v[222:225], v213 offset:18432
	ds_read_b128 v[226:229], v213 offset:19456
	ds_read_b128 v[230:233], v213 offset:20480
	ds_read_b128 v[234:237], v213 offset:21504
	ds_read_b128 v[238:241], v213 offset:22528
	ds_read_b128 v[242:245], v213 offset:23552
	global_load_lds_dwordx4 v[168:169], off
	v_lshl_add_u64 v[170:171], s[50:51], 0, v[156:157]
	s_mov_b32 m0, s54
	s_addc_u32 s79, s51, 0
	global_load_lds_dwordx4 v[170:171], off
	v_lshl_add_u64 v[152:153], s[78:79], 0, v[160:161]
	s_mov_b32 m0, s55
	v_lshl_add_u64 v[172:173], s[52:53], 0, v[162:163]
	global_load_lds_dwordx4 v[152:153], off
	v_lshl_add_u64 v[152:153], s[78:79], 0, v[156:157]
	s_mov_b32 m0, s56
	v_lshl_add_u64 v[174:175], s[52:53], 0, v[158:159]
	global_load_lds_dwordx4 v[152:153], off
	s_mov_b32 m0, s27
	s_nop 0
	global_load_lds_dwordx4 v[172:173], off
	s_mov_b32 m0, s57
	s_nop 0
	global_load_lds_dwordx4 v[174:175], off
	s_waitcnt vmcnt(8)
	s_waitcnt lgkmcnt(0)
	s_barrier
	s_setprio 1
	s_waitcnt lgkmcnt(0)
	v_mfma_scale_f32_16x16x128_f8f6f4 v[80:83], v[0:7], v[214:221], v[80:83], v30, v30 op_sel_hi:[0,0,0]
	v_mfma_scale_f32_16x16x128_f8f6f4 v[76:79], v[8:15], v[214:221], v[76:79], v30, v30 op_sel_hi:[0,0,0]
	v_mfma_scale_f32_16x16x128_f8f6f4 v[64:67], v[0:7], v[222:229], v[64:67], v30, v30 op_sel_hi:[0,0,0]
	v_mfma_scale_f32_16x16x128_f8f6f4 v[60:63], v[8:15], v[222:229], v[60:63], v30, v30 op_sel_hi:[0,0,0]
	v_mfma_scale_f32_16x16x128_f8f6f4 v[48:51], v[0:7], v[230:237], v[48:51], v30, v30 op_sel_hi:[0,0,0]
	v_mfma_scale_f32_16x16x128_f8f6f4 v[44:47], v[8:15], v[230:237], v[44:47], v30, v30 op_sel_hi:[0,0,0]
	v_mfma_scale_f32_16x16x128_f8f6f4 v[32:35], v[0:7], v[238:245], v[32:35], v30, v30 op_sel_hi:[0,0,0]
	v_mfma_scale_f32_16x16x128_f8f6f4 v[26:29], v[8:15], v[238:245], v[26:29], v30, v30 op_sel_hi:[0,0,0]
	s_setprio 0
	s_setprio 1
	v_mfma_scale_f32_16x16x128_f8f6f4 v[72:75], v[184:191], v[214:221], v[72:75], v30, v30 op_sel_hi:[0,0,0]
	v_mfma_scale_f32_16x16x128_f8f6f4 v[68:71], v[192:199], v[214:221], v[68:71], v30, v30 op_sel_hi:[0,0,0]
	v_mfma_scale_f32_16x16x128_f8f6f4 v[56:59], v[184:191], v[222:229], v[56:59], v30, v30 op_sel_hi:[0,0,0]
	v_mfma_scale_f32_16x16x128_f8f6f4 v[52:55], v[192:199], v[222:229], v[52:55], v30, v30 op_sel_hi:[0,0,0]
	v_mfma_scale_f32_16x16x128_f8f6f4 v[40:43], v[184:191], v[230:237], v[40:43], v30, v30 op_sel_hi:[0,0,0]
	v_mfma_scale_f32_16x16x128_f8f6f4 v[36:39], v[192:199], v[230:237], v[36:39], v30, v30 op_sel_hi:[0,0,0]
	v_mfma_scale_f32_16x16x128_f8f6f4 v[22:25], v[184:191], v[238:245], v[22:25], v30, v30 op_sel_hi:[0,0,0]
	v_mfma_scale_f32_16x16x128_f8f6f4 v[16:19], v[192:199], v[238:245], v[16:19], v30, v30 op_sel_hi:[0,0,0]
	s_setprio 0
	s_barrier
; #define G8_STAGE(bufoff, gbase, voff) do { _Pragma("unroll") for (int _i = 0; _i < 2; ++_i) \
;         __builtin_amdgcn_global_load_lds((const unsigned*)((const char*)(gbase) + (voff)[_i]), (LAS unsigned*)(lds + (bufoff) + ldsw + _i * 8192), 16, 0, 0); } while (0)
; #define G8_STAGE_A(bufoff, gbase, h_, nx_) do { if constexpr (Sched::GATHER) { unsigned vo_[2]; _Pragma("unroll") for (int q_ = 0; q_ < 2; ++q_) vo_[q_] = (nx_) ? gnxt[h_][q_] : goff[h_][q_]; G8_STAGE(bufoff, gbase, vo_); } \
;         else { G8_STAGE(bufoff, (gbase) + ((h_) ? hstepA : (size_t)0), voffA); } } while (0)
; #define G8_XLDA(b, h) do { if constexpr (Epi::FP8) { G8_LD8(A8, G8_SA(b, h) + aoff, 4); } else { G8_LDA(At, b, h); } } while (0)
; #define G8_XLDB0(b, h) do { if constexpr (Epi::FP8) { G8_LD8(B08, G8_SB(b, h) + boff, 2); } else { G8_LDB(B0, b, h); } } while (0)
; #define G8_XLDB1(b, h) do { if constexpr (Epi::FP8) { G8_LD8(B18, G8_SB(b, h) + boff, 2); } else { G8_LDB(B1, b, h); } } while (0)
; #define G8_MM0(ai, bj) do { if constexpr (Epi::FP8) { G8_MMA8(ai, bj, A8, B08); } else { G8_MMA(ai, bj, At, B0); } } while (0)
; #define G8_MM1(ai, bj) do { if constexpr (Epi::FP8) { G8_MMA8(ai, bj, A8, B18); } else { G8_MMA(ai, bj, At, B1); } } while (0)
; #define G8_WAIT_L(n) asm volatile("s_waitcnt lgkmcnt(" #n ")" ::: "memory")
; #define G8_BAR __builtin_amdgcn_s_barrier()
; #define G8_SCHED __builtin_amdgcn_sched_barrier(0)
; #define G8_WAIT_VK do { if constexpr (Epi::HALFN) { G8_WAIT_V(6); } else { G8_WAIT_V(8); } } while (0)
; template <int lda, int ldb, class Epi, class Sched>
; __device__ __forceinline__ void gemm_phase(LAS unsigned char* lds, int wid, int lane, const char* baseA, const char* baseB, const Sched& S, const Epi& E) {
;     ...
;             G8_XLDB0(1, 0); if constexpr (!Epi::HALFN) { G8_XLDB1(1, 1); } G8_SCHED; G8_XLDA(1, 0); G8_STAGE_A(G8_SA(0, 1), a2, 1, last);
;             G8_WAIT_VK; G8_WAIT_L(0); G8_BAR; G8_MM0(0, 0); if constexpr (!Epi::HALFN) { G8_MM1(0, 1); } G8_BAR; G8_SCHED;
;             G8_XLDA(1, 1); G8_STAGE(G8_SB(1, 0), b3, voffB); if constexpr (!Epi::HALFN) { G8_STAGE(G8_SB(1, 1), b3 + hstepB, voffB); } G8_STAGE_A(G8_SA(1, 0), a3, 0, last);
;             G8_WAIT_VK; G8_WAIT_L(0); G8_BAR; G8_MM0(1, 0); if constexpr (!Epi::HALFN) { G8_MM1(1, 1); } G8_BAR; G8_SCHED;
;         }
	ds_read_b128 v[12:15], v207
	ds_read_b128 v[184:187], v208
	ds_read_b128 v[8:11], v176
	ds_read_b128 v[0:3], v177
	ds_read_b128 v[188:191], v209
	ds_read_b128 v[4:7], v210
	ds_read_b128 v[192:195], v211
	ds_read_b128 v[196:199], v212
	s_add_u32 s52, s52, 0x8000
	s_addc_u32 s53, s53, 0
	s_mov_b32 m0, s58
	v_lshl_add_u64 v[152:153], s[52:53], 0, v[162:163]
	ds_read_b128 v[214:217], v213 offset:32768
	ds_read_b128 v[218:221], v213 offset:33792
	ds_read_b128 v[222:225], v213 offset:34816
	ds_read_b128 v[226:229], v213 offset:35840
	ds_read_b128 v[230:233], v213 offset:36864
	ds_read_b128 v[234:237], v213 offset:37888
	ds_read_b128 v[238:241], v213 offset:38912
	ds_read_b128 v[242:245], v213 offset:39936
	global_load_lds_dwordx4 v[152:153], off
	v_lshl_add_u64 v[152:153], s[52:53], 0, v[158:159]
	s_mov_b32 m0, s59
	s_nop 0
	global_load_lds_dwordx4 v[152:153], off
	s_waitcnt vmcnt(8)
	s_waitcnt lgkmcnt(0)
	s_barrier
	s_setprio 1
	s_waitcnt lgkmcnt(0)
	v_mfma_scale_f32_16x16x128_f8f6f4 v[144:147], v[8:15], v[214:221], v[144:147], v30, v30 op_sel_hi:[0,0,0]
	v_mfma_scale_f32_16x16x128_f8f6f4 v[140:143], v[184:191], v[214:221], v[140:143], v30, v30 op_sel_hi:[0,0,0]
	v_mfma_scale_f32_16x16x128_f8f6f4 v[128:131], v[8:15], v[222:229], v[128:131], v30, v30 op_sel_hi:[0,0,0]
	v_mfma_scale_f32_16x16x128_f8f6f4 v[124:127], v[184:191], v[222:229], v[124:127], v30, v30 op_sel_hi:[0,0,0]
	v_mfma_scale_f32_16x16x128_f8f6f4 v[112:115], v[8:15], v[230:237], v[112:115], v30, v30 op_sel_hi:[0,0,0]
	v_mfma_scale_f32_16x16x128_f8f6f4 v[108:111], v[184:191], v[230:237], v[108:111], v30, v30 op_sel_hi:[0,0,0]
	v_mfma_scale_f32_16x16x128_f8f6f4 v[96:99], v[8:15], v[238:245], v[96:99], v30, v30 op_sel_hi:[0,0,0]
	v_mfma_scale_f32_16x16x128_f8f6f4 v[92:95], v[184:191], v[238:245], v[92:95], v30, v30 op_sel_hi:[0,0,0]
	s_setprio 0
	s_setprio 1
	v_mfma_scale_f32_16x16x128_f8f6f4 v[136:139], v[0:7], v[214:221], v[136:139], v30, v30 op_sel_hi:[0,0,0]
	v_mfma_scale_f32_16x16x128_f8f6f4 v[132:135], v[192:199], v[214:221], v[132:135], v30, v30 op_sel_hi:[0,0,0]
	v_mfma_scale_f32_16x16x128_f8f6f4 v[120:123], v[0:7], v[222:229], v[120:123], v30, v30 op_sel_hi:[0,0,0]
	v_mfma_scale_f32_16x16x128_f8f6f4 v[116:119], v[192:199], v[222:229], v[116:119], v30, v30 op_sel_hi:[0,0,0]
	v_mfma_scale_f32_16x16x128_f8f6f4 v[104:107], v[0:7], v[230:237], v[104:107], v30, v30 op_sel_hi:[0,0,0]
	v_mfma_scale_f32_16x16x128_f8f6f4 v[100:103], v[192:199], v[230:237], v[100:103], v30, v30 op_sel_hi:[0,0,0]
	v_mfma_scale_f32_16x16x128_f8f6f4 v[88:91], v[0:7], v[238:245], v[88:91], v30, v30 op_sel_hi:[0,0,0]
	v_mfma_scale_f32_16x16x128_f8f6f4 v[84:87], v[192:199], v[238:245], v[84:87], v30, v30 op_sel_hi:[0,0,0]
	s_setprio 0
	s_barrier
	s_mov_b32 m0, s60
	v_lshl_add_u64 v[152:153], v[168:169], 0, s[22:23]
	s_add_u32 s50, s50, 0x8080
	ds_read_b128 v[214:217], v213 offset:49152
	ds_read_b128 v[218:221], v213 offset:50176
	ds_read_b128 v[222:225], v213 offset:51200
	ds_read_b128 v[226:229], v213 offset:52224
	ds_read_b128 v[230:233], v213 offset:53248
	ds_read_b128 v[234:237], v213 offset:54272
	ds_read_b128 v[238:241], v213 offset:55296
	ds_read_b128 v[242:245], v213 offset:56320
	global_load_lds_dwordx4 v[152:153], off
	v_lshl_add_u64 v[152:153], v[170:171], 0, s[22:23]
	s_mov_b32 m0, s61
	s_addc_u32 s51, s51, 0
	global_load_lds_dwordx4 v[152:153], off
	v_lshl_add_u64 v[152:153], s[50:51], 0, v[160:161]
	s_mov_b32 m0, s64
	s_nop 0
	global_load_lds_dwordx4 v[152:153], off
	v_lshl_add_u64 v[152:153], s[50:51], 0, v[156:157]
	s_mov_b32 m0, s65
	s_nop 0
	global_load_lds_dwordx4 v[152:153], off
	v_lshl_add_u64 v[152:153], v[172:173], 0, s[22:23]
	s_mov_b32 m0, s62
	s_nop 0
	global_load_lds_dwordx4 v[152:153], off
	v_lshl_add_u64 v[152:153], v[174:175], 0, s[22:23]
	s_mov_b32 m0, s63
	s_nop 0
	global_load_lds_dwordx4 v[152:153], off
	s_waitcnt vmcnt(8)
	s_waitcnt lgkmcnt(0)
	s_barrier
	s_setprio 1
	s_waitcnt lgkmcnt(0)
	v_mfma_scale_f32_16x16x128_f8f6f4 v[80:83], v[8:15], v[214:221], v[80:83], v30, v30 op_sel_hi:[0,0,0]
	v_mfma_scale_f32_16x16x128_f8f6f4 v[76:79], v[184:191], v[214:221], v[76:79], v30, v30 op_sel_hi:[0,0,0]
	v_mfma_scale_f32_16x16x128_f8f6f4 v[64:67], v[8:15], v[222:229], v[64:67], v30, v30 op_sel_hi:[0,0,0]
	v_mfma_scale_f32_16x16x128_f8f6f4 v[60:63], v[184:191], v[222:229], v[60:63], v30, v30 op_sel_hi:[0,0,0]
	v_mfma_scale_f32_16x16x128_f8f6f4 v[48:51], v[8:15], v[230:237], v[48:51], v30, v30 op_sel_hi:[0,0,0]
	v_mfma_scale_f32_16x16x128_f8f6f4 v[44:47], v[184:191], v[230:237], v[44:47], v30, v30 op_sel_hi:[0,0,0]
	v_mfma_scale_f32_16x16x128_f8f6f4 v[32:35], v[8:15], v[238:245], v[32:35], v30, v30 op_sel_hi:[0,0,0]
	v_mfma_scale_f32_16x16x128_f8f6f4 v[26:29], v[184:191], v[238:245], v[26:29], v30, v30 op_sel_hi:[0,0,0]
	s_setprio 0
	s_setprio 1
	v_mfma_scale_f32_16x16x128_f8f6f4 v[72:75], v[0:7], v[214:221], v[72:75], v30, v30 op_sel_hi:[0,0,0]
	v_mfma_scale_f32_16x16x128_f8f6f4 v[68:71], v[192:199], v[214:221], v[68:71], v30, v30 op_sel_hi:[0,0,0]
	v_mfma_scale_f32_16x16x128_f8f6f4 v[56:59], v[0:7], v[222:229], v[56:59], v30, v30 op_sel_hi:[0,0,0]
	v_mfma_scale_f32_16x16x128_f8f6f4 v[52:55], v[192:199], v[222:229], v[52:55], v30, v30 op_sel_hi:[0,0,0]
	v_mfma_scale_f32_16x16x128_f8f6f4 v[40:43], v[0:7], v[230:237], v[40:43], v30, v30 op_sel_hi:[0,0,0]
	v_mfma_scale_f32_16x16x128_f8f6f4 v[36:39], v[192:199], v[230:237], v[36:39], v30, v30 op_sel_hi:[0,0,0]
	v_mfma_scale_f32_16x16x128_f8f6f4 v[22:25], v[0:7], v[238:245], v[22:25], v30, v30 op_sel_hi:[0,0,0]
	v_mfma_scale_f32_16x16x128_f8f6f4 v[16:19], v[192:199], v[238:245], v[16:19], v30, v30 op_sel_hi:[0,0,0]
	s_setprio 0
	s_add_u32 s46, s46, 0x100
	s_addc_u32 s47, s47, 0
	s_add_u32 s75, s75, 0x100
	s_addc_u32 s76, s76, 0
	s_cmp_ge_i32 s77, s45
	s_mov_b32 s50, s77
	s_barrier
	s_cbranch_scc0 .LBB0_1728
	s_mov_b32 s75, 0x43800000
	s_mov_b32 s76, 0x9800
	s_mov_b32 s72, s82
	s_and_b64 vcc, exec, s[36:37]
	s_cbranch_vccz .LBB0_1731
